# v56 + all eight K-loops: the post-MFMA s_barrier is issued one MFMA before the end of each 32-MFMA block so the other half is released as the block drains
# baseline (speedup 1.0000x reference)
; #define PG8_STAGE(bufoff, gbase, voff) do { _Pragma("unroll") for (int _i = 0; _i < 2; ++_i) \
;         __builtin_amdgcn_global_load_lds((const unsigned*)((const char*)(gbase) + (voff)[_i]), (PG8_LAS unsigned*)(lds + (bufoff) + ldsw + _i * 8192), 16, 0, 0); } while (0)
; #define PG8_LDA(dst, b, h) do { _Pragma("unroll") for (int m = 0; m < 4; ++m) _Pragma("unroll") for (int k = 0; k < 2; ++k) dst[m][k] = *(const PG8_LAS bf16x8*)(lds + PG8_SA(b, h) + aoff + m * 2048 + k * 1024); } while (0)
; #define PG8_LDB(dst, b, h) do { _Pragma("unroll") for (int n = 0; n < 2; ++n) _Pragma("unroll") for (int k = 0; k < 2; ++k) dst[n][k] = *(const PG8_LAS bf16x8*)(lds + PG8_SB(b, h) + boff + n * 2048 + k * 1024); } while (0)
; #define PG8_MMA(ai, bj, At, Bt) do { __builtin_amdgcn_s_setprio(1); _Pragma("unroll") for (int m = 0; m < 4; ++m) _Pragma("unroll") for (int n = 0; n < 2; ++n) _Pragma("unroll") for (int k = 0; k < 2; ++k) \
;         acc[ai][bj][m][n] = __builtin_amdgcn_mfma_f32_16x16x32_bf16(Bt[n][k], At[m][k], acc[ai][bj][m][n], 0, 0, 0); __builtin_amdgcn_s_setprio(0); } while (0)
; #define PG8_WAIT_V(n) asm volatile("s_waitcnt vmcnt(" #n ")" ::: "memory")
; #define PG8_WAIT_L(n) asm volatile("s_waitcnt lgkmcnt(" #n ")" ::: "memory")
; template <class Epi, class Sched, bool ALIGN_EPI = false, bool SP2 = false>
; __device__ __forceinline__ void gemm_phase(PG8_LAS unsigned char* lds, const Gemm g, const Sched& S, const Epi& E) {
;     ...
;             const bool last = (t == nt - 2);
;             const char* a1 = cA + (size_t)(t + 1) * kstep;
;             const char* a2 = last ? nA : cA + (size_t)(t + 2) * kstep; const char* b2 = last ? nB : cB + (size_t)(t + 2) * kstep;
;             const char* a3 = a2 + kstep; const char* b3 = b2 + kstep;
;             if (last && has_next) S.a_ready(nxt);
;             if constexpr (SP2) {
;             PG8_LDB(B0, 0, 0); PG8_LDB(B1, 0, 1); PG8_SCHED; PG8_LDA(At, 0, 0); PG8_STAGE(PG8_SA(1, 1), a1 + hstepA, voffA);
;             PG8_WAIT_V(8); PG8_WAIT_L(0); PG8_BAR; PG8_MMA(0, 0, At, B0); PG8_MMA(0, 1, At, B1); PG8_BAR; PG8_SCHED;
;             PG8_LDA(At, 0, 1); PG8_STAGE(PG8_SB(0, 0), b2, voffB); PG8_STAGE(PG8_SB(0, 1), b2 + hstepB, voffB); PG8_STAGE(PG8_SA(0, 0), a2, voffA);
;             PG8_WAIT_V(8); PG8_WAIT_L(0); PG8_BAR; PG8_MMA(1, 0, At, B0); PG8_MMA(1, 1, At, B1); PG8_BAR; PG8_SCHED;
.LBB0_153:
	s_add_u32 s24, s22, 0xfffc0080
	s_addc_u32 s25, s23, -1
	s_add_i32 s54, 0, 0x10000
	s_cmp_eq_u32 s53, 12
	s_cselect_b32 s27, s15, s25
	s_cselect_b32 s26, s49, s24
	v_add_u32_e32 v144, s54, v147
	s_cselect_b32 s25, s13, s52
	s_cselect_b32 s24, s50, s51
	s_add_i32 s56, 0, 0x14000
	ds_read_b128 v[150:153], v144
	ds_read_b128 v[154:157], v144 offset:1024
	ds_read_b128 v[158:161], v144 offset:2048
	ds_read_b128 v[162:165], v144 offset:3072
	v_add_u32_e32 v144, s56, v147
	ds_read_b128 v[166:169], v144
	ds_read_b128 v[170:173], v144 offset:1024
	ds_read_b128 v[174:177], v144 offset:2048
	ds_read_b128 v[178:181], v144 offset:3072
	v_lshl_add_u64 v[144:145], s[22:23], 0, v[142:143]
	s_add_i32 m0, s41, 0xc000
	ds_read_b128 v[182:185], v149
	ds_read_b128 v[186:189], v149 offset:1024
	ds_read_b128 v[190:193], v149 offset:2048
	ds_read_b128 v[194:197], v149 offset:3072
	ds_read_b128 v[210:213], v149 offset:4096
	ds_read_b128 v[226:229], v149 offset:5120
	ds_read_b128 v[230:233], v149 offset:6144
	ds_read_b128 v[234:237], v149 offset:7168
	v_lshl_add_u64 v[244:245], v[240:241], 0, s[64:65]
	s_mov_b32 m0, s45
	s_nop 0
	global_load_lds_dwordx4 v[244:245], off
	v_lshl_add_u64 v[244:245], v[242:243], 0, s[64:65]
	s_mov_b32 m0, s46
	s_nop 0
	global_load_lds_dwordx4 v[244:245], off
	s_add_i32 m0, s41, 0xc000
	s_nop 0
	global_load_lds_dwordx4 v[144:145], off
	v_lshl_add_u64 v[144:145], s[22:23], 0, v[140:141]
	s_add_i32 m0, s41, 0xe000
	s_nop 0
	global_load_lds_dwordx4 v[144:145], off
	s_waitcnt vmcnt(8)
	s_waitcnt lgkmcnt(0)
	s_barrier
	s_setprio 1
	s_waitcnt lgkmcnt(0)
	v_mfma_f32_16x16x32_bf16 v[128:131], v[150:153], v[182:185], v[128:131]
	v_mfma_f32_16x16x32_bf16 v[120:123], v[158:161], v[182:185], v[120:123]
	v_mfma_f32_16x16x32_bf16 v[112:115], v[150:153], v[190:193], v[112:115]
	v_mfma_f32_16x16x32_bf16 v[104:107], v[158:161], v[190:193], v[104:107]
	v_mfma_f32_16x16x32_bf16 v[96:99], v[150:153], v[210:213], v[96:99]
	v_mfma_f32_16x16x32_bf16 v[88:91], v[158:161], v[210:213], v[88:91]
	v_mfma_f32_16x16x32_bf16 v[80:83], v[150:153], v[230:233], v[80:83]
	v_mfma_f32_16x16x32_bf16 v[72:75], v[158:161], v[230:233], v[72:75]
	v_mfma_f32_16x16x32_bf16 v[128:131], v[154:157], v[186:189], v[128:131]
	v_mfma_f32_16x16x32_bf16 v[120:123], v[162:165], v[186:189], v[120:123]
	v_mfma_f32_16x16x32_bf16 v[112:115], v[154:157], v[194:197], v[112:115]
	v_mfma_f32_16x16x32_bf16 v[104:107], v[162:165], v[194:197], v[104:107]
	v_mfma_f32_16x16x32_bf16 v[96:99], v[154:157], v[226:229], v[96:99]
	v_mfma_f32_16x16x32_bf16 v[88:91], v[162:165], v[226:229], v[88:91]
	v_mfma_f32_16x16x32_bf16 v[80:83], v[154:157], v[234:237], v[80:83]
	v_mfma_f32_16x16x32_bf16 v[72:75], v[162:165], v[234:237], v[72:75]
	s_setprio 0
	s_setprio 1
	v_mfma_f32_16x16x32_bf16 v[124:127], v[166:169], v[182:185], v[124:127]
	v_mfma_f32_16x16x32_bf16 v[116:119], v[174:177], v[182:185], v[116:119]
	v_mfma_f32_16x16x32_bf16 v[108:111], v[166:169], v[190:193], v[108:111]
	v_mfma_f32_16x16x32_bf16 v[100:103], v[174:177], v[190:193], v[100:103]
	v_mfma_f32_16x16x32_bf16 v[92:95], v[166:169], v[210:213], v[92:95]
	v_mfma_f32_16x16x32_bf16 v[84:87], v[174:177], v[210:213], v[84:87]
	v_mfma_f32_16x16x32_bf16 v[76:79], v[166:169], v[230:233], v[76:79]
	v_mfma_f32_16x16x32_bf16 v[68:71], v[174:177], v[230:233], v[68:71]
	v_mfma_f32_16x16x32_bf16 v[124:127], v[170:173], v[186:189], v[124:127]
	v_mfma_f32_16x16x32_bf16 v[116:119], v[178:181], v[186:189], v[116:119]
	v_mfma_f32_16x16x32_bf16 v[108:111], v[170:173], v[194:197], v[108:111]
	v_mfma_f32_16x16x32_bf16 v[100:103], v[178:181], v[194:197], v[100:103]
	v_mfma_f32_16x16x32_bf16 v[92:95], v[170:173], v[226:229], v[92:95]
	v_mfma_f32_16x16x32_bf16 v[84:87], v[178:181], v[226:229], v[84:87]
	v_mfma_f32_16x16x32_bf16 v[76:79], v[170:173], v[234:237], v[76:79]
	s_barrier
	v_mfma_f32_16x16x32_bf16 v[68:71], v[178:181], v[234:237], v[68:71]
	s_setprio 0
	s_add_i32 s54, s54, s39
	v_lshl_add_u64 v[144:145], s[24:25], 0, v[136:137]
	s_mov_b32 m0, s54
	ds_read_b128 v[182:185], v149 offset:16384
	ds_read_b128 v[186:189], v149 offset:17408
	ds_read_b128 v[190:193], v149 offset:18432
	ds_read_b128 v[194:197], v149 offset:19456
	ds_read_b128 v[210:213], v149 offset:20480
	ds_read_b128 v[226:229], v149 offset:21504
	ds_read_b128 v[230:233], v149 offset:22528
	ds_read_b128 v[234:237], v149 offset:23552
	global_load_lds_dwordx4 v[144:145], off
	s_add_i32 m0, s54, 0x2000
	s_add_u32 s54, s24, 0x40000
	v_lshl_add_u64 v[238:239], s[24:25], 0, v[132:133]
	s_addc_u32 s55, s25, 0
	s_add_i32 s56, s56, s39
	global_load_lds_dwordx4 v[238:239], off
	v_lshl_add_u64 v[240:241], s[54:55], 0, v[136:137]
	s_mov_b32 m0, s56
	v_lshl_add_u64 v[242:243], s[26:27], 0, v[134:135]
	global_load_lds_dwordx4 v[240:241], off
	v_lshl_add_u64 v[240:241], s[54:55], 0, v[132:133]
	s_add_i32 m0, s56, 0x2000
	s_nop 0
	global_load_lds_dwordx4 v[240:241], off
	v_lshl_add_u64 v[240:241], s[26:27], 0, v[138:139]
	s_waitcnt vmcnt(6)
	s_waitcnt lgkmcnt(0)
	s_barrier
; #define PG8_STAGE(bufoff, gbase, voff) do { _Pragma("unroll") for (int _i = 0; _i < 2; ++_i) \
;         __builtin_amdgcn_global_load_lds((const unsigned*)((const char*)(gbase) + (voff)[_i]), (PG8_LAS unsigned*)(lds + (bufoff) + ldsw + _i * 8192), 16, 0, 0); } while (0)
; #define PG8_LDA(dst, b, h) do { _Pragma("unroll") for (int m = 0; m < 4; ++m) _Pragma("unroll") for (int k = 0; k < 2; ++k) dst[m][k] = *(const PG8_LAS bf16x8*)(lds + PG8_SA(b, h) + aoff + m * 2048 + k * 1024); } while (0)
; #define PG8_LDB(dst, b, h) do { _Pragma("unroll") for (int n = 0; n < 2; ++n) _Pragma("unroll") for (int k = 0; k < 2; ++k) dst[n][k] = *(const PG8_LAS bf16x8*)(lds + PG8_SB(b, h) + boff + n * 2048 + k * 1024); } while (0)
; #define PG8_MMA(ai, bj, At, Bt) do { __builtin_amdgcn_s_setprio(1); _Pragma("unroll") for (int m = 0; m < 4; ++m) _Pragma("unroll") for (int n = 0; n < 2; ++n) _Pragma("unroll") for (int k = 0; k < 2; ++k) \
;         acc[ai][bj][m][n] = __builtin_amdgcn_mfma_f32_16x16x32_bf16(Bt[n][k], At[m][k], acc[ai][bj][m][n], 0, 0, 0); __builtin_amdgcn_s_setprio(0); } while (0)
; #define PG8_WAIT_V(n) asm volatile("s_waitcnt vmcnt(" #n ")" ::: "memory")
; #define PG8_WAIT_L(n) asm volatile("s_waitcnt lgkmcnt(" #n ")" ::: "memory")
; #define PG8_BAR __builtin_amdgcn_s_barrier()
; #define PG8_SCHED __builtin_amdgcn_sched_barrier(0)
; template <class Epi, class Sched, bool ALIGN_EPI = false, bool SP2 = false>
; __device__ __forceinline__ void gemm_phase(PG8_LAS unsigned char* lds, const Gemm g, const Sched& S, const Epi& E) {
;     ...
;             PG8_WAIT_V(8); PG8_WAIT_L(0); PG8_BAR; PG8_MMA(1, 0, At, B0); PG8_MMA(1, 1, At, B1); PG8_BAR; PG8_SCHED;
;             PG8_LDB(B0, 1, 0); PG8_LDB(B1, 1, 1); PG8_SCHED; PG8_LDA(At, 1, 0); PG8_STAGE(PG8_SA(0, 1), a2 + hstepA, voffA);
;             PG8_WAIT_V(8); PG8_WAIT_L(0); PG8_BAR; PG8_MMA(0, 0, At, B0); PG8_MMA(0, 1, At, B1); PG8_BAR; PG8_SCHED;
	s_setprio 1
	s_waitcnt lgkmcnt(0)
	v_mfma_f32_16x16x32_bf16 v[64:67], v[150:153], v[182:185], v[64:67]
	v_mfma_f32_16x16x32_bf16 v[56:59], v[158:161], v[182:185], v[56:59]
	v_mfma_f32_16x16x32_bf16 v[48:51], v[150:153], v[190:193], v[48:51]
	v_mfma_f32_16x16x32_bf16 v[40:43], v[158:161], v[190:193], v[40:43]
	v_mfma_f32_16x16x32_bf16 v[32:35], v[150:153], v[210:213], v[32:35]
	v_mfma_f32_16x16x32_bf16 v[24:27], v[158:161], v[210:213], v[24:27]
	v_mfma_f32_16x16x32_bf16 v[16:19], v[150:153], v[230:233], v[16:19]
	v_mfma_f32_16x16x32_bf16 v[8:11], v[158:161], v[230:233], v[8:11]
	v_mfma_f32_16x16x32_bf16 v[64:67], v[154:157], v[186:189], v[64:67]
	v_mfma_f32_16x16x32_bf16 v[56:59], v[162:165], v[186:189], v[56:59]
	v_mfma_f32_16x16x32_bf16 v[48:51], v[154:157], v[194:197], v[48:51]
	v_mfma_f32_16x16x32_bf16 v[40:43], v[162:165], v[194:197], v[40:43]
	v_mfma_f32_16x16x32_bf16 v[32:35], v[154:157], v[226:229], v[32:35]
	v_mfma_f32_16x16x32_bf16 v[24:27], v[162:165], v[226:229], v[24:27]
	v_mfma_f32_16x16x32_bf16 v[16:19], v[154:157], v[234:237], v[16:19]
	v_mfma_f32_16x16x32_bf16 v[8:11], v[162:165], v[234:237], v[8:11]
	s_setprio 0
	s_setprio 1
	v_mfma_f32_16x16x32_bf16 v[60:63], v[166:169], v[182:185], v[60:63]
	v_mfma_f32_16x16x32_bf16 v[52:55], v[174:177], v[182:185], v[52:55]
	v_mfma_f32_16x16x32_bf16 v[44:47], v[166:169], v[190:193], v[44:47]
	v_mfma_f32_16x16x32_bf16 v[36:39], v[174:177], v[190:193], v[36:39]
	v_mfma_f32_16x16x32_bf16 v[28:31], v[166:169], v[210:213], v[28:31]
	v_mfma_f32_16x16x32_bf16 v[20:23], v[174:177], v[210:213], v[20:23]
	v_mfma_f32_16x16x32_bf16 v[12:15], v[166:169], v[230:233], v[12:15]
	v_mfma_f32_16x16x32_bf16 v[4:7], v[174:177], v[230:233], v[4:7]
	v_mfma_f32_16x16x32_bf16 v[60:63], v[170:173], v[186:189], v[60:63]
	v_mfma_f32_16x16x32_bf16 v[52:55], v[178:181], v[186:189], v[52:55]
	v_mfma_f32_16x16x32_bf16 v[44:47], v[170:173], v[194:197], v[44:47]
	v_mfma_f32_16x16x32_bf16 v[36:39], v[178:181], v[194:197], v[36:39]
	v_mfma_f32_16x16x32_bf16 v[28:31], v[170:173], v[226:229], v[28:31]
	v_mfma_f32_16x16x32_bf16 v[20:23], v[178:181], v[226:229], v[20:23]
	v_mfma_f32_16x16x32_bf16 v[12:15], v[170:173], v[234:237], v[12:15]
	s_barrier
	v_mfma_f32_16x16x32_bf16 v[4:7], v[178:181], v[234:237], v[4:7]
	s_setprio 0
	s_add_i32 s54, 0, 0x18000
	s_add_i32 s55, 0, 0x1c000
	v_add_u32_e32 v162, s54, v147
	v_add_u32_e32 v178, s55, v147
	ds_read_b128 v[150:153], v162
	ds_read_b128 v[154:157], v162 offset:1024
	ds_read_b128 v[158:161], v162 offset:2048
	ds_read_b128 v[162:165], v162 offset:3072
	ds_read_b128 v[166:169], v178
	ds_read_b128 v[170:173], v178 offset:1024
	ds_read_b128 v[174:177], v178 offset:2048
	ds_read_b128 v[178:181], v178 offset:3072
	s_add_u32 s26, s26, 0x40000
	s_addc_u32 s27, s27, 0
	s_mov_b32 m0, s43
	v_lshl_add_u64 v[244:245], s[26:27], 0, v[138:139]
	ds_read_b128 v[182:185], v149 offset:32768
	ds_read_b128 v[186:189], v149 offset:33792
	ds_read_b128 v[190:193], v149 offset:34816
	ds_read_b128 v[194:197], v149 offset:35840
	ds_read_b128 v[210:213], v149 offset:36864
	ds_read_b128 v[226:229], v149 offset:37888
	ds_read_b128 v[230:233], v149 offset:38912
	ds_read_b128 v[234:237], v149 offset:39936
	s_mov_b32 m0, s41
	s_nop 0
	global_load_lds_dwordx4 v[240:241], off
	s_mov_b32 m0, s42
	s_nop 0
	global_load_lds_dwordx4 v[242:243], off
	s_mov_b32 m0, s43
	s_nop 0
	global_load_lds_dwordx4 v[244:245], off
	v_lshl_add_u64 v[244:245], s[26:27], 0, v[134:135]
	s_mov_b32 m0, s44
	s_nop 0
	global_load_lds_dwordx4 v[244:245], off
	s_waitcnt vmcnt(8)
	s_waitcnt lgkmcnt(0)
	s_barrier
; #define PG8_STAGE(bufoff, gbase, voff) do { _Pragma("unroll") for (int _i = 0; _i < 2; ++_i) \
;         __builtin_amdgcn_global_load_lds((const unsigned*)((const char*)(gbase) + (voff)[_i]), (PG8_LAS unsigned*)(lds + (bufoff) + ldsw + _i * 8192), 16, 0, 0); } while (0)
; #define PG8_LDA(dst, b, h) do { _Pragma("unroll") for (int m = 0; m < 4; ++m) _Pragma("unroll") for (int k = 0; k < 2; ++k) dst[m][k] = *(const PG8_LAS bf16x8*)(lds + PG8_SA(b, h) + aoff + m * 2048 + k * 1024); } while (0)
; #define PG8_LDB(dst, b, h) do { _Pragma("unroll") for (int n = 0; n < 2; ++n) _Pragma("unroll") for (int k = 0; k < 2; ++k) dst[n][k] = *(const PG8_LAS bf16x8*)(lds + PG8_SB(b, h) + boff + n * 2048 + k * 1024); } while (0)
; #define PG8_MMA(ai, bj, At, Bt) do { __builtin_amdgcn_s_setprio(1); _Pragma("unroll") for (int m = 0; m < 4; ++m) _Pragma("unroll") for (int n = 0; n < 2; ++n) _Pragma("unroll") for (int k = 0; k < 2; ++k) \
;         acc[ai][bj][m][n] = __builtin_amdgcn_mfma_f32_16x16x32_bf16(Bt[n][k], At[m][k], acc[ai][bj][m][n], 0, 0, 0); __builtin_amdgcn_s_setprio(0); } while (0)
; #define PG8_WAIT_V(n) asm volatile("s_waitcnt vmcnt(" #n ")" ::: "memory")
; #define PG8_WAIT_L(n) asm volatile("s_waitcnt lgkmcnt(" #n ")" ::: "memory")
; #define PG8_BAR __builtin_amdgcn_s_barrier()
; #define PG8_SCHED __builtin_amdgcn_sched_barrier(0)
; template <class Epi, class Sched, bool ALIGN_EPI = false, bool SP2 = false>
; __device__ __forceinline__ void gemm_phase(PG8_LAS unsigned char* lds, const Gemm g, const Sched& S, const Epi& E) {
;     ...
;             PG8_LDB(B0, 1, 0); PG8_LDB(B1, 1, 1); PG8_SCHED; PG8_LDA(At, 1, 0); PG8_STAGE(PG8_SA(0, 1), a2 + hstepA, voffA);
;             PG8_WAIT_V(8); PG8_WAIT_L(0); PG8_BAR; PG8_MMA(0, 0, At, B0); PG8_MMA(0, 1, At, B1); PG8_BAR; PG8_SCHED;
;             PG8_LDA(At, 1, 1); PG8_STAGE(PG8_SB(1, 0), b3, voffB); PG8_STAGE(PG8_SB(1, 1), b3 + hstepB, voffB); PG8_STAGE(PG8_SA(1, 0), a3, voffA);
;             PG8_WAIT_V(8); PG8_WAIT_L(0); PG8_BAR; PG8_MMA(1, 0, At, B0); PG8_MMA(1, 1, At, B1); PG8_BAR; PG8_SCHED;
	s_setprio 1
	s_waitcnt lgkmcnt(0)
	v_mfma_f32_16x16x32_bf16 v[128:131], v[150:153], v[182:185], v[128:131]
	v_mfma_f32_16x16x32_bf16 v[120:123], v[158:161], v[182:185], v[120:123]
	v_mfma_f32_16x16x32_bf16 v[112:115], v[150:153], v[190:193], v[112:115]
	v_mfma_f32_16x16x32_bf16 v[104:107], v[158:161], v[190:193], v[104:107]
	v_mfma_f32_16x16x32_bf16 v[96:99], v[150:153], v[210:213], v[96:99]
	v_mfma_f32_16x16x32_bf16 v[88:91], v[158:161], v[210:213], v[88:91]
	v_mfma_f32_16x16x32_bf16 v[80:83], v[150:153], v[230:233], v[80:83]
	v_mfma_f32_16x16x32_bf16 v[72:75], v[158:161], v[230:233], v[72:75]
	v_mfma_f32_16x16x32_bf16 v[128:131], v[154:157], v[186:189], v[128:131]
	v_mfma_f32_16x16x32_bf16 v[120:123], v[162:165], v[186:189], v[120:123]
	v_mfma_f32_16x16x32_bf16 v[112:115], v[154:157], v[194:197], v[112:115]
	v_mfma_f32_16x16x32_bf16 v[104:107], v[162:165], v[194:197], v[104:107]
	v_mfma_f32_16x16x32_bf16 v[96:99], v[154:157], v[226:229], v[96:99]
	v_mfma_f32_16x16x32_bf16 v[88:91], v[162:165], v[226:229], v[88:91]
	v_mfma_f32_16x16x32_bf16 v[80:83], v[154:157], v[234:237], v[80:83]
	v_mfma_f32_16x16x32_bf16 v[72:75], v[162:165], v[234:237], v[72:75]
	s_setprio 0
	s_setprio 1
	v_mfma_f32_16x16x32_bf16 v[124:127], v[166:169], v[182:185], v[124:127]
	v_mfma_f32_16x16x32_bf16 v[116:119], v[174:177], v[182:185], v[116:119]
	v_mfma_f32_16x16x32_bf16 v[108:111], v[166:169], v[190:193], v[108:111]
	v_mfma_f32_16x16x32_bf16 v[100:103], v[174:177], v[190:193], v[100:103]
	v_mfma_f32_16x16x32_bf16 v[92:95], v[166:169], v[210:213], v[92:95]
	v_mfma_f32_16x16x32_bf16 v[84:87], v[174:177], v[210:213], v[84:87]
	v_mfma_f32_16x16x32_bf16 v[76:79], v[166:169], v[230:233], v[76:79]
	v_mfma_f32_16x16x32_bf16 v[68:71], v[174:177], v[230:233], v[68:71]
	v_mfma_f32_16x16x32_bf16 v[124:127], v[170:173], v[186:189], v[124:127]
	v_mfma_f32_16x16x32_bf16 v[116:119], v[178:181], v[186:189], v[116:119]
	v_mfma_f32_16x16x32_bf16 v[108:111], v[170:173], v[194:197], v[108:111]
	v_mfma_f32_16x16x32_bf16 v[100:103], v[178:181], v[194:197], v[100:103]
	v_mfma_f32_16x16x32_bf16 v[92:95], v[170:173], v[226:229], v[92:95]
	v_mfma_f32_16x16x32_bf16 v[84:87], v[178:181], v[226:229], v[84:87]
	v_mfma_f32_16x16x32_bf16 v[76:79], v[170:173], v[234:237], v[76:79]
	s_barrier
	v_mfma_f32_16x16x32_bf16 v[68:71], v[178:181], v[234:237], v[68:71]
	s_setprio 0
	s_add_i32 s26, s54, s39
	v_lshl_add_u64 v[144:145], v[144:145], 0, s[64:65]
	s_mov_b32 m0, s26
	ds_read_b128 v[182:185], v149 offset:49152
	ds_read_b128 v[186:189], v149 offset:50176
	ds_read_b128 v[190:193], v149 offset:51200
	ds_read_b128 v[194:197], v149 offset:52224
	ds_read_b128 v[210:213], v149 offset:53248
	ds_read_b128 v[226:229], v149 offset:54272
	ds_read_b128 v[230:233], v149 offset:55296
	ds_read_b128 v[234:237], v149 offset:56320
	global_load_lds_dwordx4 v[144:145], off
	s_add_i32 m0, s26, 0x2000
	s_add_u32 s24, s24, 0x40080
	v_lshl_add_u64 v[144:145], v[238:239], 0, s[64:65]
	s_addc_u32 s25, s25, 0
	s_add_i32 s26, s55, s39
	global_load_lds_dwordx4 v[144:145], off
	v_lshl_add_u64 v[144:145], s[24:25], 0, v[136:137]
	s_mov_b32 m0, s26
	s_nop 0
	global_load_lds_dwordx4 v[144:145], off
	v_lshl_add_u64 v[144:145], s[24:25], 0, v[132:133]
	s_add_i32 m0, s26, 0x2000
	s_nop 0
	global_load_lds_dwordx4 v[144:145], off
	s_waitcnt vmcnt(6)
	s_waitcnt lgkmcnt(0)
	s_barrier
	s_setprio 1
	s_waitcnt lgkmcnt(0)
	v_mfma_f32_16x16x32_bf16 v[64:67], v[150:153], v[182:185], v[64:67]
	v_mfma_f32_16x16x32_bf16 v[56:59], v[158:161], v[182:185], v[56:59]
	v_mfma_f32_16x16x32_bf16 v[48:51], v[150:153], v[190:193], v[48:51]
	v_mfma_f32_16x16x32_bf16 v[40:43], v[158:161], v[190:193], v[40:43]
	v_mfma_f32_16x16x32_bf16 v[32:35], v[150:153], v[210:213], v[32:35]
	v_mfma_f32_16x16x32_bf16 v[24:27], v[158:161], v[210:213], v[24:27]
	v_mfma_f32_16x16x32_bf16 v[16:19], v[150:153], v[230:233], v[16:19]
	v_mfma_f32_16x16x32_bf16 v[8:11], v[158:161], v[230:233], v[8:11]
	v_mfma_f32_16x16x32_bf16 v[64:67], v[154:157], v[186:189], v[64:67]
	v_mfma_f32_16x16x32_bf16 v[56:59], v[162:165], v[186:189], v[56:59]
	v_mfma_f32_16x16x32_bf16 v[48:51], v[154:157], v[194:197], v[48:51]
	v_mfma_f32_16x16x32_bf16 v[40:43], v[162:165], v[194:197], v[40:43]
	v_mfma_f32_16x16x32_bf16 v[32:35], v[154:157], v[226:229], v[32:35]
	v_mfma_f32_16x16x32_bf16 v[24:27], v[162:165], v[226:229], v[24:27]
	v_mfma_f32_16x16x32_bf16 v[16:19], v[154:157], v[234:237], v[16:19]
	v_mfma_f32_16x16x32_bf16 v[8:11], v[162:165], v[234:237], v[8:11]
	s_setprio 0
	s_setprio 1
	v_mfma_f32_16x16x32_bf16 v[60:63], v[166:169], v[182:185], v[60:63]
	v_mfma_f32_16x16x32_bf16 v[52:55], v[174:177], v[182:185], v[52:55]
	v_mfma_f32_16x16x32_bf16 v[44:47], v[166:169], v[190:193], v[44:47]
	v_mfma_f32_16x16x32_bf16 v[36:39], v[174:177], v[190:193], v[36:39]
	v_mfma_f32_16x16x32_bf16 v[28:31], v[166:169], v[210:213], v[28:31]
	v_mfma_f32_16x16x32_bf16 v[20:23], v[174:177], v[210:213], v[20:23]
	v_mfma_f32_16x16x32_bf16 v[12:15], v[166:169], v[230:233], v[12:15]
	v_mfma_f32_16x16x32_bf16 v[4:7], v[174:177], v[230:233], v[4:7]
	v_mfma_f32_16x16x32_bf16 v[60:63], v[170:173], v[186:189], v[60:63]
	v_mfma_f32_16x16x32_bf16 v[52:55], v[178:181], v[186:189], v[52:55]
	v_mfma_f32_16x16x32_bf16 v[44:47], v[170:173], v[194:197], v[44:47]
	v_mfma_f32_16x16x32_bf16 v[36:39], v[178:181], v[194:197], v[36:39]
	v_mfma_f32_16x16x32_bf16 v[28:31], v[170:173], v[226:229], v[28:31]
	v_mfma_f32_16x16x32_bf16 v[20:23], v[178:181], v[226:229], v[20:23]
	v_mfma_f32_16x16x32_bf16 v[12:15], v[170:173], v[234:237], v[12:15]
	s_barrier
	v_mfma_f32_16x16x32_bf16 v[4:7], v[178:181], v[234:237], v[4:7]
	s_setprio 0
	s_add_i32 s53, s53, 2
	s_add_u32 s51, s51, 0x100
	s_addc_u32 s52, s52, 0
	s_add_u32 s22, s22, 0x100
	s_addc_u32 s23, s23, 0
	s_cmp_gt_u32 s53, 13
	s_cbranch_scc0 .LBB0_153

; #define PG8_STAGE(bufoff, gbase, voff) do { _Pragma("unroll") for (int _i = 0; _i < 2; ++_i) \
;         __builtin_amdgcn_global_load_lds((const unsigned*)((const char*)(gbase) + (voff)[_i]), (PG8_LAS unsigned*)(lds + (bufoff) + ldsw + _i * 8192), 16, 0, 0); } while (0)
; #define PG8_LDA(dst, b, h) do { _Pragma("unroll") for (int m = 0; m < 4; ++m) _Pragma("unroll") for (int k = 0; k < 2; ++k) dst[m][k] = *(const PG8_LAS bf16x8*)(lds + PG8_SA(b, h) + aoff + m * 2048 + k * 1024); } while (0)
; #define PG8_LDB(dst, b, h) do { _Pragma("unroll") for (int n = 0; n < 2; ++n) _Pragma("unroll") for (int k = 0; k < 2; ++k) dst[n][k] = *(const PG8_LAS bf16x8*)(lds + PG8_SB(b, h) + boff + n * 2048 + k * 1024); } while (0)
; #define PG8_MMA(ai, bj, At, Bt) do { __builtin_amdgcn_s_setprio(1); _Pragma("unroll") for (int m = 0; m < 4; ++m) _Pragma("unroll") for (int n = 0; n < 2; ++n) _Pragma("unroll") for (int k = 0; k < 2; ++k) \
;         acc[ai][bj][m][n] = __builtin_amdgcn_mfma_f32_16x16x32_bf16(Bt[n][k], At[m][k], acc[ai][bj][m][n], 0, 0, 0); __builtin_amdgcn_s_setprio(0); } while (0)
; #define PG8_WAIT_V(n) asm volatile("s_waitcnt vmcnt(" #n ")" ::: "memory")
; #define PG8_WAIT_L(n) asm volatile("s_waitcnt lgkmcnt(" #n ")" ::: "memory")
; template <class Epi, class Sched, bool ALIGN_EPI = false, bool SP2 = false>
; __device__ __forceinline__ void gemm_phase(PG8_LAS unsigned char* lds, const Gemm g, const Sched& S, const Epi& E) {
;     ...
;             const bool last = (t == nt - 2);
;             const char* a1 = cA + (size_t)(t + 1) * kstep;
;             const char* a2 = last ? nA : cA + (size_t)(t + 2) * kstep; const char* b2 = last ? nB : cB + (size_t)(t + 2) * kstep;
;             const char* a3 = a2 + kstep; const char* b3 = b2 + kstep;
;             if (last && has_next) S.a_ready(nxt);
;             if constexpr (SP2) {
;             PG8_LDB(B0, 0, 0); PG8_LDB(B1, 0, 1); PG8_SCHED; PG8_LDA(At, 0, 0); PG8_STAGE(PG8_SA(1, 1), a1 + hstepA, voffA);
;             PG8_WAIT_V(8); PG8_WAIT_L(0); PG8_BAR; PG8_MMA(0, 0, At, B0); PG8_MMA(0, 1, At, B1); PG8_BAR; PG8_SCHED;
;             PG8_LDA(At, 0, 1); PG8_STAGE(PG8_SB(0, 0), b2, voffB); PG8_STAGE(PG8_SB(0, 1), b2 + hstepB, voffB); PG8_STAGE(PG8_SA(0, 0), a2, voffA);
;             PG8_WAIT_V(8); PG8_WAIT_L(0); PG8_BAR; PG8_MMA(1, 0, At, B0); PG8_MMA(1, 1, At, B1); PG8_BAR; PG8_SCHED;
.LBB0_669:
	s_add_u32 s16, s14, 0x100
	s_addc_u32 s17, s15, 0
	s_add_i32 s47, 0, 0x10000
	s_cmp_eq_u32 s46, 40
	s_cselect_b32 s21, s5, s17
	s_cselect_b32 s20, s4, s16
	v_add_u32_e32 v144, s47, v146
	s_cselect_b32 s19, s13, s45
	s_cselect_b32 s18, s12, s44
	s_add_i32 s48, 0, 0x14000
	ds_read_b128 v[150:153], v144
	ds_read_b128 v[154:157], v144 offset:1024
	ds_read_b128 v[158:161], v144 offset:2048
	ds_read_b128 v[162:165], v144 offset:3072
	v_add_u32_e32 v144, s48, v146
	ds_read_b128 v[166:169], v144
	ds_read_b128 v[170:173], v144 offset:1024
	ds_read_b128 v[174:177], v144 offset:2048
	ds_read_b128 v[178:181], v144 offset:3072
	v_lshl_add_u64 v[144:145], s[14:15], 0, v[142:143]
	s_add_i32 m0, s28, 0xc000
	ds_read_b128 v[182:185], v148
	ds_read_b128 v[186:189], v148 offset:1024
	ds_read_b128 v[190:193], v148 offset:2048
	ds_read_b128 v[194:197], v148 offset:3072
	ds_read_b128 v[210:213], v148 offset:4096
	ds_read_b128 v[226:229], v148 offset:5120
	ds_read_b128 v[230:233], v148 offset:6144
	ds_read_b128 v[234:237], v148 offset:7168
	v_lshl_add_u64 v[244:245], v[240:241], 0, s[64:65]
	s_mov_b32 m0, s33
	s_nop 0
	global_load_lds_dwordx4 v[244:245], off
	v_lshl_add_u64 v[244:245], v[242:243], 0, s[64:65]
	s_mov_b32 m0, s34
	s_nop 0
	global_load_lds_dwordx4 v[244:245], off
	s_add_i32 m0, s28, 0xc000
	s_nop 0
	global_load_lds_dwordx4 v[144:145], off
	v_lshl_add_u64 v[144:145], s[14:15], 0, v[140:141]
	s_add_i32 m0, s28, 0xe000
	s_nop 0
	global_load_lds_dwordx4 v[144:145], off
	s_waitcnt vmcnt(8)
	s_waitcnt lgkmcnt(0)
	s_barrier
	s_setprio 1
	s_waitcnt lgkmcnt(0)
	v_mfma_f32_16x16x32_bf16 v[128:131], v[150:153], v[182:185], v[128:131]
	v_mfma_f32_16x16x32_bf16 v[124:127], v[158:161], v[182:185], v[124:127]
	v_mfma_f32_16x16x32_bf16 v[120:123], v[150:153], v[190:193], v[120:123]
	v_mfma_f32_16x16x32_bf16 v[112:115], v[158:161], v[190:193], v[112:115]
	v_mfma_f32_16x16x32_bf16 v[104:107], v[150:153], v[210:213], v[104:107]
	v_mfma_f32_16x16x32_bf16 v[96:99], v[158:161], v[210:213], v[96:99]
	v_mfma_f32_16x16x32_bf16 v[88:91], v[150:153], v[230:233], v[88:91]
	v_mfma_f32_16x16x32_bf16 v[80:83], v[158:161], v[230:233], v[80:83]
	v_mfma_f32_16x16x32_bf16 v[128:131], v[154:157], v[186:189], v[128:131]
	v_mfma_f32_16x16x32_bf16 v[124:127], v[162:165], v[186:189], v[124:127]
	v_mfma_f32_16x16x32_bf16 v[120:123], v[154:157], v[194:197], v[120:123]
	v_mfma_f32_16x16x32_bf16 v[112:115], v[162:165], v[194:197], v[112:115]
	v_mfma_f32_16x16x32_bf16 v[104:107], v[154:157], v[226:229], v[104:107]
	v_mfma_f32_16x16x32_bf16 v[96:99], v[162:165], v[226:229], v[96:99]
	v_mfma_f32_16x16x32_bf16 v[88:91], v[154:157], v[234:237], v[88:91]
	v_mfma_f32_16x16x32_bf16 v[80:83], v[162:165], v[234:237], v[80:83]
	s_setprio 0
	s_setprio 1
	v_mfma_f32_16x16x32_bf16 v[116:119], v[166:169], v[182:185], v[116:119]
	v_mfma_f32_16x16x32_bf16 v[108:111], v[174:177], v[182:185], v[108:111]
	v_mfma_f32_16x16x32_bf16 v[100:103], v[166:169], v[190:193], v[100:103]
	v_mfma_f32_16x16x32_bf16 v[92:95], v[174:177], v[190:193], v[92:95]
	v_mfma_f32_16x16x32_bf16 v[84:87], v[166:169], v[210:213], v[84:87]
	v_mfma_f32_16x16x32_bf16 v[76:79], v[174:177], v[210:213], v[76:79]
	v_mfma_f32_16x16x32_bf16 v[72:75], v[166:169], v[230:233], v[72:75]
	v_mfma_f32_16x16x32_bf16 v[68:71], v[174:177], v[230:233], v[68:71]
	v_mfma_f32_16x16x32_bf16 v[116:119], v[170:173], v[186:189], v[116:119]
	v_mfma_f32_16x16x32_bf16 v[108:111], v[178:181], v[186:189], v[108:111]
	v_mfma_f32_16x16x32_bf16 v[100:103], v[170:173], v[194:197], v[100:103]
	v_mfma_f32_16x16x32_bf16 v[92:95], v[178:181], v[194:197], v[92:95]
	v_mfma_f32_16x16x32_bf16 v[84:87], v[170:173], v[226:229], v[84:87]
	v_mfma_f32_16x16x32_bf16 v[76:79], v[178:181], v[226:229], v[76:79]
	v_mfma_f32_16x16x32_bf16 v[72:75], v[170:173], v[234:237], v[72:75]
	s_barrier
	v_mfma_f32_16x16x32_bf16 v[68:71], v[178:181], v[234:237], v[68:71]
	s_setprio 0
	s_add_i32 s14, s47, s27
	v_lshl_add_u64 v[144:145], s[18:19], 0, v[134:135]
	s_mov_b32 m0, s14
	ds_read_b128 v[182:185], v148 offset:16384
	ds_read_b128 v[186:189], v148 offset:17408
	ds_read_b128 v[190:193], v148 offset:18432
	ds_read_b128 v[194:197], v148 offset:19456
	ds_read_b128 v[210:213], v148 offset:20480
	ds_read_b128 v[226:229], v148 offset:21504
	ds_read_b128 v[230:233], v148 offset:22528
	ds_read_b128 v[234:237], v148 offset:23552
	global_load_lds_dwordx4 v[144:145], off
	s_add_i32 m0, s14, 0x2000
	s_add_u32 s14, s18, 0xb0000
	v_lshl_add_u64 v[238:239], s[18:19], 0, v[138:139]
	s_addc_u32 s15, s19, 0
	s_add_i32 s47, s48, s27
	global_load_lds_dwordx4 v[238:239], off
	v_lshl_add_u64 v[240:241], s[14:15], 0, v[134:135]
	s_mov_b32 m0, s47
	v_lshl_add_u64 v[242:243], s[20:21], 0, v[136:137]
	global_load_lds_dwordx4 v[240:241], off
	v_lshl_add_u64 v[240:241], s[14:15], 0, v[138:139]
	s_add_i32 m0, s47, 0x2000
	s_nop 0
	global_load_lds_dwordx4 v[240:241], off
	v_lshl_add_u64 v[240:241], s[20:21], 0, v[132:133]
	s_waitcnt vmcnt(6)
	s_waitcnt lgkmcnt(0)
	s_barrier
; #define PG8_STAGE(bufoff, gbase, voff) do { _Pragma("unroll") for (int _i = 0; _i < 2; ++_i) \
;         __builtin_amdgcn_global_load_lds((const unsigned*)((const char*)(gbase) + (voff)[_i]), (PG8_LAS unsigned*)(lds + (bufoff) + ldsw + _i * 8192), 16, 0, 0); } while (0)
; #define PG8_LDA(dst, b, h) do { _Pragma("unroll") for (int m = 0; m < 4; ++m) _Pragma("unroll") for (int k = 0; k < 2; ++k) dst[m][k] = *(const PG8_LAS bf16x8*)(lds + PG8_SA(b, h) + aoff + m * 2048 + k * 1024); } while (0)
; #define PG8_LDB(dst, b, h) do { _Pragma("unroll") for (int n = 0; n < 2; ++n) _Pragma("unroll") for (int k = 0; k < 2; ++k) dst[n][k] = *(const PG8_LAS bf16x8*)(lds + PG8_SB(b, h) + boff + n * 2048 + k * 1024); } while (0)
; #define PG8_MMA(ai, bj, At, Bt) do { __builtin_amdgcn_s_setprio(1); _Pragma("unroll") for (int m = 0; m < 4; ++m) _Pragma("unroll") for (int n = 0; n < 2; ++n) _Pragma("unroll") for (int k = 0; k < 2; ++k) \
;         acc[ai][bj][m][n] = __builtin_amdgcn_mfma_f32_16x16x32_bf16(Bt[n][k], At[m][k], acc[ai][bj][m][n], 0, 0, 0); __builtin_amdgcn_s_setprio(0); } while (0)
; #define PG8_WAIT_V(n) asm volatile("s_waitcnt vmcnt(" #n ")" ::: "memory")
; #define PG8_WAIT_L(n) asm volatile("s_waitcnt lgkmcnt(" #n ")" ::: "memory")
; #define PG8_BAR __builtin_amdgcn_s_barrier()
; #define PG8_SCHED __builtin_amdgcn_sched_barrier(0)
; template <class Epi, class Sched, bool ALIGN_EPI = false, bool SP2 = false>
; __device__ __forceinline__ void gemm_phase(PG8_LAS unsigned char* lds, const Gemm g, const Sched& S, const Epi& E) {
;     ...
;             PG8_WAIT_V(8); PG8_WAIT_L(0); PG8_BAR; PG8_MMA(1, 0, At, B0); PG8_MMA(1, 1, At, B1); PG8_BAR; PG8_SCHED;
;             PG8_LDB(B0, 1, 0); PG8_LDB(B1, 1, 1); PG8_SCHED; PG8_LDA(At, 1, 0); PG8_STAGE(PG8_SA(0, 1), a2 + hstepA, voffA);
;             PG8_WAIT_V(8); PG8_WAIT_L(0); PG8_BAR; PG8_MMA(0, 0, At, B0); PG8_MMA(0, 1, At, B1); PG8_BAR; PG8_SCHED;
	s_setprio 1
	s_waitcnt lgkmcnt(0)
	v_mfma_f32_16x16x32_bf16 v[64:67], v[150:153], v[182:185], v[64:67]
	v_mfma_f32_16x16x32_bf16 v[60:63], v[158:161], v[182:185], v[60:63]
	v_mfma_f32_16x16x32_bf16 v[56:59], v[150:153], v[190:193], v[56:59]
	v_mfma_f32_16x16x32_bf16 v[48:51], v[158:161], v[190:193], v[48:51]
	v_mfma_f32_16x16x32_bf16 v[40:43], v[150:153], v[210:213], v[40:43]
	v_mfma_f32_16x16x32_bf16 v[32:35], v[158:161], v[210:213], v[32:35]
	v_mfma_f32_16x16x32_bf16 v[24:27], v[150:153], v[230:233], v[24:27]
	v_mfma_f32_16x16x32_bf16 v[16:19], v[158:161], v[230:233], v[16:19]
	v_mfma_f32_16x16x32_bf16 v[64:67], v[154:157], v[186:189], v[64:67]
	v_mfma_f32_16x16x32_bf16 v[60:63], v[162:165], v[186:189], v[60:63]
	v_mfma_f32_16x16x32_bf16 v[56:59], v[154:157], v[194:197], v[56:59]
	v_mfma_f32_16x16x32_bf16 v[48:51], v[162:165], v[194:197], v[48:51]
	v_mfma_f32_16x16x32_bf16 v[40:43], v[154:157], v[226:229], v[40:43]
	v_mfma_f32_16x16x32_bf16 v[32:35], v[162:165], v[226:229], v[32:35]
	v_mfma_f32_16x16x32_bf16 v[24:27], v[154:157], v[234:237], v[24:27]
	v_mfma_f32_16x16x32_bf16 v[16:19], v[162:165], v[234:237], v[16:19]
	s_setprio 0
	s_setprio 1
	v_mfma_f32_16x16x32_bf16 v[52:55], v[166:169], v[182:185], v[52:55]
	v_mfma_f32_16x16x32_bf16 v[44:47], v[174:177], v[182:185], v[44:47]
	v_mfma_f32_16x16x32_bf16 v[36:39], v[166:169], v[190:193], v[36:39]
	v_mfma_f32_16x16x32_bf16 v[28:31], v[174:177], v[190:193], v[28:31]
	v_mfma_f32_16x16x32_bf16 v[20:23], v[166:169], v[210:213], v[20:23]
	v_mfma_f32_16x16x32_bf16 v[12:15], v[174:177], v[210:213], v[12:15]
	v_mfma_f32_16x16x32_bf16 v[8:11], v[166:169], v[230:233], v[8:11]
	v_mfma_f32_16x16x32_bf16 v[4:7], v[174:177], v[230:233], v[4:7]
	v_mfma_f32_16x16x32_bf16 v[52:55], v[170:173], v[186:189], v[52:55]
	v_mfma_f32_16x16x32_bf16 v[44:47], v[178:181], v[186:189], v[44:47]
	v_mfma_f32_16x16x32_bf16 v[36:39], v[170:173], v[194:197], v[36:39]
	v_mfma_f32_16x16x32_bf16 v[28:31], v[178:181], v[194:197], v[28:31]
	v_mfma_f32_16x16x32_bf16 v[20:23], v[170:173], v[226:229], v[20:23]
	v_mfma_f32_16x16x32_bf16 v[12:15], v[178:181], v[226:229], v[12:15]
	v_mfma_f32_16x16x32_bf16 v[8:11], v[170:173], v[234:237], v[8:11]
	s_barrier
	v_mfma_f32_16x16x32_bf16 v[4:7], v[178:181], v[234:237], v[4:7]
	s_setprio 0
	s_add_i32 s47, 0, 0x18000
	v_add_u32_e32 v149, s47, v146
	s_add_i32 s48, 0, 0x1c000
	ds_read_b128 v[150:153], v149
	ds_read_b128 v[154:157], v149 offset:1024
	ds_read_b128 v[158:161], v149 offset:2048
	ds_read_b128 v[162:165], v149 offset:3072
	v_add_u32_e32 v149, s48, v146
	ds_read_b128 v[166:169], v149
	ds_read_b128 v[170:173], v149 offset:1024
	ds_read_b128 v[174:177], v149 offset:2048
	ds_read_b128 v[178:181], v149 offset:3072
	s_add_u32 s14, s20, 0xb0000
	s_addc_u32 s15, s21, 0
	s_mov_b32 m0, s30
	v_lshl_add_u64 v[244:245], s[14:15], 0, v[132:133]
	ds_read_b128 v[182:185], v148 offset:32768
	ds_read_b128 v[186:189], v148 offset:33792
	ds_read_b128 v[190:193], v148 offset:34816
	ds_read_b128 v[194:197], v148 offset:35840
	ds_read_b128 v[210:213], v148 offset:36864
	ds_read_b128 v[226:229], v148 offset:37888
	ds_read_b128 v[230:233], v148 offset:38912
	ds_read_b128 v[234:237], v148 offset:39936
	s_mov_b32 m0, s28
	s_nop 0
	global_load_lds_dwordx4 v[240:241], off
	s_mov_b32 m0, s29
	s_nop 0
	global_load_lds_dwordx4 v[242:243], off
	s_mov_b32 m0, s30
	s_nop 0
	global_load_lds_dwordx4 v[244:245], off
	v_lshl_add_u64 v[244:245], s[14:15], 0, v[136:137]
	s_mov_b32 m0, s31
	s_nop 0
	global_load_lds_dwordx4 v[244:245], off
	s_waitcnt vmcnt(8)
	s_waitcnt lgkmcnt(0)
	s_barrier
; #define PG8_STAGE(bufoff, gbase, voff) do { _Pragma("unroll") for (int _i = 0; _i < 2; ++_i) \
;         __builtin_amdgcn_global_load_lds((const unsigned*)((const char*)(gbase) + (voff)[_i]), (PG8_LAS unsigned*)(lds + (bufoff) + ldsw + _i * 8192), 16, 0, 0); } while (0)
; #define PG8_LDA(dst, b, h) do { _Pragma("unroll") for (int m = 0; m < 4; ++m) _Pragma("unroll") for (int k = 0; k < 2; ++k) dst[m][k] = *(const PG8_LAS bf16x8*)(lds + PG8_SA(b, h) + aoff + m * 2048 + k * 1024); } while (0)
; #define PG8_MMA(ai, bj, At, Bt) do { __builtin_amdgcn_s_setprio(1); _Pragma("unroll") for (int m = 0; m < 4; ++m) _Pragma("unroll") for (int n = 0; n < 2; ++n) _Pragma("unroll") for (int k = 0; k < 2; ++k) \
;         acc[ai][bj][m][n] = __builtin_amdgcn_mfma_f32_16x16x32_bf16(Bt[n][k], At[m][k], acc[ai][bj][m][n], 0, 0, 0); __builtin_amdgcn_s_setprio(0); } while (0)
; #define PG8_WAIT_V(n) asm volatile("s_waitcnt vmcnt(" #n ")" ::: "memory")
; #define PG8_WAIT_L(n) asm volatile("s_waitcnt lgkmcnt(" #n ")" ::: "memory")
; #define PG8_BAR __builtin_amdgcn_s_barrier()
; #define PG8_SCHED __builtin_amdgcn_sched_barrier(0)
; template <class Epi, class Sched, bool ALIGN_EPI = false, bool SP2 = false>
; __device__ __forceinline__ void gemm_phase(PG8_LAS unsigned char* lds, const Gemm g, const Sched& S, const Epi& E) {
;     ...
;             PG8_WAIT_V(8); PG8_WAIT_L(0); PG8_BAR; PG8_MMA(0, 0, At, B0); PG8_MMA(0, 1, At, B1); PG8_BAR; PG8_SCHED;
;             PG8_LDA(At, 1, 1); PG8_STAGE(PG8_SB(1, 0), b3, voffB); PG8_STAGE(PG8_SB(1, 1), b3 + hstepB, voffB); PG8_STAGE(PG8_SA(1, 0), a3, voffA);
;             PG8_WAIT_V(8); PG8_WAIT_L(0); PG8_BAR; PG8_MMA(1, 0, At, B0); PG8_MMA(1, 1, At, B1); PG8_BAR; PG8_SCHED;
;     ...
;         if constexpr (ALIGN_EPI) { if (wr == 0) PG8_BAR; }
	s_setprio 1
	s_waitcnt lgkmcnt(0)
	v_mfma_f32_16x16x32_bf16 v[128:131], v[150:153], v[182:185], v[128:131]
	v_mfma_f32_16x16x32_bf16 v[124:127], v[158:161], v[182:185], v[124:127]
	v_mfma_f32_16x16x32_bf16 v[120:123], v[150:153], v[190:193], v[120:123]
	v_mfma_f32_16x16x32_bf16 v[112:115], v[158:161], v[190:193], v[112:115]
	v_mfma_f32_16x16x32_bf16 v[104:107], v[150:153], v[210:213], v[104:107]
	v_mfma_f32_16x16x32_bf16 v[96:99], v[158:161], v[210:213], v[96:99]
	v_mfma_f32_16x16x32_bf16 v[88:91], v[150:153], v[230:233], v[88:91]
	v_mfma_f32_16x16x32_bf16 v[80:83], v[158:161], v[230:233], v[80:83]
	v_mfma_f32_16x16x32_bf16 v[128:131], v[154:157], v[186:189], v[128:131]
	v_mfma_f32_16x16x32_bf16 v[124:127], v[162:165], v[186:189], v[124:127]
	v_mfma_f32_16x16x32_bf16 v[120:123], v[154:157], v[194:197], v[120:123]
	v_mfma_f32_16x16x32_bf16 v[112:115], v[162:165], v[194:197], v[112:115]
	v_mfma_f32_16x16x32_bf16 v[104:107], v[154:157], v[226:229], v[104:107]
	v_mfma_f32_16x16x32_bf16 v[96:99], v[162:165], v[226:229], v[96:99]
	v_mfma_f32_16x16x32_bf16 v[88:91], v[154:157], v[234:237], v[88:91]
	v_mfma_f32_16x16x32_bf16 v[80:83], v[162:165], v[234:237], v[80:83]
	s_setprio 0
	s_setprio 1
	v_mfma_f32_16x16x32_bf16 v[116:119], v[166:169], v[182:185], v[116:119]
	v_mfma_f32_16x16x32_bf16 v[108:111], v[174:177], v[182:185], v[108:111]
	v_mfma_f32_16x16x32_bf16 v[100:103], v[166:169], v[190:193], v[100:103]
	v_mfma_f32_16x16x32_bf16 v[92:95], v[174:177], v[190:193], v[92:95]
	v_mfma_f32_16x16x32_bf16 v[84:87], v[166:169], v[210:213], v[84:87]
	v_mfma_f32_16x16x32_bf16 v[76:79], v[174:177], v[210:213], v[76:79]
	v_mfma_f32_16x16x32_bf16 v[72:75], v[166:169], v[230:233], v[72:75]
	v_mfma_f32_16x16x32_bf16 v[68:71], v[174:177], v[230:233], v[68:71]
	v_mfma_f32_16x16x32_bf16 v[116:119], v[170:173], v[186:189], v[116:119]
	v_mfma_f32_16x16x32_bf16 v[108:111], v[178:181], v[186:189], v[108:111]
	v_mfma_f32_16x16x32_bf16 v[100:103], v[170:173], v[194:197], v[100:103]
	v_mfma_f32_16x16x32_bf16 v[92:95], v[178:181], v[194:197], v[92:95]
	v_mfma_f32_16x16x32_bf16 v[84:87], v[170:173], v[226:229], v[84:87]
	v_mfma_f32_16x16x32_bf16 v[76:79], v[178:181], v[226:229], v[76:79]
	v_mfma_f32_16x16x32_bf16 v[72:75], v[170:173], v[234:237], v[72:75]
	s_barrier
	v_mfma_f32_16x16x32_bf16 v[68:71], v[178:181], v[234:237], v[68:71]
	s_setprio 0
	s_add_i32 s14, s47, s27
	v_lshl_add_u64 v[144:145], v[144:145], 0, s[64:65]
	s_mov_b32 m0, s14
	ds_read_b128 v[182:185], v148 offset:49152
	ds_read_b128 v[186:189], v148 offset:50176
	ds_read_b128 v[190:193], v148 offset:51200
	ds_read_b128 v[194:197], v148 offset:52224
	ds_read_b128 v[210:213], v148 offset:53248
	ds_read_b128 v[226:229], v148 offset:54272
	ds_read_b128 v[230:233], v148 offset:55296
	ds_read_b128 v[234:237], v148 offset:56320
	global_load_lds_dwordx4 v[144:145], off
	s_add_i32 m0, s14, 0x2000
	s_add_u32 s14, s18, 0xb0080
	v_lshl_add_u64 v[144:145], v[238:239], 0, s[64:65]
	s_addc_u32 s15, s19, 0
	s_add_i32 s18, s48, s27
	global_load_lds_dwordx4 v[144:145], off
	v_lshl_add_u64 v[144:145], s[14:15], 0, v[134:135]
	s_mov_b32 m0, s18
	s_nop 0
	global_load_lds_dwordx4 v[144:145], off
	v_lshl_add_u64 v[144:145], s[14:15], 0, v[138:139]
	s_add_i32 m0, s18, 0x2000
	s_nop 0
	global_load_lds_dwordx4 v[144:145], off
	s_waitcnt vmcnt(6)
	s_waitcnt lgkmcnt(0)
	s_barrier
	s_setprio 1
	s_waitcnt lgkmcnt(0)
	v_mfma_f32_16x16x32_bf16 v[64:67], v[150:153], v[182:185], v[64:67]
	v_mfma_f32_16x16x32_bf16 v[60:63], v[158:161], v[182:185], v[60:63]
	v_mfma_f32_16x16x32_bf16 v[56:59], v[150:153], v[190:193], v[56:59]
	v_mfma_f32_16x16x32_bf16 v[48:51], v[158:161], v[190:193], v[48:51]
	v_mfma_f32_16x16x32_bf16 v[40:43], v[150:153], v[210:213], v[40:43]
	v_mfma_f32_16x16x32_bf16 v[32:35], v[158:161], v[210:213], v[32:35]
	v_mfma_f32_16x16x32_bf16 v[24:27], v[150:153], v[230:233], v[24:27]
	v_mfma_f32_16x16x32_bf16 v[16:19], v[158:161], v[230:233], v[16:19]
	v_mfma_f32_16x16x32_bf16 v[64:67], v[154:157], v[186:189], v[64:67]
	v_mfma_f32_16x16x32_bf16 v[60:63], v[162:165], v[186:189], v[60:63]
	v_mfma_f32_16x16x32_bf16 v[56:59], v[154:157], v[194:197], v[56:59]
	v_mfma_f32_16x16x32_bf16 v[48:51], v[162:165], v[194:197], v[48:51]
	v_mfma_f32_16x16x32_bf16 v[40:43], v[154:157], v[226:229], v[40:43]
	v_mfma_f32_16x16x32_bf16 v[32:35], v[162:165], v[226:229], v[32:35]
	v_mfma_f32_16x16x32_bf16 v[24:27], v[154:157], v[234:237], v[24:27]
	v_mfma_f32_16x16x32_bf16 v[16:19], v[162:165], v[234:237], v[16:19]
	s_setprio 0
	s_setprio 1
	v_mfma_f32_16x16x32_bf16 v[52:55], v[166:169], v[182:185], v[52:55]
	v_mfma_f32_16x16x32_bf16 v[44:47], v[174:177], v[182:185], v[44:47]
	v_mfma_f32_16x16x32_bf16 v[36:39], v[166:169], v[190:193], v[36:39]
	v_mfma_f32_16x16x32_bf16 v[28:31], v[174:177], v[190:193], v[28:31]
	v_mfma_f32_16x16x32_bf16 v[20:23], v[166:169], v[210:213], v[20:23]
	v_mfma_f32_16x16x32_bf16 v[12:15], v[174:177], v[210:213], v[12:15]
	v_mfma_f32_16x16x32_bf16 v[8:11], v[166:169], v[230:233], v[8:11]
	v_mfma_f32_16x16x32_bf16 v[4:7], v[174:177], v[230:233], v[4:7]
	v_mfma_f32_16x16x32_bf16 v[52:55], v[170:173], v[186:189], v[52:55]
	v_mfma_f32_16x16x32_bf16 v[44:47], v[178:181], v[186:189], v[44:47]
	v_mfma_f32_16x16x32_bf16 v[36:39], v[170:173], v[194:197], v[36:39]
	v_mfma_f32_16x16x32_bf16 v[28:31], v[178:181], v[194:197], v[28:31]
	v_mfma_f32_16x16x32_bf16 v[20:23], v[170:173], v[226:229], v[20:23]
	v_mfma_f32_16x16x32_bf16 v[12:15], v[178:181], v[226:229], v[12:15]
	v_mfma_f32_16x16x32_bf16 v[8:11], v[170:173], v[234:237], v[8:11]
	s_barrier
	v_mfma_f32_16x16x32_bf16 v[4:7], v[178:181], v[234:237], v[4:7]
	s_setprio 0
	s_add_i32 s46, s46, 2
	s_add_u32 s44, s44, 0x100
	s_addc_u32 s45, s45, 0
	s_cmp_gt_u32 s46, 41
	s_mov_b64 s[14:15], s[16:17]
	s_cbranch_scc0 .LBB0_669
	s_and_b64 vcc, exec, s[10:11]
	s_cbranch_vccz .LBB0_672
	s_barrier

; #define PG8_STAGE(bufoff, gbase, voff) do { _Pragma("unroll") for (int _i = 0; _i < 2; ++_i) \
;         __builtin_amdgcn_global_load_lds((const unsigned*)((const char*)(gbase) + (voff)[_i]), (PG8_LAS unsigned*)(lds + (bufoff) + ldsw + _i * 8192), 16, 0, 0); } while (0)
; #define PG8_LDA(dst, b, h) do { _Pragma("unroll") for (int m = 0; m < 4; ++m) _Pragma("unroll") for (int k = 0; k < 2; ++k) dst[m][k] = *(const PG8_LAS bf16x8*)(lds + PG8_SA(b, h) + aoff + m * 2048 + k * 1024); } while (0)
; #define PG8_LDB(dst, b, h) do { _Pragma("unroll") for (int n = 0; n < 2; ++n) _Pragma("unroll") for (int k = 0; k < 2; ++k) dst[n][k] = *(const PG8_LAS bf16x8*)(lds + PG8_SB(b, h) + boff + n * 2048 + k * 1024); } while (0)
; #define PG8_MMA(ai, bj, At, Bt) do { __builtin_amdgcn_s_setprio(1); _Pragma("unroll") for (int m = 0; m < 4; ++m) _Pragma("unroll") for (int n = 0; n < 2; ++n) _Pragma("unroll") for (int k = 0; k < 2; ++k) \
;         acc[ai][bj][m][n] = __builtin_amdgcn_mfma_f32_16x16x32_bf16(Bt[n][k], At[m][k], acc[ai][bj][m][n], 0, 0, 0); __builtin_amdgcn_s_setprio(0); } while (0)
; #define PG8_WAIT_V(n) asm volatile("s_waitcnt vmcnt(" #n ")" ::: "memory")
; #define PG8_WAIT_L(n) asm volatile("s_waitcnt lgkmcnt(" #n ")" ::: "memory")
; template <class Epi, class Sched, bool ALIGN_EPI = false, bool SP2 = false>
; __device__ __forceinline__ void gemm_phase(PG8_LAS unsigned char* lds, const Gemm g, const Sched& S, const Epi& E) {
;     ...
;             const bool last = (t == nt - 2);
;             const char* a1 = cA + (size_t)(t + 1) * kstep;
;             const char* a2 = last ? nA : cA + (size_t)(t + 2) * kstep; const char* b2 = last ? nB : cB + (size_t)(t + 2) * kstep;
;             const char* a3 = a2 + kstep; const char* b3 = b2 + kstep;
;             if (last && has_next) S.a_ready(nxt);
;             if constexpr (SP2) {
;             PG8_LDB(B0, 0, 0); PG8_LDB(B1, 0, 1); PG8_SCHED; PG8_LDA(At, 0, 0); PG8_STAGE(PG8_SA(1, 1), a1 + hstepA, voffA);
;             PG8_WAIT_V(8); PG8_WAIT_L(0); PG8_BAR; PG8_MMA(0, 0, At, B0); PG8_MMA(0, 1, At, B1); PG8_BAR; PG8_SCHED;
;             PG8_LDA(At, 0, 1); PG8_STAGE(PG8_SB(0, 0), b2, voffB); PG8_STAGE(PG8_SB(0, 1), b2 + hstepB, voffB); PG8_STAGE(PG8_SA(0, 0), a2, voffA);
;             PG8_WAIT_V(8); PG8_WAIT_L(0); PG8_BAR; PG8_MMA(1, 0, At, B0); PG8_MMA(1, 1, At, B1); PG8_BAR; PG8_SCHED;
.LBB0_816:
	s_add_u32 s28, s26, 0xfffc0080
	s_addc_u32 s29, s27, -1
	s_add_i32 s52, 0, 0x10000
	s_cmp_eq_u32 s51, 12
	s_cselect_b32 s31, s19, s29
	s_cselect_b32 s30, s25, s28
	v_add_u32_e32 v2, s52, v153
	s_cselect_b32 s29, s17, s50
	s_cselect_b32 s28, s48, s49
	s_add_i32 s54, 0, 0x14000
	ds_read_b128 v[148:151], v2
	ds_read_b128 v[156:159], v2 offset:1024
	ds_read_b128 v[160:163], v2 offset:2048
	ds_read_b128 v[164:167], v2 offset:3072
	v_add_u32_e32 v2, s54, v153
	ds_read_b128 v[168:171], v2
	ds_read_b128 v[172:175], v2 offset:1024
	ds_read_b128 v[176:179], v2 offset:2048
	ds_read_b128 v[180:183], v2 offset:3072
	v_lshl_add_u64 v[196:197], s[26:27], 0, v[144:145]
	s_add_i32 m0, s35, 0xc000
	ds_read_b128 v[184:187], v154
	ds_read_b128 v[188:191], v154 offset:1024
	ds_read_b128 v[192:195], v154 offset:2048
	ds_read_b128 v[210:213], v154 offset:3072
	ds_read_b128 v[226:229], v154 offset:4096
	ds_read_b128 v[230:233], v154 offset:5120
	ds_read_b128 v[234:237], v154 offset:6144
	ds_read_b128 v[238:241], v154 offset:7168
	v_lshl_add_u64 v[248:249], v[244:245], 0, s[64:65]
	s_mov_b32 m0, s43
	s_nop 0
	global_load_lds_dwordx4 v[248:249], off
	v_lshl_add_u64 v[248:249], v[246:247], 0, s[64:65]
	s_mov_b32 m0, s44
	s_nop 0
	global_load_lds_dwordx4 v[248:249], off
	s_add_i32 m0, s35, 0xc000
	s_nop 0
	global_load_lds_dwordx4 v[196:197], off
	v_lshl_add_u64 v[196:197], s[26:27], 0, v[142:143]
	s_add_i32 m0, s35, 0xe000
	s_nop 0
	global_load_lds_dwordx4 v[196:197], off
	s_waitcnt vmcnt(8)
	s_waitcnt lgkmcnt(0)
	s_barrier
	s_setprio 1
	s_waitcnt lgkmcnt(0)
	v_mfma_f32_16x16x32_bf16 v[128:131], v[148:151], v[184:187], v[128:131]
	v_mfma_f32_16x16x32_bf16 v[124:127], v[160:163], v[184:187], v[124:127]
	v_mfma_f32_16x16x32_bf16 v[116:119], v[148:151], v[192:195], v[116:119]
	v_mfma_f32_16x16x32_bf16 v[108:111], v[160:163], v[192:195], v[108:111]
	v_mfma_f32_16x16x32_bf16 v[100:103], v[148:151], v[226:229], v[100:103]
	v_mfma_f32_16x16x32_bf16 v[92:95], v[160:163], v[226:229], v[92:95]
	v_mfma_f32_16x16x32_bf16 v[84:87], v[148:151], v[234:237], v[84:87]
	v_mfma_f32_16x16x32_bf16 v[76:79], v[160:163], v[234:237], v[76:79]
	v_mfma_f32_16x16x32_bf16 v[128:131], v[156:159], v[188:191], v[128:131]
	v_mfma_f32_16x16x32_bf16 v[124:127], v[164:167], v[188:191], v[124:127]
	v_mfma_f32_16x16x32_bf16 v[116:119], v[156:159], v[210:213], v[116:119]
	v_mfma_f32_16x16x32_bf16 v[108:111], v[164:167], v[210:213], v[108:111]
	v_mfma_f32_16x16x32_bf16 v[100:103], v[156:159], v[230:233], v[100:103]
	v_mfma_f32_16x16x32_bf16 v[92:95], v[164:167], v[230:233], v[92:95]
	v_mfma_f32_16x16x32_bf16 v[84:87], v[156:159], v[238:241], v[84:87]
	v_mfma_f32_16x16x32_bf16 v[76:79], v[164:167], v[238:241], v[76:79]
	s_setprio 0
	s_setprio 1
	v_mfma_f32_16x16x32_bf16 v[120:123], v[168:171], v[184:187], v[120:123]
	v_mfma_f32_16x16x32_bf16 v[112:115], v[176:179], v[184:187], v[112:115]
	v_mfma_f32_16x16x32_bf16 v[104:107], v[168:171], v[192:195], v[104:107]
	v_mfma_f32_16x16x32_bf16 v[96:99], v[176:179], v[192:195], v[96:99]
	v_mfma_f32_16x16x32_bf16 v[88:91], v[168:171], v[226:229], v[88:91]
	v_mfma_f32_16x16x32_bf16 v[80:83], v[176:179], v[226:229], v[80:83]
	v_mfma_f32_16x16x32_bf16 v[72:75], v[168:171], v[234:237], v[72:75]
	v_mfma_f32_16x16x32_bf16 v[68:71], v[176:179], v[234:237], v[68:71]
	v_mfma_f32_16x16x32_bf16 v[120:123], v[172:175], v[188:191], v[120:123]
	v_mfma_f32_16x16x32_bf16 v[112:115], v[180:183], v[188:191], v[112:115]
	v_mfma_f32_16x16x32_bf16 v[104:107], v[172:175], v[210:213], v[104:107]
	v_mfma_f32_16x16x32_bf16 v[96:99], v[180:183], v[210:213], v[96:99]
	v_mfma_f32_16x16x32_bf16 v[88:91], v[172:175], v[230:233], v[88:91]
	v_mfma_f32_16x16x32_bf16 v[80:83], v[180:183], v[230:233], v[80:83]
	v_mfma_f32_16x16x32_bf16 v[72:75], v[172:175], v[238:241], v[72:75]
	s_barrier
	v_mfma_f32_16x16x32_bf16 v[68:71], v[180:183], v[238:241], v[68:71]
	s_setprio 0
	s_add_i32 s52, s52, s33
	v_lshl_add_u64 v[196:197], s[28:29], 0, v[136:137]
	s_mov_b32 m0, s52
	ds_read_b128 v[184:187], v154 offset:16384
	ds_read_b128 v[188:191], v154 offset:17408
	ds_read_b128 v[192:195], v154 offset:18432
	ds_read_b128 v[210:213], v154 offset:19456
	ds_read_b128 v[226:229], v154 offset:20480
	ds_read_b128 v[230:233], v154 offset:21504
	ds_read_b128 v[234:237], v154 offset:22528
	ds_read_b128 v[238:241], v154 offset:23552
	global_load_lds_dwordx4 v[196:197], off
	s_add_i32 m0, s52, 0x2000
	s_add_u32 s52, s28, 0x40000
	v_lshl_add_u64 v[242:243], s[28:29], 0, v[132:133]
	s_addc_u32 s53, s29, 0
	s_add_i32 s54, s54, s33
	global_load_lds_dwordx4 v[242:243], off
	v_lshl_add_u64 v[244:245], s[52:53], 0, v[136:137]
	s_mov_b32 m0, s54
	v_lshl_add_u64 v[246:247], s[30:31], 0, v[134:135]
	global_load_lds_dwordx4 v[244:245], off
	v_lshl_add_u64 v[244:245], s[52:53], 0, v[132:133]
	s_add_i32 m0, s54, 0x2000
	s_nop 0
	global_load_lds_dwordx4 v[244:245], off
	v_lshl_add_u64 v[244:245], s[30:31], 0, v[138:139]
	s_waitcnt vmcnt(6)
	s_waitcnt lgkmcnt(0)
	s_barrier
; #define PG8_STAGE(bufoff, gbase, voff) do { _Pragma("unroll") for (int _i = 0; _i < 2; ++_i) \
;         __builtin_amdgcn_global_load_lds((const unsigned*)((const char*)(gbase) + (voff)[_i]), (PG8_LAS unsigned*)(lds + (bufoff) + ldsw + _i * 8192), 16, 0, 0); } while (0)
; #define PG8_LDA(dst, b, h) do { _Pragma("unroll") for (int m = 0; m < 4; ++m) _Pragma("unroll") for (int k = 0; k < 2; ++k) dst[m][k] = *(const PG8_LAS bf16x8*)(lds + PG8_SA(b, h) + aoff + m * 2048 + k * 1024); } while (0)
; #define PG8_LDB(dst, b, h) do { _Pragma("unroll") for (int n = 0; n < 2; ++n) _Pragma("unroll") for (int k = 0; k < 2; ++k) dst[n][k] = *(const PG8_LAS bf16x8*)(lds + PG8_SB(b, h) + boff + n * 2048 + k * 1024); } while (0)
; #define PG8_MMA(ai, bj, At, Bt) do { __builtin_amdgcn_s_setprio(1); _Pragma("unroll") for (int m = 0; m < 4; ++m) _Pragma("unroll") for (int n = 0; n < 2; ++n) _Pragma("unroll") for (int k = 0; k < 2; ++k) \
;         acc[ai][bj][m][n] = __builtin_amdgcn_mfma_f32_16x16x32_bf16(Bt[n][k], At[m][k], acc[ai][bj][m][n], 0, 0, 0); __builtin_amdgcn_s_setprio(0); } while (0)
; #define PG8_WAIT_V(n) asm volatile("s_waitcnt vmcnt(" #n ")" ::: "memory")
; #define PG8_WAIT_L(n) asm volatile("s_waitcnt lgkmcnt(" #n ")" ::: "memory")
; #define PG8_BAR __builtin_amdgcn_s_barrier()
; #define PG8_SCHED __builtin_amdgcn_sched_barrier(0)
; template <class Epi, class Sched, bool ALIGN_EPI = false, bool SP2 = false>
; __device__ __forceinline__ void gemm_phase(PG8_LAS unsigned char* lds, const Gemm g, const Sched& S, const Epi& E) {
;     ...
;             PG8_WAIT_V(8); PG8_WAIT_L(0); PG8_BAR; PG8_MMA(1, 0, At, B0); PG8_MMA(1, 1, At, B1); PG8_BAR; PG8_SCHED;
;             PG8_LDB(B0, 1, 0); PG8_LDB(B1, 1, 1); PG8_SCHED; PG8_LDA(At, 1, 0); PG8_STAGE(PG8_SA(0, 1), a2 + hstepA, voffA);
;             PG8_WAIT_V(8); PG8_WAIT_L(0); PG8_BAR; PG8_MMA(0, 0, At, B0); PG8_MMA(0, 1, At, B1); PG8_BAR; PG8_SCHED;
;             PG8_LDA(At, 1, 1); PG8_STAGE(PG8_SB(1, 0), b3, voffB); PG8_STAGE(PG8_SB(1, 1), b3 + hstepB, voffB); PG8_STAGE(PG8_SA(1, 0), a3, voffA);
	s_setprio 1
	s_waitcnt lgkmcnt(0)
	v_mfma_f32_16x16x32_bf16 v[64:67], v[148:151], v[184:187], v[64:67]
	v_mfma_f32_16x16x32_bf16 v[60:63], v[160:163], v[184:187], v[60:63]
	v_mfma_f32_16x16x32_bf16 v[52:55], v[148:151], v[192:195], v[52:55]
	v_mfma_f32_16x16x32_bf16 v[44:47], v[160:163], v[192:195], v[44:47]
	v_mfma_f32_16x16x32_bf16 v[36:39], v[148:151], v[226:229], v[36:39]
	v_mfma_f32_16x16x32_bf16 v[28:31], v[160:163], v[226:229], v[28:31]
	v_mfma_f32_16x16x32_bf16 v[20:23], v[148:151], v[234:237], v[20:23]
	v_mfma_f32_16x16x32_bf16 v[12:15], v[160:163], v[234:237], v[12:15]
	v_mfma_f32_16x16x32_bf16 v[64:67], v[156:159], v[188:191], v[64:67]
	v_mfma_f32_16x16x32_bf16 v[60:63], v[164:167], v[188:191], v[60:63]
	v_mfma_f32_16x16x32_bf16 v[52:55], v[156:159], v[210:213], v[52:55]
	v_mfma_f32_16x16x32_bf16 v[44:47], v[164:167], v[210:213], v[44:47]
	v_mfma_f32_16x16x32_bf16 v[36:39], v[156:159], v[230:233], v[36:39]
	v_mfma_f32_16x16x32_bf16 v[28:31], v[164:167], v[230:233], v[28:31]
	v_mfma_f32_16x16x32_bf16 v[20:23], v[156:159], v[238:241], v[20:23]
	v_mfma_f32_16x16x32_bf16 v[12:15], v[164:167], v[238:241], v[12:15]
	s_setprio 0
	s_setprio 1
	v_mfma_f32_16x16x32_bf16 v[56:59], v[168:171], v[184:187], v[56:59]
	v_mfma_f32_16x16x32_bf16 v[48:51], v[176:179], v[184:187], v[48:51]
	v_mfma_f32_16x16x32_bf16 v[40:43], v[168:171], v[192:195], v[40:43]
	v_mfma_f32_16x16x32_bf16 v[32:35], v[176:179], v[192:195], v[32:35]
	v_mfma_f32_16x16x32_bf16 v[24:27], v[168:171], v[226:229], v[24:27]
	v_mfma_f32_16x16x32_bf16 v[16:19], v[176:179], v[226:229], v[16:19]
	v_mfma_f32_16x16x32_bf16 v[8:11], v[168:171], v[234:237], v[8:11]
	v_mfma_f32_16x16x32_bf16 v[4:7], v[176:179], v[234:237], v[4:7]
	v_mfma_f32_16x16x32_bf16 v[56:59], v[172:175], v[188:191], v[56:59]
	v_mfma_f32_16x16x32_bf16 v[48:51], v[180:183], v[188:191], v[48:51]
	v_mfma_f32_16x16x32_bf16 v[40:43], v[172:175], v[210:213], v[40:43]
	v_mfma_f32_16x16x32_bf16 v[32:35], v[180:183], v[210:213], v[32:35]
	v_mfma_f32_16x16x32_bf16 v[24:27], v[172:175], v[230:233], v[24:27]
	v_mfma_f32_16x16x32_bf16 v[16:19], v[180:183], v[230:233], v[16:19]
	v_mfma_f32_16x16x32_bf16 v[8:11], v[172:175], v[238:241], v[8:11]
	s_barrier
	v_mfma_f32_16x16x32_bf16 v[4:7], v[180:183], v[238:241], v[4:7]
	s_setprio 0
	s_add_i32 s52, 0, 0x18000
	v_add_u32_e32 v2, s52, v153
	s_add_i32 s53, 0, 0x1c000
	ds_read_b128 v[148:151], v2
	ds_read_b128 v[156:159], v2 offset:1024
	ds_read_b128 v[160:163], v2 offset:2048
	ds_read_b128 v[164:167], v2 offset:3072
	v_add_u32_e32 v2, s53, v153
	ds_read_b128 v[168:171], v2
	ds_read_b128 v[172:175], v2 offset:1024
	ds_read_b128 v[176:179], v2 offset:2048
	ds_read_b128 v[180:183], v2 offset:3072
	s_add_u32 s30, s30, 0x40000
	s_addc_u32 s31, s31, 0
	s_mov_b32 m0, s39
	v_lshl_add_u64 v[248:249], s[30:31], 0, v[138:139]
	ds_read_b128 v[184:187], v154 offset:32768
	ds_read_b128 v[188:191], v154 offset:33792
	ds_read_b128 v[192:195], v154 offset:34816
	ds_read_b128 v[210:213], v154 offset:35840
	ds_read_b128 v[226:229], v154 offset:36864
	ds_read_b128 v[230:233], v154 offset:37888
	ds_read_b128 v[234:237], v154 offset:38912
	ds_read_b128 v[238:241], v154 offset:39936
	s_mov_b32 m0, s35
	s_nop 0
	global_load_lds_dwordx4 v[244:245], off
	s_mov_b32 m0, s37
	s_nop 0
	global_load_lds_dwordx4 v[246:247], off
	s_mov_b32 m0, s39
	s_nop 0
	global_load_lds_dwordx4 v[248:249], off
	v_lshl_add_u64 v[248:249], s[30:31], 0, v[134:135]
	s_mov_b32 m0, s40
	s_nop 0
	global_load_lds_dwordx4 v[248:249], off
	s_waitcnt vmcnt(8)
	s_waitcnt lgkmcnt(0)
	s_barrier
	s_setprio 1
	s_waitcnt lgkmcnt(0)
	v_mfma_f32_16x16x32_bf16 v[128:131], v[148:151], v[184:187], v[128:131]
	v_mfma_f32_16x16x32_bf16 v[124:127], v[160:163], v[184:187], v[124:127]
	v_mfma_f32_16x16x32_bf16 v[116:119], v[148:151], v[192:195], v[116:119]
	v_mfma_f32_16x16x32_bf16 v[108:111], v[160:163], v[192:195], v[108:111]
	v_mfma_f32_16x16x32_bf16 v[100:103], v[148:151], v[226:229], v[100:103]
	v_mfma_f32_16x16x32_bf16 v[92:95], v[160:163], v[226:229], v[92:95]
	v_mfma_f32_16x16x32_bf16 v[84:87], v[148:151], v[234:237], v[84:87]
	v_mfma_f32_16x16x32_bf16 v[76:79], v[160:163], v[234:237], v[76:79]
	v_mfma_f32_16x16x32_bf16 v[128:131], v[156:159], v[188:191], v[128:131]
	v_mfma_f32_16x16x32_bf16 v[124:127], v[164:167], v[188:191], v[124:127]
	v_mfma_f32_16x16x32_bf16 v[116:119], v[156:159], v[210:213], v[116:119]
	v_mfma_f32_16x16x32_bf16 v[108:111], v[164:167], v[210:213], v[108:111]
	v_mfma_f32_16x16x32_bf16 v[100:103], v[156:159], v[230:233], v[100:103]
	v_mfma_f32_16x16x32_bf16 v[92:95], v[164:167], v[230:233], v[92:95]
	v_mfma_f32_16x16x32_bf16 v[84:87], v[156:159], v[238:241], v[84:87]
	v_mfma_f32_16x16x32_bf16 v[76:79], v[164:167], v[238:241], v[76:79]
	s_setprio 0
	s_setprio 1
	v_mfma_f32_16x16x32_bf16 v[120:123], v[168:171], v[184:187], v[120:123]
	v_mfma_f32_16x16x32_bf16 v[112:115], v[176:179], v[184:187], v[112:115]
	v_mfma_f32_16x16x32_bf16 v[104:107], v[168:171], v[192:195], v[104:107]
	v_mfma_f32_16x16x32_bf16 v[96:99], v[176:179], v[192:195], v[96:99]
	v_mfma_f32_16x16x32_bf16 v[88:91], v[168:171], v[226:229], v[88:91]
	v_mfma_f32_16x16x32_bf16 v[80:83], v[176:179], v[226:229], v[80:83]
	v_mfma_f32_16x16x32_bf16 v[72:75], v[168:171], v[234:237], v[72:75]
	v_mfma_f32_16x16x32_bf16 v[68:71], v[176:179], v[234:237], v[68:71]
	v_mfma_f32_16x16x32_bf16 v[120:123], v[172:175], v[188:191], v[120:123]
	v_mfma_f32_16x16x32_bf16 v[112:115], v[180:183], v[188:191], v[112:115]
	v_mfma_f32_16x16x32_bf16 v[104:107], v[172:175], v[210:213], v[104:107]
	v_mfma_f32_16x16x32_bf16 v[96:99], v[180:183], v[210:213], v[96:99]
	v_mfma_f32_16x16x32_bf16 v[88:91], v[172:175], v[230:233], v[88:91]
	v_mfma_f32_16x16x32_bf16 v[80:83], v[180:183], v[230:233], v[80:83]
	v_mfma_f32_16x16x32_bf16 v[72:75], v[172:175], v[238:241], v[72:75]
	s_barrier
; #define PG8_STAGE(bufoff, gbase, voff) do { _Pragma("unroll") for (int _i = 0; _i < 2; ++_i) \
;         __builtin_amdgcn_global_load_lds((const unsigned*)((const char*)(gbase) + (voff)[_i]), (PG8_LAS unsigned*)(lds + (bufoff) + ldsw + _i * 8192), 16, 0, 0); } while (0)
; #define PG8_LDA(dst, b, h) do { _Pragma("unroll") for (int m = 0; m < 4; ++m) _Pragma("unroll") for (int k = 0; k < 2; ++k) dst[m][k] = *(const PG8_LAS bf16x8*)(lds + PG8_SA(b, h) + aoff + m * 2048 + k * 1024); } while (0)
; #define PG8_MMA(ai, bj, At, Bt) do { __builtin_amdgcn_s_setprio(1); _Pragma("unroll") for (int m = 0; m < 4; ++m) _Pragma("unroll") for (int n = 0; n < 2; ++n) _Pragma("unroll") for (int k = 0; k < 2; ++k) \
;         acc[ai][bj][m][n] = __builtin_amdgcn_mfma_f32_16x16x32_bf16(Bt[n][k], At[m][k], acc[ai][bj][m][n], 0, 0, 0); __builtin_amdgcn_s_setprio(0); } while (0)
; #define PG8_WAIT_V(n) asm volatile("s_waitcnt vmcnt(" #n ")" ::: "memory")
; #define PG8_WAIT_L(n) asm volatile("s_waitcnt lgkmcnt(" #n ")" ::: "memory")
; #define PG8_BAR __builtin_amdgcn_s_barrier()
; #define PG8_SCHED __builtin_amdgcn_sched_barrier(0)
; template <class Epi, class Sched, bool ALIGN_EPI = false, bool SP2 = false>
; __device__ __forceinline__ void gemm_phase(PG8_LAS unsigned char* lds, const Gemm g, const Sched& S, const Epi& E) {
;     ...
;             PG8_WAIT_V(8); PG8_WAIT_L(0); PG8_BAR; PG8_MMA(0, 0, At, B0); PG8_MMA(0, 1, At, B1); PG8_BAR; PG8_SCHED;
;             PG8_LDA(At, 1, 1); PG8_STAGE(PG8_SB(1, 0), b3, voffB); PG8_STAGE(PG8_SB(1, 1), b3 + hstepB, voffB); PG8_STAGE(PG8_SA(1, 0), a3, voffA);
;             PG8_WAIT_V(8); PG8_WAIT_L(0); PG8_BAR; PG8_MMA(1, 0, At, B0); PG8_MMA(1, 1, At, B1); PG8_BAR; PG8_SCHED;
	v_mfma_f32_16x16x32_bf16 v[68:71], v[180:183], v[238:241], v[68:71]
	s_setprio 0
	s_add_i32 s30, s52, s33
	v_lshl_add_u64 v[196:197], v[196:197], 0, s[64:65]
	s_mov_b32 m0, s30
	ds_read_b128 v[184:187], v154 offset:49152
	ds_read_b128 v[188:191], v154 offset:50176
	ds_read_b128 v[192:195], v154 offset:51200
	ds_read_b128 v[210:213], v154 offset:52224
	ds_read_b128 v[226:229], v154 offset:53248
	ds_read_b128 v[230:233], v154 offset:54272
	ds_read_b128 v[234:237], v154 offset:55296
	ds_read_b128 v[238:241], v154 offset:56320
	global_load_lds_dwordx4 v[196:197], off
	s_add_i32 m0, s30, 0x2000
	s_add_u32 s28, s28, 0x40080
	v_lshl_add_u64 v[196:197], v[242:243], 0, s[64:65]
	s_addc_u32 s29, s29, 0
	s_add_i32 s30, s53, s33
	global_load_lds_dwordx4 v[196:197], off
	v_lshl_add_u64 v[196:197], s[28:29], 0, v[136:137]
	s_mov_b32 m0, s30
	s_nop 0
	global_load_lds_dwordx4 v[196:197], off
	v_lshl_add_u64 v[196:197], s[28:29], 0, v[132:133]
	s_add_i32 m0, s30, 0x2000
	s_nop 0
	global_load_lds_dwordx4 v[196:197], off
	s_waitcnt vmcnt(6)
	s_waitcnt lgkmcnt(0)
	s_barrier
	s_setprio 1
	s_waitcnt lgkmcnt(0)
	v_mfma_f32_16x16x32_bf16 v[64:67], v[148:151], v[184:187], v[64:67]
	v_mfma_f32_16x16x32_bf16 v[60:63], v[160:163], v[184:187], v[60:63]
	v_mfma_f32_16x16x32_bf16 v[52:55], v[148:151], v[192:195], v[52:55]
	v_mfma_f32_16x16x32_bf16 v[44:47], v[160:163], v[192:195], v[44:47]
	v_mfma_f32_16x16x32_bf16 v[36:39], v[148:151], v[226:229], v[36:39]
	v_mfma_f32_16x16x32_bf16 v[28:31], v[160:163], v[226:229], v[28:31]
	v_mfma_f32_16x16x32_bf16 v[20:23], v[148:151], v[234:237], v[20:23]
	v_mfma_f32_16x16x32_bf16 v[12:15], v[160:163], v[234:237], v[12:15]
	v_mfma_f32_16x16x32_bf16 v[64:67], v[156:159], v[188:191], v[64:67]
	v_mfma_f32_16x16x32_bf16 v[60:63], v[164:167], v[188:191], v[60:63]
	v_mfma_f32_16x16x32_bf16 v[52:55], v[156:159], v[210:213], v[52:55]
	v_mfma_f32_16x16x32_bf16 v[44:47], v[164:167], v[210:213], v[44:47]
	v_mfma_f32_16x16x32_bf16 v[36:39], v[156:159], v[230:233], v[36:39]
	v_mfma_f32_16x16x32_bf16 v[28:31], v[164:167], v[230:233], v[28:31]
	v_mfma_f32_16x16x32_bf16 v[20:23], v[156:159], v[238:241], v[20:23]
	v_mfma_f32_16x16x32_bf16 v[12:15], v[164:167], v[238:241], v[12:15]
	s_setprio 0
	s_setprio 1
	v_mfma_f32_16x16x32_bf16 v[56:59], v[168:171], v[184:187], v[56:59]
	v_mfma_f32_16x16x32_bf16 v[48:51], v[176:179], v[184:187], v[48:51]
	v_mfma_f32_16x16x32_bf16 v[40:43], v[168:171], v[192:195], v[40:43]
	v_mfma_f32_16x16x32_bf16 v[32:35], v[176:179], v[192:195], v[32:35]
	v_mfma_f32_16x16x32_bf16 v[24:27], v[168:171], v[226:229], v[24:27]
	v_mfma_f32_16x16x32_bf16 v[16:19], v[176:179], v[226:229], v[16:19]
	v_mfma_f32_16x16x32_bf16 v[8:11], v[168:171], v[234:237], v[8:11]
	v_mfma_f32_16x16x32_bf16 v[4:7], v[176:179], v[234:237], v[4:7]
	v_mfma_f32_16x16x32_bf16 v[56:59], v[172:175], v[188:191], v[56:59]
	v_mfma_f32_16x16x32_bf16 v[48:51], v[180:183], v[188:191], v[48:51]
	v_mfma_f32_16x16x32_bf16 v[40:43], v[172:175], v[210:213], v[40:43]
	v_mfma_f32_16x16x32_bf16 v[32:35], v[180:183], v[210:213], v[32:35]
	v_mfma_f32_16x16x32_bf16 v[24:27], v[172:175], v[230:233], v[24:27]
	v_mfma_f32_16x16x32_bf16 v[16:19], v[180:183], v[230:233], v[16:19]
	v_mfma_f32_16x16x32_bf16 v[8:11], v[172:175], v[238:241], v[8:11]
	s_barrier
	v_mfma_f32_16x16x32_bf16 v[4:7], v[180:183], v[238:241], v[4:7]
	s_setprio 0
	s_add_i32 s51, s51, 2
	s_add_u32 s49, s49, 0x100
	s_addc_u32 s50, s50, 0
	s_add_u32 s26, s26, 0x100
	s_addc_u32 s27, s27, 0
	s_cmp_gt_u32 s51, 13
	s_cbranch_scc0 .LBB0_816
	s_and_b64 vcc, exec, s[14:15]
	s_cbranch_vccnz .LBB0_821
	v_lshl_add_u32 v150, s24, 8, v152
	s_cmp_gt_i32 s47, 11
	s_mov_b64 s[24:25], -1
	s_cbranch_scc1 .LBB0_822

; #define PG8_STAGE(bufoff, gbase, voff) do { _Pragma("unroll") for (int _i = 0; _i < 2; ++_i) \
;         __builtin_amdgcn_global_load_lds((const unsigned*)((const char*)(gbase) + (voff)[_i]), (PG8_LAS unsigned*)(lds + (bufoff) + ldsw + _i * 8192), 16, 0, 0); } while (0)
; #define PG8_LDA(dst, b, h) do { _Pragma("unroll") for (int m = 0; m < 4; ++m) _Pragma("unroll") for (int k = 0; k < 2; ++k) dst[m][k] = *(const PG8_LAS bf16x8*)(lds + PG8_SA(b, h) + aoff + m * 2048 + k * 1024); } while (0)
; #define PG8_LDB(dst, b, h) do { _Pragma("unroll") for (int n = 0; n < 2; ++n) _Pragma("unroll") for (int k = 0; k < 2; ++k) dst[n][k] = *(const PG8_LAS bf16x8*)(lds + PG8_SB(b, h) + boff + n * 2048 + k * 1024); } while (0)
; #define PG8_MMA(ai, bj, At, Bt) do { __builtin_amdgcn_s_setprio(1); _Pragma("unroll") for (int m = 0; m < 4; ++m) _Pragma("unroll") for (int n = 0; n < 2; ++n) _Pragma("unroll") for (int k = 0; k < 2; ++k) \
;         acc[ai][bj][m][n] = __builtin_amdgcn_mfma_f32_16x16x32_bf16(Bt[n][k], At[m][k], acc[ai][bj][m][n], 0, 0, 0); __builtin_amdgcn_s_setprio(0); } while (0)
; #define PG8_WAIT_V(n) asm volatile("s_waitcnt vmcnt(" #n ")" ::: "memory")
; #define PG8_WAIT_L(n) asm volatile("s_waitcnt lgkmcnt(" #n ")" ::: "memory")
; template <class Epi, class Sched, bool ALIGN_EPI = false, bool SP2 = false>
; __device__ __forceinline__ void gemm_phase(PG8_LAS unsigned char* lds, const Gemm g, const Sched& S, const Epi& E) {
;     ...
;             const bool last = (t == nt - 2);
;             const char* a1 = cA + (size_t)(t + 1) * kstep;
;             const char* a2 = last ? nA : cA + (size_t)(t + 2) * kstep; const char* b2 = last ? nB : cB + (size_t)(t + 2) * kstep;
;             const char* a3 = a2 + kstep; const char* b3 = b2 + kstep;
;             if (last && has_next) S.a_ready(nxt);
;             if constexpr (SP2) {
;             PG8_LDB(B0, 0, 0); PG8_LDB(B1, 0, 1); PG8_SCHED; PG8_LDA(At, 0, 0); PG8_STAGE(PG8_SA(1, 1), a1 + hstepA, voffA);
;             PG8_WAIT_V(8); PG8_WAIT_L(0); PG8_BAR; PG8_MMA(0, 0, At, B0); PG8_MMA(0, 1, At, B1); PG8_BAR; PG8_SCHED;
;             PG8_LDA(At, 0, 1); PG8_STAGE(PG8_SB(0, 0), b2, voffB); PG8_STAGE(PG8_SB(0, 1), b2 + hstepB, voffB); PG8_STAGE(PG8_SA(0, 0), a2, voffA);
;             PG8_WAIT_V(8); PG8_WAIT_L(0); PG8_BAR; PG8_MMA(1, 0, At, B0); PG8_MMA(1, 1, At, B1); PG8_BAR; PG8_SCHED;
.LBB0_1093:
	s_add_u32 s24, s22, 0xfffc0080
	s_addc_u32 s25, s23, -1
	s_add_i32 s49, 0, 0x10000
	s_cmp_eq_u32 s48, 12
	s_cselect_b32 s27, s15, s25
	s_cselect_b32 s26, s44, s24
	v_add_u32_e32 v144, s49, v146
	s_cselect_b32 s25, s13, s47
	s_cselect_b32 s24, s45, s46
	s_add_i32 s52, 0, 0x14000
	ds_read_b128 v[150:153], v144
	ds_read_b128 v[154:157], v144 offset:1024
	ds_read_b128 v[158:161], v144 offset:2048
	ds_read_b128 v[162:165], v144 offset:3072
	v_add_u32_e32 v144, s52, v146
	ds_read_b128 v[166:169], v144
	ds_read_b128 v[170:173], v144 offset:1024
	ds_read_b128 v[174:177], v144 offset:2048
	ds_read_b128 v[178:181], v144 offset:3072
	v_lshl_add_u64 v[144:145], s[22:23], 0, v[142:143]
	s_add_i32 m0, s17, 0xc000
	ds_read_b128 v[182:185], v148
	ds_read_b128 v[186:189], v148 offset:1024
	ds_read_b128 v[190:193], v148 offset:2048
	ds_read_b128 v[194:197], v148 offset:3072
	ds_read_b128 v[210:213], v148 offset:4096
	ds_read_b128 v[226:229], v148 offset:5120
	ds_read_b128 v[230:233], v148 offset:6144
	ds_read_b128 v[234:237], v148 offset:7168
	v_lshl_add_u64 v[244:245], v[240:241], 0, s[64:65]
	s_mov_b32 m0, s39
	s_nop 0
	global_load_lds_dwordx4 v[244:245], off
	v_lshl_add_u64 v[244:245], v[242:243], 0, s[64:65]
	s_mov_b32 m0, s40
	s_nop 0
	global_load_lds_dwordx4 v[244:245], off
	s_add_i32 m0, s17, 0xc000
	s_nop 0
	global_load_lds_dwordx4 v[144:145], off
	v_lshl_add_u64 v[144:145], s[22:23], 0, v[140:141]
	s_add_i32 m0, s17, 0xe000
	s_nop 0
	global_load_lds_dwordx4 v[144:145], off
	s_waitcnt vmcnt(8)
	s_waitcnt lgkmcnt(0)
	s_barrier
	s_setprio 1
	s_waitcnt lgkmcnt(0)
	v_mfma_f32_16x16x32_bf16 v[128:131], v[150:153], v[182:185], v[128:131]
	v_mfma_f32_16x16x32_bf16 v[124:127], v[158:161], v[182:185], v[124:127]
	v_mfma_f32_16x16x32_bf16 v[120:123], v[150:153], v[190:193], v[120:123]
	v_mfma_f32_16x16x32_bf16 v[112:115], v[158:161], v[190:193], v[112:115]
	v_mfma_f32_16x16x32_bf16 v[104:107], v[150:153], v[210:213], v[104:107]
	v_mfma_f32_16x16x32_bf16 v[96:99], v[158:161], v[210:213], v[96:99]
	v_mfma_f32_16x16x32_bf16 v[88:91], v[150:153], v[230:233], v[88:91]
	v_mfma_f32_16x16x32_bf16 v[80:83], v[158:161], v[230:233], v[80:83]
	v_mfma_f32_16x16x32_bf16 v[128:131], v[154:157], v[186:189], v[128:131]
	v_mfma_f32_16x16x32_bf16 v[124:127], v[162:165], v[186:189], v[124:127]
	v_mfma_f32_16x16x32_bf16 v[120:123], v[154:157], v[194:197], v[120:123]
	v_mfma_f32_16x16x32_bf16 v[112:115], v[162:165], v[194:197], v[112:115]
	v_mfma_f32_16x16x32_bf16 v[104:107], v[154:157], v[226:229], v[104:107]
	v_mfma_f32_16x16x32_bf16 v[96:99], v[162:165], v[226:229], v[96:99]
	v_mfma_f32_16x16x32_bf16 v[88:91], v[154:157], v[234:237], v[88:91]
	v_mfma_f32_16x16x32_bf16 v[80:83], v[162:165], v[234:237], v[80:83]
	s_setprio 0
	s_setprio 1
	v_mfma_f32_16x16x32_bf16 v[116:119], v[166:169], v[182:185], v[116:119]
	v_mfma_f32_16x16x32_bf16 v[108:111], v[174:177], v[182:185], v[108:111]
	v_mfma_f32_16x16x32_bf16 v[100:103], v[166:169], v[190:193], v[100:103]
	v_mfma_f32_16x16x32_bf16 v[92:95], v[174:177], v[190:193], v[92:95]
	v_mfma_f32_16x16x32_bf16 v[84:87], v[166:169], v[210:213], v[84:87]
	v_mfma_f32_16x16x32_bf16 v[76:79], v[174:177], v[210:213], v[76:79]
	v_mfma_f32_16x16x32_bf16 v[72:75], v[166:169], v[230:233], v[72:75]
	v_mfma_f32_16x16x32_bf16 v[68:71], v[174:177], v[230:233], v[68:71]
	v_mfma_f32_16x16x32_bf16 v[116:119], v[170:173], v[186:189], v[116:119]
	v_mfma_f32_16x16x32_bf16 v[108:111], v[178:181], v[186:189], v[108:111]
	v_mfma_f32_16x16x32_bf16 v[100:103], v[170:173], v[194:197], v[100:103]
	v_mfma_f32_16x16x32_bf16 v[92:95], v[178:181], v[194:197], v[92:95]
	v_mfma_f32_16x16x32_bf16 v[84:87], v[170:173], v[226:229], v[84:87]
	v_mfma_f32_16x16x32_bf16 v[76:79], v[178:181], v[226:229], v[76:79]
	v_mfma_f32_16x16x32_bf16 v[72:75], v[170:173], v[234:237], v[72:75]
	s_barrier
	v_mfma_f32_16x16x32_bf16 v[68:71], v[178:181], v[234:237], v[68:71]
	s_setprio 0
	s_add_i32 s49, s49, s34
	v_lshl_add_u64 v[144:145], s[24:25], 0, v[134:135]
	s_mov_b32 m0, s49
	ds_read_b128 v[182:185], v148 offset:16384
	ds_read_b128 v[186:189], v148 offset:17408
	ds_read_b128 v[190:193], v148 offset:18432
	ds_read_b128 v[194:197], v148 offset:19456
	ds_read_b128 v[210:213], v148 offset:20480
	ds_read_b128 v[226:229], v148 offset:21504
	ds_read_b128 v[230:233], v148 offset:22528
	ds_read_b128 v[234:237], v148 offset:23552
	global_load_lds_dwordx4 v[144:145], off
	s_add_i32 m0, s49, 0x2000
	s_add_u32 s50, s24, 0x40000
	v_lshl_add_u64 v[238:239], s[24:25], 0, v[138:139]
	s_addc_u32 s51, s25, 0
	s_add_i32 s49, s52, s34
	global_load_lds_dwordx4 v[238:239], off
	v_lshl_add_u64 v[240:241], s[50:51], 0, v[134:135]
	s_mov_b32 m0, s49
	v_lshl_add_u64 v[242:243], s[26:27], 0, v[136:137]
	global_load_lds_dwordx4 v[240:241], off
	v_lshl_add_u64 v[240:241], s[50:51], 0, v[138:139]
	s_add_i32 m0, s49, 0x2000
	s_nop 0
	global_load_lds_dwordx4 v[240:241], off
	v_lshl_add_u64 v[240:241], s[26:27], 0, v[132:133]
	s_waitcnt vmcnt(6)
	s_waitcnt lgkmcnt(0)
	s_barrier
; #define PG8_STAGE(bufoff, gbase, voff) do { _Pragma("unroll") for (int _i = 0; _i < 2; ++_i) \
;         __builtin_amdgcn_global_load_lds((const unsigned*)((const char*)(gbase) + (voff)[_i]), (PG8_LAS unsigned*)(lds + (bufoff) + ldsw + _i * 8192), 16, 0, 0); } while (0)
; #define PG8_LDA(dst, b, h) do { _Pragma("unroll") for (int m = 0; m < 4; ++m) _Pragma("unroll") for (int k = 0; k < 2; ++k) dst[m][k] = *(const PG8_LAS bf16x8*)(lds + PG8_SA(b, h) + aoff + m * 2048 + k * 1024); } while (0)
; #define PG8_LDB(dst, b, h) do { _Pragma("unroll") for (int n = 0; n < 2; ++n) _Pragma("unroll") for (int k = 0; k < 2; ++k) dst[n][k] = *(const PG8_LAS bf16x8*)(lds + PG8_SB(b, h) + boff + n * 2048 + k * 1024); } while (0)
; #define PG8_MMA(ai, bj, At, Bt) do { __builtin_amdgcn_s_setprio(1); _Pragma("unroll") for (int m = 0; m < 4; ++m) _Pragma("unroll") for (int n = 0; n < 2; ++n) _Pragma("unroll") for (int k = 0; k < 2; ++k) \
;         acc[ai][bj][m][n] = __builtin_amdgcn_mfma_f32_16x16x32_bf16(Bt[n][k], At[m][k], acc[ai][bj][m][n], 0, 0, 0); __builtin_amdgcn_s_setprio(0); } while (0)
; #define PG8_WAIT_V(n) asm volatile("s_waitcnt vmcnt(" #n ")" ::: "memory")
; #define PG8_WAIT_L(n) asm volatile("s_waitcnt lgkmcnt(" #n ")" ::: "memory")
; #define PG8_BAR __builtin_amdgcn_s_barrier()
; #define PG8_SCHED __builtin_amdgcn_sched_barrier(0)
; template <class Epi, class Sched, bool ALIGN_EPI = false, bool SP2 = false>
; __device__ __forceinline__ void gemm_phase(PG8_LAS unsigned char* lds, const Gemm g, const Sched& S, const Epi& E) {
;     ...
;             PG8_WAIT_V(8); PG8_WAIT_L(0); PG8_BAR; PG8_MMA(1, 0, At, B0); PG8_MMA(1, 1, At, B1); PG8_BAR; PG8_SCHED;
;             PG8_LDB(B0, 1, 0); PG8_LDB(B1, 1, 1); PG8_SCHED; PG8_LDA(At, 1, 0); PG8_STAGE(PG8_SA(0, 1), a2 + hstepA, voffA);
;             PG8_WAIT_V(8); PG8_WAIT_L(0); PG8_BAR; PG8_MMA(0, 0, At, B0); PG8_MMA(0, 1, At, B1); PG8_BAR; PG8_SCHED;
;             PG8_LDA(At, 1, 1); PG8_STAGE(PG8_SB(1, 0), b3, voffB); PG8_STAGE(PG8_SB(1, 1), b3 + hstepB, voffB); PG8_STAGE(PG8_SA(1, 0), a3, voffA);
	s_setprio 1
	s_waitcnt lgkmcnt(0)
	v_mfma_f32_16x16x32_bf16 v[64:67], v[150:153], v[182:185], v[64:67]
	v_mfma_f32_16x16x32_bf16 v[60:63], v[158:161], v[182:185], v[60:63]
	v_mfma_f32_16x16x32_bf16 v[56:59], v[150:153], v[190:193], v[56:59]
	v_mfma_f32_16x16x32_bf16 v[48:51], v[158:161], v[190:193], v[48:51]
	v_mfma_f32_16x16x32_bf16 v[40:43], v[150:153], v[210:213], v[40:43]
	v_mfma_f32_16x16x32_bf16 v[32:35], v[158:161], v[210:213], v[32:35]
	v_mfma_f32_16x16x32_bf16 v[24:27], v[150:153], v[230:233], v[24:27]
	v_mfma_f32_16x16x32_bf16 v[16:19], v[158:161], v[230:233], v[16:19]
	v_mfma_f32_16x16x32_bf16 v[64:67], v[154:157], v[186:189], v[64:67]
	v_mfma_f32_16x16x32_bf16 v[60:63], v[162:165], v[186:189], v[60:63]
	v_mfma_f32_16x16x32_bf16 v[56:59], v[154:157], v[194:197], v[56:59]
	v_mfma_f32_16x16x32_bf16 v[48:51], v[162:165], v[194:197], v[48:51]
	v_mfma_f32_16x16x32_bf16 v[40:43], v[154:157], v[226:229], v[40:43]
	v_mfma_f32_16x16x32_bf16 v[32:35], v[162:165], v[226:229], v[32:35]
	v_mfma_f32_16x16x32_bf16 v[24:27], v[154:157], v[234:237], v[24:27]
	v_mfma_f32_16x16x32_bf16 v[16:19], v[162:165], v[234:237], v[16:19]
	s_setprio 0
	s_setprio 1
	v_mfma_f32_16x16x32_bf16 v[52:55], v[166:169], v[182:185], v[52:55]
	v_mfma_f32_16x16x32_bf16 v[44:47], v[174:177], v[182:185], v[44:47]
	v_mfma_f32_16x16x32_bf16 v[36:39], v[166:169], v[190:193], v[36:39]
	v_mfma_f32_16x16x32_bf16 v[28:31], v[174:177], v[190:193], v[28:31]
	v_mfma_f32_16x16x32_bf16 v[20:23], v[166:169], v[210:213], v[20:23]
	v_mfma_f32_16x16x32_bf16 v[12:15], v[174:177], v[210:213], v[12:15]
	v_mfma_f32_16x16x32_bf16 v[8:11], v[166:169], v[230:233], v[8:11]
	v_mfma_f32_16x16x32_bf16 v[4:7], v[174:177], v[230:233], v[4:7]
	v_mfma_f32_16x16x32_bf16 v[52:55], v[170:173], v[186:189], v[52:55]
	v_mfma_f32_16x16x32_bf16 v[44:47], v[178:181], v[186:189], v[44:47]
	v_mfma_f32_16x16x32_bf16 v[36:39], v[170:173], v[194:197], v[36:39]
	v_mfma_f32_16x16x32_bf16 v[28:31], v[178:181], v[194:197], v[28:31]
	v_mfma_f32_16x16x32_bf16 v[20:23], v[170:173], v[226:229], v[20:23]
	v_mfma_f32_16x16x32_bf16 v[12:15], v[178:181], v[226:229], v[12:15]
	v_mfma_f32_16x16x32_bf16 v[8:11], v[170:173], v[234:237], v[8:11]
	s_barrier
	v_mfma_f32_16x16x32_bf16 v[4:7], v[178:181], v[234:237], v[4:7]
	s_setprio 0
	s_add_i32 s49, 0, 0x18000
	v_add_u32_e32 v149, s49, v146
	s_add_i32 s50, 0, 0x1c000
	ds_read_b128 v[150:153], v149
	ds_read_b128 v[154:157], v149 offset:1024
	ds_read_b128 v[158:161], v149 offset:2048
	ds_read_b128 v[162:165], v149 offset:3072
	v_add_u32_e32 v149, s50, v146
	ds_read_b128 v[166:169], v149
	ds_read_b128 v[170:173], v149 offset:1024
	ds_read_b128 v[174:177], v149 offset:2048
	ds_read_b128 v[178:181], v149 offset:3072
	s_add_u32 s26, s26, 0x40000
	s_addc_u32 s27, s27, 0
	s_mov_b32 m0, s37
	v_lshl_add_u64 v[244:245], s[26:27], 0, v[132:133]
	ds_read_b128 v[182:185], v148 offset:32768
	ds_read_b128 v[186:189], v148 offset:33792
	ds_read_b128 v[190:193], v148 offset:34816
	ds_read_b128 v[194:197], v148 offset:35840
	ds_read_b128 v[210:213], v148 offset:36864
	ds_read_b128 v[226:229], v148 offset:37888
	ds_read_b128 v[230:233], v148 offset:38912
	ds_read_b128 v[234:237], v148 offset:39936
	s_mov_b32 m0, s17
	s_nop 0
	global_load_lds_dwordx4 v[240:241], off
	s_mov_b32 m0, s35
	s_nop 0
	global_load_lds_dwordx4 v[242:243], off
	s_mov_b32 m0, s37
	s_nop 0
	global_load_lds_dwordx4 v[244:245], off
	v_lshl_add_u64 v[244:245], s[26:27], 0, v[136:137]
	s_mov_b32 m0, s38
	s_nop 0
	global_load_lds_dwordx4 v[244:245], off
	s_waitcnt vmcnt(8)
	s_waitcnt lgkmcnt(0)
	s_barrier
	s_setprio 1
	s_waitcnt lgkmcnt(0)
	v_mfma_f32_16x16x32_bf16 v[128:131], v[150:153], v[182:185], v[128:131]
	v_mfma_f32_16x16x32_bf16 v[124:127], v[158:161], v[182:185], v[124:127]
	v_mfma_f32_16x16x32_bf16 v[120:123], v[150:153], v[190:193], v[120:123]
	v_mfma_f32_16x16x32_bf16 v[112:115], v[158:161], v[190:193], v[112:115]
	v_mfma_f32_16x16x32_bf16 v[104:107], v[150:153], v[210:213], v[104:107]
	v_mfma_f32_16x16x32_bf16 v[96:99], v[158:161], v[210:213], v[96:99]
	v_mfma_f32_16x16x32_bf16 v[88:91], v[150:153], v[230:233], v[88:91]
	v_mfma_f32_16x16x32_bf16 v[80:83], v[158:161], v[230:233], v[80:83]
	v_mfma_f32_16x16x32_bf16 v[128:131], v[154:157], v[186:189], v[128:131]
	v_mfma_f32_16x16x32_bf16 v[124:127], v[162:165], v[186:189], v[124:127]
	v_mfma_f32_16x16x32_bf16 v[120:123], v[154:157], v[194:197], v[120:123]
	v_mfma_f32_16x16x32_bf16 v[112:115], v[162:165], v[194:197], v[112:115]
	v_mfma_f32_16x16x32_bf16 v[104:107], v[154:157], v[226:229], v[104:107]
	v_mfma_f32_16x16x32_bf16 v[96:99], v[162:165], v[226:229], v[96:99]
	v_mfma_f32_16x16x32_bf16 v[88:91], v[154:157], v[234:237], v[88:91]
	v_mfma_f32_16x16x32_bf16 v[80:83], v[162:165], v[234:237], v[80:83]
	s_setprio 0
	s_setprio 1
	v_mfma_f32_16x16x32_bf16 v[116:119], v[166:169], v[182:185], v[116:119]
	v_mfma_f32_16x16x32_bf16 v[108:111], v[174:177], v[182:185], v[108:111]
	v_mfma_f32_16x16x32_bf16 v[100:103], v[166:169], v[190:193], v[100:103]
	v_mfma_f32_16x16x32_bf16 v[92:95], v[174:177], v[190:193], v[92:95]
	v_mfma_f32_16x16x32_bf16 v[84:87], v[166:169], v[210:213], v[84:87]
	v_mfma_f32_16x16x32_bf16 v[76:79], v[174:177], v[210:213], v[76:79]
	v_mfma_f32_16x16x32_bf16 v[72:75], v[166:169], v[230:233], v[72:75]
	v_mfma_f32_16x16x32_bf16 v[68:71], v[174:177], v[230:233], v[68:71]
	v_mfma_f32_16x16x32_bf16 v[116:119], v[170:173], v[186:189], v[116:119]
	v_mfma_f32_16x16x32_bf16 v[108:111], v[178:181], v[186:189], v[108:111]
	v_mfma_f32_16x16x32_bf16 v[100:103], v[170:173], v[194:197], v[100:103]
	v_mfma_f32_16x16x32_bf16 v[92:95], v[178:181], v[194:197], v[92:95]
	v_mfma_f32_16x16x32_bf16 v[84:87], v[170:173], v[226:229], v[84:87]
	v_mfma_f32_16x16x32_bf16 v[76:79], v[178:181], v[226:229], v[76:79]
	v_mfma_f32_16x16x32_bf16 v[72:75], v[170:173], v[234:237], v[72:75]
	s_barrier
; #define PG8_STAGE(bufoff, gbase, voff) do { _Pragma("unroll") for (int _i = 0; _i < 2; ++_i) \
;         __builtin_amdgcn_global_load_lds((const unsigned*)((const char*)(gbase) + (voff)[_i]), (PG8_LAS unsigned*)(lds + (bufoff) + ldsw + _i * 8192), 16, 0, 0); } while (0)
; #define PG8_LDA(dst, b, h) do { _Pragma("unroll") for (int m = 0; m < 4; ++m) _Pragma("unroll") for (int k = 0; k < 2; ++k) dst[m][k] = *(const PG8_LAS bf16x8*)(lds + PG8_SA(b, h) + aoff + m * 2048 + k * 1024); } while (0)
; #define PG8_MMA(ai, bj, At, Bt) do { __builtin_amdgcn_s_setprio(1); _Pragma("unroll") for (int m = 0; m < 4; ++m) _Pragma("unroll") for (int n = 0; n < 2; ++n) _Pragma("unroll") for (int k = 0; k < 2; ++k) \
;         acc[ai][bj][m][n] = __builtin_amdgcn_mfma_f32_16x16x32_bf16(Bt[n][k], At[m][k], acc[ai][bj][m][n], 0, 0, 0); __builtin_amdgcn_s_setprio(0); } while (0)
; #define PG8_WAIT_V(n) asm volatile("s_waitcnt vmcnt(" #n ")" ::: "memory")
; #define PG8_WAIT_L(n) asm volatile("s_waitcnt lgkmcnt(" #n ")" ::: "memory")
; #define PG8_BAR __builtin_amdgcn_s_barrier()
; #define PG8_SCHED __builtin_amdgcn_sched_barrier(0)
; template <class Epi, class Sched, bool ALIGN_EPI = false, bool SP2 = false>
; __device__ __forceinline__ void gemm_phase(PG8_LAS unsigned char* lds, const Gemm g, const Sched& S, const Epi& E) {
;     ...
;             PG8_WAIT_V(8); PG8_WAIT_L(0); PG8_BAR; PG8_MMA(0, 0, At, B0); PG8_MMA(0, 1, At, B1); PG8_BAR; PG8_SCHED;
;             PG8_LDA(At, 1, 1); PG8_STAGE(PG8_SB(1, 0), b3, voffB); PG8_STAGE(PG8_SB(1, 1), b3 + hstepB, voffB); PG8_STAGE(PG8_SA(1, 0), a3, voffA);
;             PG8_WAIT_V(8); PG8_WAIT_L(0); PG8_BAR; PG8_MMA(1, 0, At, B0); PG8_MMA(1, 1, At, B1); PG8_BAR; PG8_SCHED;
;     ...
;         if constexpr (ALIGN_EPI) { if (wr == 0) PG8_BAR; }
	v_mfma_f32_16x16x32_bf16 v[68:71], v[178:181], v[234:237], v[68:71]
	s_setprio 0
	s_add_i32 s26, s49, s34
	v_lshl_add_u64 v[144:145], v[144:145], 0, s[64:65]
	s_mov_b32 m0, s26
	ds_read_b128 v[182:185], v148 offset:49152
	ds_read_b128 v[186:189], v148 offset:50176
	ds_read_b128 v[190:193], v148 offset:51200
	ds_read_b128 v[194:197], v148 offset:52224
	ds_read_b128 v[210:213], v148 offset:53248
	ds_read_b128 v[226:229], v148 offset:54272
	ds_read_b128 v[230:233], v148 offset:55296
	ds_read_b128 v[234:237], v148 offset:56320
	global_load_lds_dwordx4 v[144:145], off
	s_add_i32 m0, s26, 0x2000
	s_add_u32 s24, s24, 0x40080
	v_lshl_add_u64 v[144:145], v[238:239], 0, s[64:65]
	s_addc_u32 s25, s25, 0
	s_add_i32 s26, s50, s34
	global_load_lds_dwordx4 v[144:145], off
	v_lshl_add_u64 v[144:145], s[24:25], 0, v[134:135]
	s_mov_b32 m0, s26
	s_nop 0
	global_load_lds_dwordx4 v[144:145], off
	v_lshl_add_u64 v[144:145], s[24:25], 0, v[138:139]
	s_add_i32 m0, s26, 0x2000
	s_nop 0
	global_load_lds_dwordx4 v[144:145], off
	s_waitcnt vmcnt(6)
	s_waitcnt lgkmcnt(0)
	s_barrier
	s_setprio 1
	s_waitcnt lgkmcnt(0)
	v_mfma_f32_16x16x32_bf16 v[64:67], v[150:153], v[182:185], v[64:67]
	v_mfma_f32_16x16x32_bf16 v[60:63], v[158:161], v[182:185], v[60:63]
	v_mfma_f32_16x16x32_bf16 v[56:59], v[150:153], v[190:193], v[56:59]
	v_mfma_f32_16x16x32_bf16 v[48:51], v[158:161], v[190:193], v[48:51]
	v_mfma_f32_16x16x32_bf16 v[40:43], v[150:153], v[210:213], v[40:43]
	v_mfma_f32_16x16x32_bf16 v[32:35], v[158:161], v[210:213], v[32:35]
	v_mfma_f32_16x16x32_bf16 v[24:27], v[150:153], v[230:233], v[24:27]
	v_mfma_f32_16x16x32_bf16 v[16:19], v[158:161], v[230:233], v[16:19]
	v_mfma_f32_16x16x32_bf16 v[64:67], v[154:157], v[186:189], v[64:67]
	v_mfma_f32_16x16x32_bf16 v[60:63], v[162:165], v[186:189], v[60:63]
	v_mfma_f32_16x16x32_bf16 v[56:59], v[154:157], v[194:197], v[56:59]
	v_mfma_f32_16x16x32_bf16 v[48:51], v[162:165], v[194:197], v[48:51]
	v_mfma_f32_16x16x32_bf16 v[40:43], v[154:157], v[226:229], v[40:43]
	v_mfma_f32_16x16x32_bf16 v[32:35], v[162:165], v[226:229], v[32:35]
	v_mfma_f32_16x16x32_bf16 v[24:27], v[154:157], v[234:237], v[24:27]
	v_mfma_f32_16x16x32_bf16 v[16:19], v[162:165], v[234:237], v[16:19]
	s_setprio 0
	s_setprio 1
	v_mfma_f32_16x16x32_bf16 v[52:55], v[166:169], v[182:185], v[52:55]
	v_mfma_f32_16x16x32_bf16 v[44:47], v[174:177], v[182:185], v[44:47]
	v_mfma_f32_16x16x32_bf16 v[36:39], v[166:169], v[190:193], v[36:39]
	v_mfma_f32_16x16x32_bf16 v[28:31], v[174:177], v[190:193], v[28:31]
	v_mfma_f32_16x16x32_bf16 v[20:23], v[166:169], v[210:213], v[20:23]
	v_mfma_f32_16x16x32_bf16 v[12:15], v[174:177], v[210:213], v[12:15]
	v_mfma_f32_16x16x32_bf16 v[8:11], v[166:169], v[230:233], v[8:11]
	v_mfma_f32_16x16x32_bf16 v[4:7], v[174:177], v[230:233], v[4:7]
	v_mfma_f32_16x16x32_bf16 v[52:55], v[170:173], v[186:189], v[52:55]
	v_mfma_f32_16x16x32_bf16 v[44:47], v[178:181], v[186:189], v[44:47]
	v_mfma_f32_16x16x32_bf16 v[36:39], v[170:173], v[194:197], v[36:39]
	v_mfma_f32_16x16x32_bf16 v[28:31], v[178:181], v[194:197], v[28:31]
	v_mfma_f32_16x16x32_bf16 v[20:23], v[170:173], v[226:229], v[20:23]
	v_mfma_f32_16x16x32_bf16 v[12:15], v[178:181], v[226:229], v[12:15]
	v_mfma_f32_16x16x32_bf16 v[8:11], v[170:173], v[234:237], v[8:11]
	s_barrier
	v_mfma_f32_16x16x32_bf16 v[4:7], v[178:181], v[234:237], v[4:7]
	s_setprio 0
	s_add_i32 s48, s48, 2
	s_add_u32 s46, s46, 0x100
	s_addc_u32 s47, s47, 0
	s_add_u32 s22, s22, 0x100
	s_addc_u32 s23, s23, 0
	s_cmp_gt_u32 s48, 13
	s_cbranch_scc0 .LBB0_1093
	s_and_b64 vcc, exec, s[10:11]
	s_cbranch_vccz .LBB0_1096
	s_barrier

; #define PG8_STAGE(bufoff, gbase, voff) do { _Pragma("unroll") for (int _i = 0; _i < 2; ++_i) \
;         __builtin_amdgcn_global_load_lds((const unsigned*)((const char*)(gbase) + (voff)[_i]), (PG8_LAS unsigned*)(lds + (bufoff) + ldsw + _i * 8192), 16, 0, 0); } while (0)
; #define PG8_LDA(dst, b, h) do { _Pragma("unroll") for (int m = 0; m < 4; ++m) _Pragma("unroll") for (int k = 0; k < 2; ++k) dst[m][k] = *(const PG8_LAS bf16x8*)(lds + PG8_SA(b, h) + aoff + m * 2048 + k * 1024); } while (0)
; #define PG8_LDB(dst, b, h) do { _Pragma("unroll") for (int n = 0; n < 2; ++n) _Pragma("unroll") for (int k = 0; k < 2; ++k) dst[n][k] = *(const PG8_LAS bf16x8*)(lds + PG8_SB(b, h) + boff + n * 2048 + k * 1024); } while (0)
; #define PG8_MMA(ai, bj, At, Bt) do { __builtin_amdgcn_s_setprio(1); _Pragma("unroll") for (int m = 0; m < 4; ++m) _Pragma("unroll") for (int n = 0; n < 2; ++n) _Pragma("unroll") for (int k = 0; k < 2; ++k) \
;         acc[ai][bj][m][n] = __builtin_amdgcn_mfma_f32_16x16x32_bf16(Bt[n][k], At[m][k], acc[ai][bj][m][n], 0, 0, 0); __builtin_amdgcn_s_setprio(0); } while (0)
; #define PG8_WAIT_V(n) asm volatile("s_waitcnt vmcnt(" #n ")" ::: "memory")
; #define PG8_WAIT_L(n) asm volatile("s_waitcnt lgkmcnt(" #n ")" ::: "memory")
; template <class Epi, class Sched, bool ALIGN_EPI = false, bool SP2 = false>
; __device__ __forceinline__ void gemm_phase(PG8_LAS unsigned char* lds, const Gemm g, const Sched& S, const Epi& E) {
;     ...
;             const bool last = (t == nt - 2);
;             const char* a1 = cA + (size_t)(t + 1) * kstep;
;             const char* a2 = last ? nA : cA + (size_t)(t + 2) * kstep; const char* b2 = last ? nB : cB + (size_t)(t + 2) * kstep;
;             const char* a3 = a2 + kstep; const char* b3 = b2 + kstep;
;             if (last && has_next) S.a_ready(nxt);
;             if constexpr (SP2) {
;             PG8_LDB(B0, 0, 0); PG8_LDB(B1, 0, 1); PG8_SCHED; PG8_LDA(At, 0, 0); PG8_STAGE(PG8_SA(1, 1), a1 + hstepA, voffA);
;             PG8_WAIT_V(8); PG8_WAIT_L(0); PG8_BAR; PG8_MMA(0, 0, At, B0); PG8_MMA(0, 1, At, B1); PG8_BAR; PG8_SCHED;
;             PG8_LDA(At, 0, 1); PG8_STAGE(PG8_SB(0, 0), b2, voffB); PG8_STAGE(PG8_SB(0, 1), b2 + hstepB, voffB); PG8_STAGE(PG8_SA(0, 0), a2, voffA);
;             PG8_WAIT_V(8); PG8_WAIT_L(0); PG8_BAR; PG8_MMA(1, 0, At, B0); PG8_MMA(1, 1, At, B1); PG8_BAR; PG8_SCHED;
.LBB0_1161:
	s_add_u32 s24, s22, 0xfffc0080
	s_addc_u32 s25, s23, -1
	s_add_i32 s49, 0, 0x10000
	s_cmp_eq_u32 s48, 12
	s_cselect_b32 s27, s19, s25
	s_cselect_b32 s26, s21, s24
	v_add_u32_e32 v149, s49, v154
	s_cselect_b32 s25, s44, s47
	s_cselect_b32 s24, s45, s46
	s_add_i32 s52, 0, 0x14000
	ds_read_b128 v[150:153], v149
	ds_read_b128 v[156:159], v149 offset:1024
	ds_read_b128 v[160:163], v149 offset:2048
	ds_read_b128 v[164:167], v149 offset:3072
	v_add_u32_e32 v149, s52, v154
	ds_read_b128 v[168:171], v149
	ds_read_b128 v[172:175], v149 offset:1024
	ds_read_b128 v[176:179], v149 offset:2048
	ds_read_b128 v[180:183], v149 offset:3072
	v_lshl_add_u64 v[196:197], s[22:23], 0, v[146:147]
	s_add_i32 m0, s31, 0xc000
	ds_read_b128 v[184:187], v155
	ds_read_b128 v[188:191], v155 offset:1024
	ds_read_b128 v[192:195], v155 offset:2048
	ds_read_b128 v[210:213], v155 offset:3072
	ds_read_b128 v[226:229], v155 offset:4096
	ds_read_b128 v[230:233], v155 offset:5120
	ds_read_b128 v[234:237], v155 offset:6144
	ds_read_b128 v[238:241], v155 offset:7168
	v_lshl_add_u64 v[248:249], v[244:245], 0, s[64:65]
	s_mov_b32 m0, s38
	s_nop 0
	global_load_lds_dwordx4 v[248:249], off
	v_lshl_add_u64 v[248:249], v[246:247], 0, s[64:65]
	s_mov_b32 m0, s39
	s_nop 0
	global_load_lds_dwordx4 v[248:249], off
	s_add_i32 m0, s31, 0xc000
	s_nop 0
	global_load_lds_dwordx4 v[196:197], off
	v_lshl_add_u64 v[196:197], s[22:23], 0, v[144:145]
	s_add_i32 m0, s31, 0xe000
	s_nop 0
	global_load_lds_dwordx4 v[196:197], off
	s_waitcnt vmcnt(8)
	s_waitcnt lgkmcnt(0)
	s_barrier
	s_setprio 1
	s_waitcnt lgkmcnt(0)
	v_mfma_f32_16x16x32_bf16 v[128:131], v[150:153], v[184:187], v[128:131]
	v_mfma_f32_16x16x32_bf16 v[124:127], v[160:163], v[184:187], v[124:127]
	v_mfma_f32_16x16x32_bf16 v[112:115], v[150:153], v[192:195], v[112:115]
	v_mfma_f32_16x16x32_bf16 v[108:111], v[160:163], v[192:195], v[108:111]
	v_mfma_f32_16x16x32_bf16 v[96:99], v[150:153], v[226:229], v[96:99]
	v_mfma_f32_16x16x32_bf16 v[92:95], v[160:163], v[226:229], v[92:95]
	v_mfma_f32_16x16x32_bf16 v[80:83], v[150:153], v[234:237], v[80:83]
	v_mfma_f32_16x16x32_bf16 v[76:79], v[160:163], v[234:237], v[76:79]
	v_mfma_f32_16x16x32_bf16 v[128:131], v[156:159], v[188:191], v[128:131]
	v_mfma_f32_16x16x32_bf16 v[124:127], v[164:167], v[188:191], v[124:127]
	v_mfma_f32_16x16x32_bf16 v[112:115], v[156:159], v[210:213], v[112:115]
	v_mfma_f32_16x16x32_bf16 v[108:111], v[164:167], v[210:213], v[108:111]
	v_mfma_f32_16x16x32_bf16 v[96:99], v[156:159], v[230:233], v[96:99]
	v_mfma_f32_16x16x32_bf16 v[92:95], v[164:167], v[230:233], v[92:95]
	v_mfma_f32_16x16x32_bf16 v[80:83], v[156:159], v[238:241], v[80:83]
	v_mfma_f32_16x16x32_bf16 v[76:79], v[164:167], v[238:241], v[76:79]
	s_setprio 0
	s_setprio 1
	v_mfma_f32_16x16x32_bf16 v[120:123], v[168:171], v[184:187], v[120:123]
	v_mfma_f32_16x16x32_bf16 v[116:119], v[176:179], v[184:187], v[116:119]
	v_mfma_f32_16x16x32_bf16 v[104:107], v[168:171], v[192:195], v[104:107]
	v_mfma_f32_16x16x32_bf16 v[100:103], v[176:179], v[192:195], v[100:103]
	v_mfma_f32_16x16x32_bf16 v[88:91], v[168:171], v[226:229], v[88:91]
	v_mfma_f32_16x16x32_bf16 v[84:87], v[176:179], v[226:229], v[84:87]
	v_mfma_f32_16x16x32_bf16 v[72:75], v[168:171], v[234:237], v[72:75]
	v_mfma_f32_16x16x32_bf16 v[68:71], v[176:179], v[234:237], v[68:71]
	v_mfma_f32_16x16x32_bf16 v[120:123], v[172:175], v[188:191], v[120:123]
	v_mfma_f32_16x16x32_bf16 v[116:119], v[180:183], v[188:191], v[116:119]
	v_mfma_f32_16x16x32_bf16 v[104:107], v[172:175], v[210:213], v[104:107]
	v_mfma_f32_16x16x32_bf16 v[100:103], v[180:183], v[210:213], v[100:103]
	v_mfma_f32_16x16x32_bf16 v[88:91], v[172:175], v[230:233], v[88:91]
	v_mfma_f32_16x16x32_bf16 v[84:87], v[180:183], v[230:233], v[84:87]
	v_mfma_f32_16x16x32_bf16 v[72:75], v[172:175], v[238:241], v[72:75]
	s_barrier
	v_mfma_f32_16x16x32_bf16 v[68:71], v[180:183], v[238:241], v[68:71]
	s_setprio 0
	s_add_i32 s49, s49, s30
	v_lshl_add_u64 v[196:197], s[24:25], 0, v[134:135]
	s_mov_b32 m0, s49
	ds_read_b128 v[184:187], v155 offset:16384
	ds_read_b128 v[188:191], v155 offset:17408
	ds_read_b128 v[192:195], v155 offset:18432
	ds_read_b128 v[210:213], v155 offset:19456
	ds_read_b128 v[226:229], v155 offset:20480
	ds_read_b128 v[230:233], v155 offset:21504
	ds_read_b128 v[234:237], v155 offset:22528
	ds_read_b128 v[238:241], v155 offset:23552
	global_load_lds_dwordx4 v[196:197], off
	s_add_i32 m0, s49, 0x2000
	s_add_u32 s50, s24, 0x40000
	v_lshl_add_u64 v[242:243], s[24:25], 0, v[138:139]
	s_addc_u32 s51, s25, 0
	s_add_i32 s49, s52, s30
	global_load_lds_dwordx4 v[242:243], off
	v_lshl_add_u64 v[244:245], s[50:51], 0, v[134:135]
	s_mov_b32 m0, s49
	v_lshl_add_u64 v[246:247], s[26:27], 0, v[136:137]
	global_load_lds_dwordx4 v[244:245], off
	v_lshl_add_u64 v[244:245], s[50:51], 0, v[138:139]
	s_add_i32 m0, s49, 0x2000
	s_nop 0
	global_load_lds_dwordx4 v[244:245], off
	v_lshl_add_u64 v[244:245], s[26:27], 0, v[132:133]
	s_waitcnt vmcnt(6)
	s_waitcnt lgkmcnt(0)
	s_barrier
; #define PG8_STAGE(bufoff, gbase, voff) do { _Pragma("unroll") for (int _i = 0; _i < 2; ++_i) \
;         __builtin_amdgcn_global_load_lds((const unsigned*)((const char*)(gbase) + (voff)[_i]), (PG8_LAS unsigned*)(lds + (bufoff) + ldsw + _i * 8192), 16, 0, 0); } while (0)
; #define PG8_LDA(dst, b, h) do { _Pragma("unroll") for (int m = 0; m < 4; ++m) _Pragma("unroll") for (int k = 0; k < 2; ++k) dst[m][k] = *(const PG8_LAS bf16x8*)(lds + PG8_SA(b, h) + aoff + m * 2048 + k * 1024); } while (0)
; #define PG8_LDB(dst, b, h) do { _Pragma("unroll") for (int n = 0; n < 2; ++n) _Pragma("unroll") for (int k = 0; k < 2; ++k) dst[n][k] = *(const PG8_LAS bf16x8*)(lds + PG8_SB(b, h) + boff + n * 2048 + k * 1024); } while (0)
; #define PG8_MMA(ai, bj, At, Bt) do { __builtin_amdgcn_s_setprio(1); _Pragma("unroll") for (int m = 0; m < 4; ++m) _Pragma("unroll") for (int n = 0; n < 2; ++n) _Pragma("unroll") for (int k = 0; k < 2; ++k) \
;         acc[ai][bj][m][n] = __builtin_amdgcn_mfma_f32_16x16x32_bf16(Bt[n][k], At[m][k], acc[ai][bj][m][n], 0, 0, 0); __builtin_amdgcn_s_setprio(0); } while (0)
; #define PG8_WAIT_V(n) asm volatile("s_waitcnt vmcnt(" #n ")" ::: "memory")
; #define PG8_WAIT_L(n) asm volatile("s_waitcnt lgkmcnt(" #n ")" ::: "memory")
; #define PG8_BAR __builtin_amdgcn_s_barrier()
; #define PG8_SCHED __builtin_amdgcn_sched_barrier(0)
; template <class Epi, class Sched, bool ALIGN_EPI = false, bool SP2 = false>
; __device__ __forceinline__ void gemm_phase(PG8_LAS unsigned char* lds, const Gemm g, const Sched& S, const Epi& E) {
;     ...
;             PG8_WAIT_V(8); PG8_WAIT_L(0); PG8_BAR; PG8_MMA(1, 0, At, B0); PG8_MMA(1, 1, At, B1); PG8_BAR; PG8_SCHED;
;             PG8_LDB(B0, 1, 0); PG8_LDB(B1, 1, 1); PG8_SCHED; PG8_LDA(At, 1, 0); PG8_STAGE(PG8_SA(0, 1), a2 + hstepA, voffA);
;             PG8_WAIT_V(8); PG8_WAIT_L(0); PG8_BAR; PG8_MMA(0, 0, At, B0); PG8_MMA(0, 1, At, B1); PG8_BAR; PG8_SCHED;
;             PG8_LDA(At, 1, 1); PG8_STAGE(PG8_SB(1, 0), b3, voffB); PG8_STAGE(PG8_SB(1, 1), b3 + hstepB, voffB); PG8_STAGE(PG8_SA(1, 0), a3, voffA);
	s_setprio 1
	s_waitcnt lgkmcnt(0)
	v_mfma_f32_16x16x32_bf16 v[64:67], v[150:153], v[184:187], v[64:67]
	v_mfma_f32_16x16x32_bf16 v[60:63], v[160:163], v[184:187], v[60:63]
	v_mfma_f32_16x16x32_bf16 v[52:55], v[150:153], v[192:195], v[52:55]
	v_mfma_f32_16x16x32_bf16 v[44:47], v[160:163], v[192:195], v[44:47]
	v_mfma_f32_16x16x32_bf16 v[36:39], v[150:153], v[226:229], v[36:39]
	v_mfma_f32_16x16x32_bf16 v[28:31], v[160:163], v[226:229], v[28:31]
	v_mfma_f32_16x16x32_bf16 v[20:23], v[150:153], v[234:237], v[20:23]
	v_mfma_f32_16x16x32_bf16 v[12:15], v[160:163], v[234:237], v[12:15]
	v_mfma_f32_16x16x32_bf16 v[64:67], v[156:159], v[188:191], v[64:67]
	v_mfma_f32_16x16x32_bf16 v[60:63], v[164:167], v[188:191], v[60:63]
	v_mfma_f32_16x16x32_bf16 v[52:55], v[156:159], v[210:213], v[52:55]
	v_mfma_f32_16x16x32_bf16 v[44:47], v[164:167], v[210:213], v[44:47]
	v_mfma_f32_16x16x32_bf16 v[36:39], v[156:159], v[230:233], v[36:39]
	v_mfma_f32_16x16x32_bf16 v[28:31], v[164:167], v[230:233], v[28:31]
	v_mfma_f32_16x16x32_bf16 v[20:23], v[156:159], v[238:241], v[20:23]
	v_mfma_f32_16x16x32_bf16 v[12:15], v[164:167], v[238:241], v[12:15]
	s_setprio 0
	s_setprio 1
	v_mfma_f32_16x16x32_bf16 v[56:59], v[168:171], v[184:187], v[56:59]
	v_mfma_f32_16x16x32_bf16 v[48:51], v[176:179], v[184:187], v[48:51]
	v_mfma_f32_16x16x32_bf16 v[40:43], v[168:171], v[192:195], v[40:43]
	v_mfma_f32_16x16x32_bf16 v[32:35], v[176:179], v[192:195], v[32:35]
	v_mfma_f32_16x16x32_bf16 v[24:27], v[168:171], v[226:229], v[24:27]
	v_mfma_f32_16x16x32_bf16 v[16:19], v[176:179], v[226:229], v[16:19]
	v_mfma_f32_16x16x32_bf16 v[8:11], v[168:171], v[234:237], v[8:11]
	v_mfma_f32_16x16x32_bf16 v[4:7], v[176:179], v[234:237], v[4:7]
	v_mfma_f32_16x16x32_bf16 v[56:59], v[172:175], v[188:191], v[56:59]
	v_mfma_f32_16x16x32_bf16 v[48:51], v[180:183], v[188:191], v[48:51]
	v_mfma_f32_16x16x32_bf16 v[40:43], v[172:175], v[210:213], v[40:43]
	v_mfma_f32_16x16x32_bf16 v[32:35], v[180:183], v[210:213], v[32:35]
	v_mfma_f32_16x16x32_bf16 v[24:27], v[172:175], v[230:233], v[24:27]
	v_mfma_f32_16x16x32_bf16 v[16:19], v[180:183], v[230:233], v[16:19]
	v_mfma_f32_16x16x32_bf16 v[8:11], v[172:175], v[238:241], v[8:11]
	s_barrier
	v_mfma_f32_16x16x32_bf16 v[4:7], v[180:183], v[238:241], v[4:7]
	s_setprio 0
	s_add_i32 s49, 0, 0x18000
	v_add_u32_e32 v149, s49, v154
	s_add_i32 s50, 0, 0x1c000
	ds_read_b128 v[150:153], v149
	ds_read_b128 v[156:159], v149 offset:1024
	ds_read_b128 v[160:163], v149 offset:2048
	ds_read_b128 v[164:167], v149 offset:3072
	v_add_u32_e32 v149, s50, v154
	ds_read_b128 v[168:171], v149
	ds_read_b128 v[172:175], v149 offset:1024
	ds_read_b128 v[176:179], v149 offset:2048
	ds_read_b128 v[180:183], v149 offset:3072
	s_add_u32 s26, s26, 0x40000
	s_addc_u32 s27, s27, 0
	s_mov_b32 m0, s34
	v_lshl_add_u64 v[248:249], s[26:27], 0, v[132:133]
	ds_read_b128 v[184:187], v155 offset:32768
	ds_read_b128 v[188:191], v155 offset:33792
	ds_read_b128 v[192:195], v155 offset:34816
	ds_read_b128 v[210:213], v155 offset:35840
	ds_read_b128 v[226:229], v155 offset:36864
	ds_read_b128 v[230:233], v155 offset:37888
	ds_read_b128 v[234:237], v155 offset:38912
	ds_read_b128 v[238:241], v155 offset:39936
	s_mov_b32 m0, s31
	s_nop 0
	global_load_lds_dwordx4 v[244:245], off
	s_mov_b32 m0, s33
	s_nop 0
	global_load_lds_dwordx4 v[246:247], off
	s_mov_b32 m0, s34
	s_nop 0
	global_load_lds_dwordx4 v[248:249], off
	v_lshl_add_u64 v[248:249], s[26:27], 0, v[136:137]
	s_mov_b32 m0, s35
	s_nop 0
	global_load_lds_dwordx4 v[248:249], off
	s_waitcnt vmcnt(8)
	s_waitcnt lgkmcnt(0)
	s_barrier
	s_setprio 1
	s_waitcnt lgkmcnt(0)
	v_mfma_f32_16x16x32_bf16 v[128:131], v[150:153], v[184:187], v[128:131]
	v_mfma_f32_16x16x32_bf16 v[124:127], v[160:163], v[184:187], v[124:127]
	v_mfma_f32_16x16x32_bf16 v[112:115], v[150:153], v[192:195], v[112:115]
	v_mfma_f32_16x16x32_bf16 v[108:111], v[160:163], v[192:195], v[108:111]
	v_mfma_f32_16x16x32_bf16 v[96:99], v[150:153], v[226:229], v[96:99]
	v_mfma_f32_16x16x32_bf16 v[92:95], v[160:163], v[226:229], v[92:95]
	v_mfma_f32_16x16x32_bf16 v[80:83], v[150:153], v[234:237], v[80:83]
	v_mfma_f32_16x16x32_bf16 v[76:79], v[160:163], v[234:237], v[76:79]
	v_mfma_f32_16x16x32_bf16 v[128:131], v[156:159], v[188:191], v[128:131]
	v_mfma_f32_16x16x32_bf16 v[124:127], v[164:167], v[188:191], v[124:127]
	v_mfma_f32_16x16x32_bf16 v[112:115], v[156:159], v[210:213], v[112:115]
	v_mfma_f32_16x16x32_bf16 v[108:111], v[164:167], v[210:213], v[108:111]
	v_mfma_f32_16x16x32_bf16 v[96:99], v[156:159], v[230:233], v[96:99]
	v_mfma_f32_16x16x32_bf16 v[92:95], v[164:167], v[230:233], v[92:95]
	v_mfma_f32_16x16x32_bf16 v[80:83], v[156:159], v[238:241], v[80:83]
	v_mfma_f32_16x16x32_bf16 v[76:79], v[164:167], v[238:241], v[76:79]
	s_setprio 0
	s_setprio 1
	v_mfma_f32_16x16x32_bf16 v[120:123], v[168:171], v[184:187], v[120:123]
	v_mfma_f32_16x16x32_bf16 v[116:119], v[176:179], v[184:187], v[116:119]
	v_mfma_f32_16x16x32_bf16 v[104:107], v[168:171], v[192:195], v[104:107]
	v_mfma_f32_16x16x32_bf16 v[100:103], v[176:179], v[192:195], v[100:103]
	v_mfma_f32_16x16x32_bf16 v[88:91], v[168:171], v[226:229], v[88:91]
	v_mfma_f32_16x16x32_bf16 v[84:87], v[176:179], v[226:229], v[84:87]
	v_mfma_f32_16x16x32_bf16 v[72:75], v[168:171], v[234:237], v[72:75]
	v_mfma_f32_16x16x32_bf16 v[68:71], v[176:179], v[234:237], v[68:71]
	v_mfma_f32_16x16x32_bf16 v[120:123], v[172:175], v[188:191], v[120:123]
	v_mfma_f32_16x16x32_bf16 v[116:119], v[180:183], v[188:191], v[116:119]
	v_mfma_f32_16x16x32_bf16 v[104:107], v[172:175], v[210:213], v[104:107]
	v_mfma_f32_16x16x32_bf16 v[100:103], v[180:183], v[210:213], v[100:103]
	v_mfma_f32_16x16x32_bf16 v[88:91], v[172:175], v[230:233], v[88:91]
	v_mfma_f32_16x16x32_bf16 v[84:87], v[180:183], v[230:233], v[84:87]
	v_mfma_f32_16x16x32_bf16 v[72:75], v[172:175], v[238:241], v[72:75]
	s_barrier
; #define PG8_STAGE(bufoff, gbase, voff) do { _Pragma("unroll") for (int _i = 0; _i < 2; ++_i) \
;         __builtin_amdgcn_global_load_lds((const unsigned*)((const char*)(gbase) + (voff)[_i]), (PG8_LAS unsigned*)(lds + (bufoff) + ldsw + _i * 8192), 16, 0, 0); } while (0)
; #define PG8_LDA(dst, b, h) do { _Pragma("unroll") for (int m = 0; m < 4; ++m) _Pragma("unroll") for (int k = 0; k < 2; ++k) dst[m][k] = *(const PG8_LAS bf16x8*)(lds + PG8_SA(b, h) + aoff + m * 2048 + k * 1024); } while (0)
; #define PG8_MMA(ai, bj, At, Bt) do { __builtin_amdgcn_s_setprio(1); _Pragma("unroll") for (int m = 0; m < 4; ++m) _Pragma("unroll") for (int n = 0; n < 2; ++n) _Pragma("unroll") for (int k = 0; k < 2; ++k) \
;         acc[ai][bj][m][n] = __builtin_amdgcn_mfma_f32_16x16x32_bf16(Bt[n][k], At[m][k], acc[ai][bj][m][n], 0, 0, 0); __builtin_amdgcn_s_setprio(0); } while (0)
; #define PG8_WAIT_V(n) asm volatile("s_waitcnt vmcnt(" #n ")" ::: "memory")
; #define PG8_WAIT_L(n) asm volatile("s_waitcnt lgkmcnt(" #n ")" ::: "memory")
; #define PG8_BAR __builtin_amdgcn_s_barrier()
; #define PG8_SCHED __builtin_amdgcn_sched_barrier(0)
; template <class Epi, class Sched, bool ALIGN_EPI = false, bool SP2 = false>
; __device__ __forceinline__ void gemm_phase(PG8_LAS unsigned char* lds, const Gemm g, const Sched& S, const Epi& E) {
;     ...
;             PG8_WAIT_V(8); PG8_WAIT_L(0); PG8_BAR; PG8_MMA(0, 0, At, B0); PG8_MMA(0, 1, At, B1); PG8_BAR; PG8_SCHED;
;             PG8_LDA(At, 1, 1); PG8_STAGE(PG8_SB(1, 0), b3, voffB); PG8_STAGE(PG8_SB(1, 1), b3 + hstepB, voffB); PG8_STAGE(PG8_SA(1, 0), a3, voffA);
;             PG8_WAIT_V(8); PG8_WAIT_L(0); PG8_BAR; PG8_MMA(1, 0, At, B0); PG8_MMA(1, 1, At, B1); PG8_BAR; PG8_SCHED;
;     ...
;         if constexpr (ALIGN_EPI) { if (wr == 0) PG8_BAR; }
	v_mfma_f32_16x16x32_bf16 v[68:71], v[180:183], v[238:241], v[68:71]
	s_setprio 0
	s_add_i32 s26, s49, s30
	v_lshl_add_u64 v[196:197], v[196:197], 0, s[64:65]
	s_mov_b32 m0, s26
	ds_read_b128 v[184:187], v155 offset:49152
	ds_read_b128 v[188:191], v155 offset:50176
	ds_read_b128 v[192:195], v155 offset:51200
	ds_read_b128 v[210:213], v155 offset:52224
	ds_read_b128 v[226:229], v155 offset:53248
	ds_read_b128 v[230:233], v155 offset:54272
	ds_read_b128 v[234:237], v155 offset:55296
	ds_read_b128 v[238:241], v155 offset:56320
	global_load_lds_dwordx4 v[196:197], off
	s_add_i32 m0, s26, 0x2000
	s_add_u32 s24, s24, 0x40080
	v_lshl_add_u64 v[196:197], v[242:243], 0, s[64:65]
	s_addc_u32 s25, s25, 0
	s_add_i32 s26, s50, s30
	global_load_lds_dwordx4 v[196:197], off
	v_lshl_add_u64 v[196:197], s[24:25], 0, v[134:135]
	s_mov_b32 m0, s26
	s_nop 0
	global_load_lds_dwordx4 v[196:197], off
	v_lshl_add_u64 v[196:197], s[24:25], 0, v[138:139]
	s_add_i32 m0, s26, 0x2000
	s_nop 0
	global_load_lds_dwordx4 v[196:197], off
	s_waitcnt vmcnt(6)
	s_waitcnt lgkmcnt(0)
	s_barrier
	s_setprio 1
	s_waitcnt lgkmcnt(0)
	v_mfma_f32_16x16x32_bf16 v[64:67], v[150:153], v[184:187], v[64:67]
	v_mfma_f32_16x16x32_bf16 v[60:63], v[160:163], v[184:187], v[60:63]
	v_mfma_f32_16x16x32_bf16 v[52:55], v[150:153], v[192:195], v[52:55]
	v_mfma_f32_16x16x32_bf16 v[44:47], v[160:163], v[192:195], v[44:47]
	v_mfma_f32_16x16x32_bf16 v[36:39], v[150:153], v[226:229], v[36:39]
	v_mfma_f32_16x16x32_bf16 v[28:31], v[160:163], v[226:229], v[28:31]
	v_mfma_f32_16x16x32_bf16 v[20:23], v[150:153], v[234:237], v[20:23]
	v_mfma_f32_16x16x32_bf16 v[12:15], v[160:163], v[234:237], v[12:15]
	v_mfma_f32_16x16x32_bf16 v[64:67], v[156:159], v[188:191], v[64:67]
	v_mfma_f32_16x16x32_bf16 v[60:63], v[164:167], v[188:191], v[60:63]
	v_mfma_f32_16x16x32_bf16 v[52:55], v[156:159], v[210:213], v[52:55]
	v_mfma_f32_16x16x32_bf16 v[44:47], v[164:167], v[210:213], v[44:47]
	v_mfma_f32_16x16x32_bf16 v[36:39], v[156:159], v[230:233], v[36:39]
	v_mfma_f32_16x16x32_bf16 v[28:31], v[164:167], v[230:233], v[28:31]
	v_mfma_f32_16x16x32_bf16 v[20:23], v[156:159], v[238:241], v[20:23]
	v_mfma_f32_16x16x32_bf16 v[12:15], v[164:167], v[238:241], v[12:15]
	s_setprio 0
	s_setprio 1
	v_mfma_f32_16x16x32_bf16 v[56:59], v[168:171], v[184:187], v[56:59]
	v_mfma_f32_16x16x32_bf16 v[48:51], v[176:179], v[184:187], v[48:51]
	v_mfma_f32_16x16x32_bf16 v[40:43], v[168:171], v[192:195], v[40:43]
	v_mfma_f32_16x16x32_bf16 v[32:35], v[176:179], v[192:195], v[32:35]
	v_mfma_f32_16x16x32_bf16 v[24:27], v[168:171], v[226:229], v[24:27]
	v_mfma_f32_16x16x32_bf16 v[16:19], v[176:179], v[226:229], v[16:19]
	v_mfma_f32_16x16x32_bf16 v[8:11], v[168:171], v[234:237], v[8:11]
	v_mfma_f32_16x16x32_bf16 v[4:7], v[176:179], v[234:237], v[4:7]
	v_mfma_f32_16x16x32_bf16 v[56:59], v[172:175], v[188:191], v[56:59]
	v_mfma_f32_16x16x32_bf16 v[48:51], v[180:183], v[188:191], v[48:51]
	v_mfma_f32_16x16x32_bf16 v[40:43], v[172:175], v[210:213], v[40:43]
	v_mfma_f32_16x16x32_bf16 v[32:35], v[180:183], v[210:213], v[32:35]
	v_mfma_f32_16x16x32_bf16 v[24:27], v[172:175], v[230:233], v[24:27]
	v_mfma_f32_16x16x32_bf16 v[16:19], v[180:183], v[230:233], v[16:19]
	v_mfma_f32_16x16x32_bf16 v[8:11], v[172:175], v[238:241], v[8:11]
	s_barrier
	v_mfma_f32_16x16x32_bf16 v[4:7], v[180:183], v[238:241], v[4:7]
	s_setprio 0
	s_add_i32 s48, s48, 2
	s_add_u32 s46, s46, 0x100
	s_addc_u32 s47, s47, 0
	s_add_u32 s22, s22, 0x100
	s_addc_u32 s23, s23, 0
	s_cmp_gt_u32 s48, 13
	s_cbranch_scc0 .LBB0_1161
	s_and_b64 vcc, exec, s[12:13]
	s_cbranch_vccz .LBB0_1164
	s_barrier

; #define PG8_STAGE(bufoff, gbase, voff) do { _Pragma("unroll") for (int _i = 0; _i < 2; ++_i) \
;         __builtin_amdgcn_global_load_lds((const unsigned*)((const char*)(gbase) + (voff)[_i]), (PG8_LAS unsigned*)(lds + (bufoff) + ldsw + _i * 8192), 16, 0, 0); } while (0)
; #define PG8_LDA(dst, b, h) do { _Pragma("unroll") for (int m = 0; m < 4; ++m) _Pragma("unroll") for (int k = 0; k < 2; ++k) dst[m][k] = *(const PG8_LAS bf16x8*)(lds + PG8_SA(b, h) + aoff + m * 2048 + k * 1024); } while (0)
; #define PG8_LDB(dst, b, h) do { _Pragma("unroll") for (int n = 0; n < 2; ++n) _Pragma("unroll") for (int k = 0; k < 2; ++k) dst[n][k] = *(const PG8_LAS bf16x8*)(lds + PG8_SB(b, h) + boff + n * 2048 + k * 1024); } while (0)
; #define PG8_MMA(ai, bj, At, Bt) do { __builtin_amdgcn_s_setprio(1); _Pragma("unroll") for (int m = 0; m < 4; ++m) _Pragma("unroll") for (int n = 0; n < 2; ++n) _Pragma("unroll") for (int k = 0; k < 2; ++k) \
;         acc[ai][bj][m][n] = __builtin_amdgcn_mfma_f32_16x16x32_bf16(Bt[n][k], At[m][k], acc[ai][bj][m][n], 0, 0, 0); __builtin_amdgcn_s_setprio(0); } while (0)
; #define PG8_WAIT_V(n) asm volatile("s_waitcnt vmcnt(" #n ")" ::: "memory")
; #define PG8_WAIT_L(n) asm volatile("s_waitcnt lgkmcnt(" #n ")" ::: "memory")
; template <class Epi, class Sched, bool ALIGN_EPI = false, bool SP2 = false>
; __device__ __forceinline__ void gemm_phase(PG8_LAS unsigned char* lds, const Gemm g, const Sched& S, const Epi& E) {
;     ...
;             const bool last = (t == nt - 2);
;             const char* a1 = cA + (size_t)(t + 1) * kstep;
;             const char* a2 = last ? nA : cA + (size_t)(t + 2) * kstep; const char* b2 = last ? nB : cB + (size_t)(t + 2) * kstep;
;             const char* a3 = a2 + kstep; const char* b3 = b2 + kstep;
;             if (last && has_next) S.a_ready(nxt);
;             if constexpr (SP2) {
;             PG8_LDB(B0, 0, 0); PG8_LDB(B1, 0, 1); PG8_SCHED; PG8_LDA(At, 0, 0); PG8_STAGE(PG8_SA(1, 1), a1 + hstepA, voffA);
;             PG8_WAIT_V(8); PG8_WAIT_L(0); PG8_BAR; PG8_MMA(0, 0, At, B0); PG8_MMA(0, 1, At, B1); PG8_BAR; PG8_SCHED;
;             PG8_LDA(At, 0, 1); PG8_STAGE(PG8_SB(0, 0), b2, voffB); PG8_STAGE(PG8_SB(0, 1), b2 + hstepB, voffB); PG8_STAGE(PG8_SA(0, 0), a2, voffA);
;             PG8_WAIT_V(8); PG8_WAIT_L(0); PG8_BAR; PG8_MMA(1, 0, At, B0); PG8_MMA(1, 1, At, B1); PG8_BAR; PG8_SCHED;
.LBB0_1236:
	s_add_i32 s49, s18, 2
	s_add_u32 s19, s16, 0xfffc0080
	s_addc_u32 s20, s17, -1
	s_add_i32 s50, 0, 0x10000
	s_cmp_eq_u32 s37, s18
	s_cselect_b32 s21, s43, s20
	s_cselect_b32 s20, s44, s19
	s_cselect_b32 s19, s45, s48
	s_cselect_b32 s18, s46, s47
	s_add_i32 s52, 0, 0x14000
	v_add_u32_e32 v160, s50, v146
	v_add_u32_e32 v176, s52, v146
	ds_read_b128 v[148:151], v160
	ds_read_b128 v[152:155], v160 offset:1024
	ds_read_b128 v[156:159], v160 offset:2048
	ds_read_b128 v[160:163], v160 offset:3072
	ds_read_b128 v[164:167], v176
	ds_read_b128 v[168:171], v176 offset:1024
	ds_read_b128 v[172:175], v176 offset:2048
	ds_read_b128 v[176:179], v176 offset:3072
	v_lshl_add_u64 v[196:197], s[16:17], 0, v[144:145]
	s_add_i32 m0, s28, 0xc000
	ds_read_b128 v[180:183], v147
	ds_read_b128 v[184:187], v147 offset:1024
	ds_read_b128 v[188:191], v147 offset:2048
	ds_read_b128 v[192:195], v147 offset:3072
	ds_read_b128 v[210:213], v147 offset:4096
	ds_read_b128 v[226:229], v147 offset:5120
	ds_read_b128 v[230:233], v147 offset:6144
	ds_read_b128 v[234:237], v147 offset:7168
	global_load_lds_dwordx4 v[196:197], off
	v_lshl_add_u64 v[196:197], s[16:17], 0, v[142:143]
	s_add_i32 m0, s28, 0xe000
	s_nop 0
	global_load_lds_dwordx4 v[196:197], off
	s_waitcnt vmcnt(8)
	s_waitcnt lgkmcnt(0)
	s_barrier
	s_setprio 1
	s_waitcnt lgkmcnt(0)
	v_mfma_f32_16x16x32_bf16 v[124:127], v[148:151], v[180:183], v[124:127]
	v_mfma_f32_16x16x32_bf16 v[128:131], v[156:159], v[180:183], v[128:131]
	v_mfma_f32_16x16x32_bf16 v[112:115], v[148:151], v[188:191], v[112:115]
	v_mfma_f32_16x16x32_bf16 v[108:111], v[156:159], v[188:191], v[108:111]
	v_mfma_f32_16x16x32_bf16 v[96:99], v[148:151], v[210:213], v[96:99]
	v_mfma_f32_16x16x32_bf16 v[92:95], v[156:159], v[210:213], v[92:95]
	v_mfma_f32_16x16x32_bf16 v[80:83], v[148:151], v[230:233], v[80:83]
	v_mfma_f32_16x16x32_bf16 v[76:79], v[156:159], v[230:233], v[76:79]
	v_mfma_f32_16x16x32_bf16 v[124:127], v[152:155], v[184:187], v[124:127]
	v_mfma_f32_16x16x32_bf16 v[128:131], v[160:163], v[184:187], v[128:131]
	v_mfma_f32_16x16x32_bf16 v[112:115], v[152:155], v[192:195], v[112:115]
	v_mfma_f32_16x16x32_bf16 v[108:111], v[160:163], v[192:195], v[108:111]
	v_mfma_f32_16x16x32_bf16 v[96:99], v[152:155], v[226:229], v[96:99]
	v_mfma_f32_16x16x32_bf16 v[92:95], v[160:163], v[226:229], v[92:95]
	v_mfma_f32_16x16x32_bf16 v[80:83], v[152:155], v[234:237], v[80:83]
	v_mfma_f32_16x16x32_bf16 v[76:79], v[160:163], v[234:237], v[76:79]
	s_setprio 0
	s_setprio 1
	v_mfma_f32_16x16x32_bf16 v[120:123], v[164:167], v[180:183], v[120:123]
	v_mfma_f32_16x16x32_bf16 v[116:119], v[172:175], v[180:183], v[116:119]
	v_mfma_f32_16x16x32_bf16 v[104:107], v[164:167], v[188:191], v[104:107]
	v_mfma_f32_16x16x32_bf16 v[100:103], v[172:175], v[188:191], v[100:103]
	v_mfma_f32_16x16x32_bf16 v[88:91], v[164:167], v[210:213], v[88:91]
	v_mfma_f32_16x16x32_bf16 v[84:87], v[172:175], v[210:213], v[84:87]
	v_mfma_f32_16x16x32_bf16 v[72:75], v[164:167], v[230:233], v[72:75]
	v_mfma_f32_16x16x32_bf16 v[68:71], v[172:175], v[230:233], v[68:71]
	v_mfma_f32_16x16x32_bf16 v[120:123], v[168:171], v[184:187], v[120:123]
	v_mfma_f32_16x16x32_bf16 v[116:119], v[176:179], v[184:187], v[116:119]
	v_mfma_f32_16x16x32_bf16 v[104:107], v[168:171], v[192:195], v[104:107]
	v_mfma_f32_16x16x32_bf16 v[100:103], v[176:179], v[192:195], v[100:103]
	v_mfma_f32_16x16x32_bf16 v[88:91], v[168:171], v[226:229], v[88:91]
	v_mfma_f32_16x16x32_bf16 v[84:87], v[176:179], v[226:229], v[84:87]
	v_mfma_f32_16x16x32_bf16 v[72:75], v[168:171], v[234:237], v[72:75]
	s_barrier
	v_mfma_f32_16x16x32_bf16 v[68:71], v[176:179], v[234:237], v[68:71]
	s_setprio 0
	s_add_i32 s50, s50, s26
	v_lshl_add_u64 v[196:197], s[18:19], 0, v[134:135]
	s_mov_b32 m0, s50
	ds_read_b128 v[180:183], v147 offset:16384
	ds_read_b128 v[184:187], v147 offset:17408
	ds_read_b128 v[188:191], v147 offset:18432
	ds_read_b128 v[192:195], v147 offset:19456
	ds_read_b128 v[210:213], v147 offset:20480
	ds_read_b128 v[226:229], v147 offset:21504
	ds_read_b128 v[230:233], v147 offset:22528
	ds_read_b128 v[234:237], v147 offset:23552
	global_load_lds_dwordx4 v[196:197], off
	s_add_i32 m0, s50, 0x2000
	s_add_u32 s50, s18, 0x80000
	v_lshl_add_u64 v[238:239], s[18:19], 0, v[138:139]
	s_addc_u32 s51, s19, 0
	s_add_i32 s52, s52, s26
	global_load_lds_dwordx4 v[238:239], off
	v_lshl_add_u64 v[240:241], s[50:51], 0, v[134:135]
	s_mov_b32 m0, s52
	v_lshl_add_u64 v[242:243], s[20:21], 0, v[136:137]
	global_load_lds_dwordx4 v[240:241], off
	v_lshl_add_u64 v[240:241], s[50:51], 0, v[138:139]
	s_add_i32 m0, s52, 0x2000
	s_nop 0
	global_load_lds_dwordx4 v[240:241], off
	v_lshl_add_u64 v[240:241], s[20:21], 0, v[132:133]
	s_mov_b32 m0, s28
	s_nop 0
	global_load_lds_dwordx4 v[240:241], off
	s_mov_b32 m0, s29
	s_nop 0
	global_load_lds_dwordx4 v[242:243], off
	s_waitcnt vmcnt(8)
	s_waitcnt lgkmcnt(0)
	s_barrier
; #define PG8_STAGE(bufoff, gbase, voff) do { _Pragma("unroll") for (int _i = 0; _i < 2; ++_i) \
;         __builtin_amdgcn_global_load_lds((const unsigned*)((const char*)(gbase) + (voff)[_i]), (PG8_LAS unsigned*)(lds + (bufoff) + ldsw + _i * 8192), 16, 0, 0); } while (0)
; #define PG8_LDA(dst, b, h) do { _Pragma("unroll") for (int m = 0; m < 4; ++m) _Pragma("unroll") for (int k = 0; k < 2; ++k) dst[m][k] = *(const PG8_LAS bf16x8*)(lds + PG8_SA(b, h) + aoff + m * 2048 + k * 1024); } while (0)
; #define PG8_LDB(dst, b, h) do { _Pragma("unroll") for (int n = 0; n < 2; ++n) _Pragma("unroll") for (int k = 0; k < 2; ++k) dst[n][k] = *(const PG8_LAS bf16x8*)(lds + PG8_SB(b, h) + boff + n * 2048 + k * 1024); } while (0)
; #define PG8_MMA(ai, bj, At, Bt) do { __builtin_amdgcn_s_setprio(1); _Pragma("unroll") for (int m = 0; m < 4; ++m) _Pragma("unroll") for (int n = 0; n < 2; ++n) _Pragma("unroll") for (int k = 0; k < 2; ++k) \
;         acc[ai][bj][m][n] = __builtin_amdgcn_mfma_f32_16x16x32_bf16(Bt[n][k], At[m][k], acc[ai][bj][m][n], 0, 0, 0); __builtin_amdgcn_s_setprio(0); } while (0)
; #define PG8_WAIT_V(n) asm volatile("s_waitcnt vmcnt(" #n ")" ::: "memory")
; #define PG8_WAIT_L(n) asm volatile("s_waitcnt lgkmcnt(" #n ")" ::: "memory")
; #define PG8_BAR __builtin_amdgcn_s_barrier()
; #define PG8_SCHED __builtin_amdgcn_sched_barrier(0)
; template <class Epi, class Sched, bool ALIGN_EPI = false, bool SP2 = false>
; __device__ __forceinline__ void gemm_phase(PG8_LAS unsigned char* lds, const Gemm g, const Sched& S, const Epi& E) {
;     ...
;             PG8_WAIT_V(8); PG8_WAIT_L(0); PG8_BAR; PG8_MMA(1, 0, At, B0); PG8_MMA(1, 1, At, B1); PG8_BAR; PG8_SCHED;
;             PG8_LDB(B0, 1, 0); PG8_LDB(B1, 1, 1); PG8_SCHED; PG8_LDA(At, 1, 0); PG8_STAGE(PG8_SA(0, 1), a2 + hstepA, voffA);
;             PG8_WAIT_V(8); PG8_WAIT_L(0); PG8_BAR; PG8_MMA(0, 0, At, B0); PG8_MMA(0, 1, At, B1); PG8_BAR; PG8_SCHED;
;             PG8_LDA(At, 1, 1); PG8_STAGE(PG8_SB(1, 0), b3, voffB); PG8_STAGE(PG8_SB(1, 1), b3 + hstepB, voffB); PG8_STAGE(PG8_SA(1, 0), a3, voffA);
	s_setprio 1
	s_waitcnt lgkmcnt(0)
	v_mfma_f32_16x16x32_bf16 v[64:67], v[148:151], v[180:183], v[64:67]
	v_mfma_f32_16x16x32_bf16 v[60:63], v[156:159], v[180:183], v[60:63]
	v_mfma_f32_16x16x32_bf16 v[48:51], v[148:151], v[188:191], v[48:51]
	v_mfma_f32_16x16x32_bf16 v[44:47], v[156:159], v[188:191], v[44:47]
	v_mfma_f32_16x16x32_bf16 v[32:35], v[148:151], v[210:213], v[32:35]
	v_mfma_f32_16x16x32_bf16 v[28:31], v[156:159], v[210:213], v[28:31]
	v_mfma_f32_16x16x32_bf16 v[16:19], v[148:151], v[230:233], v[16:19]
	v_mfma_f32_16x16x32_bf16 v[12:15], v[156:159], v[230:233], v[12:15]
	v_mfma_f32_16x16x32_bf16 v[64:67], v[152:155], v[184:187], v[64:67]
	v_mfma_f32_16x16x32_bf16 v[60:63], v[160:163], v[184:187], v[60:63]
	v_mfma_f32_16x16x32_bf16 v[48:51], v[152:155], v[192:195], v[48:51]
	v_mfma_f32_16x16x32_bf16 v[44:47], v[160:163], v[192:195], v[44:47]
	v_mfma_f32_16x16x32_bf16 v[32:35], v[152:155], v[226:229], v[32:35]
	v_mfma_f32_16x16x32_bf16 v[28:31], v[160:163], v[226:229], v[28:31]
	v_mfma_f32_16x16x32_bf16 v[16:19], v[152:155], v[234:237], v[16:19]
	v_mfma_f32_16x16x32_bf16 v[12:15], v[160:163], v[234:237], v[12:15]
	s_setprio 0
	s_setprio 1
	v_mfma_f32_16x16x32_bf16 v[56:59], v[164:167], v[180:183], v[56:59]
	v_mfma_f32_16x16x32_bf16 v[52:55], v[172:175], v[180:183], v[52:55]
	v_mfma_f32_16x16x32_bf16 v[40:43], v[164:167], v[188:191], v[40:43]
	v_mfma_f32_16x16x32_bf16 v[36:39], v[172:175], v[188:191], v[36:39]
	v_mfma_f32_16x16x32_bf16 v[24:27], v[164:167], v[210:213], v[24:27]
	v_mfma_f32_16x16x32_bf16 v[20:23], v[172:175], v[210:213], v[20:23]
	v_mfma_f32_16x16x32_bf16 v[8:11], v[164:167], v[230:233], v[8:11]
	v_mfma_f32_16x16x32_bf16 v[4:7], v[172:175], v[230:233], v[4:7]
	v_mfma_f32_16x16x32_bf16 v[56:59], v[168:171], v[184:187], v[56:59]
	v_mfma_f32_16x16x32_bf16 v[52:55], v[176:179], v[184:187], v[52:55]
	v_mfma_f32_16x16x32_bf16 v[40:43], v[168:171], v[192:195], v[40:43]
	v_mfma_f32_16x16x32_bf16 v[36:39], v[176:179], v[192:195], v[36:39]
	v_mfma_f32_16x16x32_bf16 v[24:27], v[168:171], v[226:229], v[24:27]
	v_mfma_f32_16x16x32_bf16 v[20:23], v[176:179], v[226:229], v[20:23]
	v_mfma_f32_16x16x32_bf16 v[8:11], v[168:171], v[234:237], v[8:11]
	s_barrier
	v_mfma_f32_16x16x32_bf16 v[4:7], v[176:179], v[234:237], v[4:7]
	s_setprio 0
	s_add_i32 s50, 0, 0x18000
	s_add_i32 s51, 0, 0x1c000
	v_add_u32_e32 v160, s50, v146
	v_add_u32_e32 v176, s51, v146
	ds_read_b128 v[148:151], v160
	ds_read_b128 v[152:155], v160 offset:1024
	ds_read_b128 v[156:159], v160 offset:2048
	ds_read_b128 v[160:163], v160 offset:3072
	ds_read_b128 v[164:167], v176
	ds_read_b128 v[168:171], v176 offset:1024
	ds_read_b128 v[172:175], v176 offset:2048
	ds_read_b128 v[176:179], v176 offset:3072
	s_add_u32 s20, s20, 0x40000
	s_addc_u32 s21, s21, 0
	s_mov_b32 m0, s30
	v_lshl_add_u64 v[244:245], s[20:21], 0, v[132:133]
	ds_read_b128 v[180:183], v147 offset:32768
	ds_read_b128 v[184:187], v147 offset:33792
	ds_read_b128 v[188:191], v147 offset:34816
	ds_read_b128 v[192:195], v147 offset:35840
	ds_read_b128 v[210:213], v147 offset:36864
	ds_read_b128 v[226:229], v147 offset:37888
	ds_read_b128 v[230:233], v147 offset:38912
	ds_read_b128 v[234:237], v147 offset:39936
	global_load_lds_dwordx4 v[244:245], off
	v_lshl_add_u64 v[244:245], s[20:21], 0, v[136:137]
	s_mov_b32 m0, s31
	s_nop 0
	global_load_lds_dwordx4 v[244:245], off
	s_waitcnt vmcnt(8)
	s_waitcnt lgkmcnt(0)
	s_barrier
	s_setprio 1
	s_waitcnt lgkmcnt(0)
	v_mfma_f32_16x16x32_bf16 v[124:127], v[148:151], v[180:183], v[124:127]
	v_mfma_f32_16x16x32_bf16 v[128:131], v[156:159], v[180:183], v[128:131]
	v_mfma_f32_16x16x32_bf16 v[112:115], v[148:151], v[188:191], v[112:115]
	v_mfma_f32_16x16x32_bf16 v[108:111], v[156:159], v[188:191], v[108:111]
	v_mfma_f32_16x16x32_bf16 v[96:99], v[148:151], v[210:213], v[96:99]
	v_mfma_f32_16x16x32_bf16 v[92:95], v[156:159], v[210:213], v[92:95]
	v_mfma_f32_16x16x32_bf16 v[80:83], v[148:151], v[230:233], v[80:83]
	v_mfma_f32_16x16x32_bf16 v[76:79], v[156:159], v[230:233], v[76:79]
	v_mfma_f32_16x16x32_bf16 v[124:127], v[152:155], v[184:187], v[124:127]
	v_mfma_f32_16x16x32_bf16 v[128:131], v[160:163], v[184:187], v[128:131]
	v_mfma_f32_16x16x32_bf16 v[112:115], v[152:155], v[192:195], v[112:115]
	v_mfma_f32_16x16x32_bf16 v[108:111], v[160:163], v[192:195], v[108:111]
	v_mfma_f32_16x16x32_bf16 v[96:99], v[152:155], v[226:229], v[96:99]
	v_mfma_f32_16x16x32_bf16 v[92:95], v[160:163], v[226:229], v[92:95]
	v_mfma_f32_16x16x32_bf16 v[80:83], v[152:155], v[234:237], v[80:83]
	v_mfma_f32_16x16x32_bf16 v[76:79], v[160:163], v[234:237], v[76:79]
	s_setprio 0
	s_setprio 1
	v_mfma_f32_16x16x32_bf16 v[120:123], v[164:167], v[180:183], v[120:123]
	v_mfma_f32_16x16x32_bf16 v[116:119], v[172:175], v[180:183], v[116:119]
	v_mfma_f32_16x16x32_bf16 v[104:107], v[164:167], v[188:191], v[104:107]
	v_mfma_f32_16x16x32_bf16 v[100:103], v[172:175], v[188:191], v[100:103]
	v_mfma_f32_16x16x32_bf16 v[88:91], v[164:167], v[210:213], v[88:91]
	v_mfma_f32_16x16x32_bf16 v[84:87], v[172:175], v[210:213], v[84:87]
	v_mfma_f32_16x16x32_bf16 v[72:75], v[164:167], v[230:233], v[72:75]
	v_mfma_f32_16x16x32_bf16 v[68:71], v[172:175], v[230:233], v[68:71]
	v_mfma_f32_16x16x32_bf16 v[120:123], v[168:171], v[184:187], v[120:123]
	v_mfma_f32_16x16x32_bf16 v[116:119], v[176:179], v[184:187], v[116:119]
	v_mfma_f32_16x16x32_bf16 v[104:107], v[168:171], v[192:195], v[104:107]
	v_mfma_f32_16x16x32_bf16 v[100:103], v[176:179], v[192:195], v[100:103]
	v_mfma_f32_16x16x32_bf16 v[88:91], v[168:171], v[226:229], v[88:91]
	v_mfma_f32_16x16x32_bf16 v[84:87], v[176:179], v[226:229], v[84:87]
	v_mfma_f32_16x16x32_bf16 v[72:75], v[168:171], v[234:237], v[72:75]
	s_barrier
; #define PG8_STAGE(bufoff, gbase, voff) do { _Pragma("unroll") for (int _i = 0; _i < 2; ++_i) \
;         __builtin_amdgcn_global_load_lds((const unsigned*)((const char*)(gbase) + (voff)[_i]), (PG8_LAS unsigned*)(lds + (bufoff) + ldsw + _i * 8192), 16, 0, 0); } while (0)
; #define PG8_LDA(dst, b, h) do { _Pragma("unroll") for (int m = 0; m < 4; ++m) _Pragma("unroll") for (int k = 0; k < 2; ++k) dst[m][k] = *(const PG8_LAS bf16x8*)(lds + PG8_SA(b, h) + aoff + m * 2048 + k * 1024); } while (0)
; #define PG8_MMA(ai, bj, At, Bt) do { __builtin_amdgcn_s_setprio(1); _Pragma("unroll") for (int m = 0; m < 4; ++m) _Pragma("unroll") for (int n = 0; n < 2; ++n) _Pragma("unroll") for (int k = 0; k < 2; ++k) \
;         acc[ai][bj][m][n] = __builtin_amdgcn_mfma_f32_16x16x32_bf16(Bt[n][k], At[m][k], acc[ai][bj][m][n], 0, 0, 0); __builtin_amdgcn_s_setprio(0); } while (0)
; #define PG8_WAIT_V(n) asm volatile("s_waitcnt vmcnt(" #n ")" ::: "memory")
; #define PG8_WAIT_L(n) asm volatile("s_waitcnt lgkmcnt(" #n ")" ::: "memory")
; #define PG8_BAR __builtin_amdgcn_s_barrier()
; #define PG8_SCHED __builtin_amdgcn_sched_barrier(0)
; template <class Epi, class Sched, bool ALIGN_EPI = false, bool SP2 = false>
; __device__ __forceinline__ void gemm_phase(PG8_LAS unsigned char* lds, const Gemm g, const Sched& S, const Epi& E) {
;     ...
;         for (int t = 0; t < nt; t += 2) {
;     ...
;             PG8_WAIT_V(8); PG8_WAIT_L(0); PG8_BAR; PG8_MMA(0, 0, At, B0); PG8_MMA(0, 1, At, B1); PG8_BAR; PG8_SCHED;
;             PG8_LDA(At, 1, 1); PG8_STAGE(PG8_SB(1, 0), b3, voffB); PG8_STAGE(PG8_SB(1, 1), b3 + hstepB, voffB); PG8_STAGE(PG8_SA(1, 0), a3, voffA);
;             PG8_WAIT_V(8); PG8_WAIT_L(0); PG8_BAR; PG8_MMA(1, 0, At, B0); PG8_MMA(1, 1, At, B1); PG8_BAR; PG8_SCHED;
	v_mfma_f32_16x16x32_bf16 v[68:71], v[176:179], v[234:237], v[68:71]
	s_setprio 0
	s_add_i32 s20, s50, s26
	v_lshl_add_u64 v[196:197], v[196:197], 0, s[64:65]
	s_mov_b32 m0, s20
	ds_read_b128 v[180:183], v147 offset:49152
	ds_read_b128 v[184:187], v147 offset:50176
	ds_read_b128 v[188:191], v147 offset:51200
	ds_read_b128 v[192:195], v147 offset:52224
	ds_read_b128 v[210:213], v147 offset:53248
	ds_read_b128 v[226:229], v147 offset:54272
	ds_read_b128 v[230:233], v147 offset:55296
	ds_read_b128 v[234:237], v147 offset:56320
	global_load_lds_dwordx4 v[196:197], off
	s_add_i32 m0, s20, 0x2000
	s_add_u32 s18, s18, 0x80080
	v_lshl_add_u64 v[196:197], v[238:239], 0, s[64:65]
	s_addc_u32 s19, s19, 0
	s_add_i32 s20, s51, s26
	global_load_lds_dwordx4 v[196:197], off
	v_lshl_add_u64 v[196:197], s[18:19], 0, v[134:135]
	s_mov_b32 m0, s20
	s_nop 0
	global_load_lds_dwordx4 v[196:197], off
	v_lshl_add_u64 v[196:197], s[18:19], 0, v[138:139]
	s_add_i32 m0, s20, 0x2000
	s_nop 0
	global_load_lds_dwordx4 v[196:197], off
	v_lshl_add_u64 v[196:197], v[240:241], 0, s[64:65]
	s_mov_b32 m0, s34
	s_nop 0
	global_load_lds_dwordx4 v[196:197], off
	v_lshl_add_u64 v[196:197], v[242:243], 0, s[64:65]
	s_mov_b32 m0, s35
	s_nop 0
	global_load_lds_dwordx4 v[196:197], off
	s_waitcnt vmcnt(8)
	s_waitcnt lgkmcnt(0)
	s_barrier
	s_setprio 1
	s_waitcnt lgkmcnt(0)
	v_mfma_f32_16x16x32_bf16 v[64:67], v[148:151], v[180:183], v[64:67]
	v_mfma_f32_16x16x32_bf16 v[60:63], v[156:159], v[180:183], v[60:63]
	v_mfma_f32_16x16x32_bf16 v[48:51], v[148:151], v[188:191], v[48:51]
	v_mfma_f32_16x16x32_bf16 v[44:47], v[156:159], v[188:191], v[44:47]
	v_mfma_f32_16x16x32_bf16 v[32:35], v[148:151], v[210:213], v[32:35]
	v_mfma_f32_16x16x32_bf16 v[28:31], v[156:159], v[210:213], v[28:31]
	v_mfma_f32_16x16x32_bf16 v[16:19], v[148:151], v[230:233], v[16:19]
	v_mfma_f32_16x16x32_bf16 v[12:15], v[156:159], v[230:233], v[12:15]
	v_mfma_f32_16x16x32_bf16 v[64:67], v[152:155], v[184:187], v[64:67]
	v_mfma_f32_16x16x32_bf16 v[60:63], v[160:163], v[184:187], v[60:63]
	v_mfma_f32_16x16x32_bf16 v[48:51], v[152:155], v[192:195], v[48:51]
	v_mfma_f32_16x16x32_bf16 v[44:47], v[160:163], v[192:195], v[44:47]
	v_mfma_f32_16x16x32_bf16 v[32:35], v[152:155], v[226:229], v[32:35]
	v_mfma_f32_16x16x32_bf16 v[28:31], v[160:163], v[226:229], v[28:31]
	v_mfma_f32_16x16x32_bf16 v[16:19], v[152:155], v[234:237], v[16:19]
	v_mfma_f32_16x16x32_bf16 v[12:15], v[160:163], v[234:237], v[12:15]
	s_setprio 0
	s_setprio 1
	v_mfma_f32_16x16x32_bf16 v[56:59], v[164:167], v[180:183], v[56:59]
	v_mfma_f32_16x16x32_bf16 v[52:55], v[172:175], v[180:183], v[52:55]
	v_mfma_f32_16x16x32_bf16 v[40:43], v[164:167], v[188:191], v[40:43]
	v_mfma_f32_16x16x32_bf16 v[36:39], v[172:175], v[188:191], v[36:39]
	v_mfma_f32_16x16x32_bf16 v[24:27], v[164:167], v[210:213], v[24:27]
	v_mfma_f32_16x16x32_bf16 v[20:23], v[172:175], v[210:213], v[20:23]
	v_mfma_f32_16x16x32_bf16 v[8:11], v[164:167], v[230:233], v[8:11]
	v_mfma_f32_16x16x32_bf16 v[4:7], v[172:175], v[230:233], v[4:7]
	v_mfma_f32_16x16x32_bf16 v[56:59], v[168:171], v[184:187], v[56:59]
	v_mfma_f32_16x16x32_bf16 v[52:55], v[176:179], v[184:187], v[52:55]
	v_mfma_f32_16x16x32_bf16 v[40:43], v[168:171], v[192:195], v[40:43]
	v_mfma_f32_16x16x32_bf16 v[36:39], v[176:179], v[192:195], v[36:39]
	v_mfma_f32_16x16x32_bf16 v[24:27], v[168:171], v[226:229], v[24:27]
	v_mfma_f32_16x16x32_bf16 v[20:23], v[176:179], v[226:229], v[20:23]
	v_mfma_f32_16x16x32_bf16 v[8:11], v[168:171], v[234:237], v[8:11]
	s_barrier
	v_mfma_f32_16x16x32_bf16 v[4:7], v[176:179], v[234:237], v[4:7]
	s_setprio 0
	s_add_u32 s47, s47, 0x100
	s_addc_u32 s48, s48, 0
	s_add_u32 s16, s16, 0x100
	s_addc_u32 s17, s17, 0
	s_cmp_ge_i32 s49, s33
	s_mov_b32 s18, s49
	s_cbranch_scc0 .LBB0_1236

; #define PG8_STAGE(bufoff, gbase, voff) do { _Pragma("unroll") for (int _i = 0; _i < 2; ++_i) \
;         __builtin_amdgcn_global_load_lds((const unsigned*)((const char*)(gbase) + (voff)[_i]), (PG8_LAS unsigned*)(lds + (bufoff) + ldsw + _i * 8192), 16, 0, 0); } while (0)
; #define PG8_LDA(dst, b, h) do { _Pragma("unroll") for (int m = 0; m < 4; ++m) _Pragma("unroll") for (int k = 0; k < 2; ++k) dst[m][k] = *(const PG8_LAS bf16x8*)(lds + PG8_SA(b, h) + aoff + m * 2048 + k * 1024); } while (0)
; #define PG8_LDB(dst, b, h) do { _Pragma("unroll") for (int n = 0; n < 2; ++n) _Pragma("unroll") for (int k = 0; k < 2; ++k) dst[n][k] = *(const PG8_LAS bf16x8*)(lds + PG8_SB(b, h) + boff + n * 2048 + k * 1024); } while (0)
; #define PG8_MMA(ai, bj, At, Bt) do { __builtin_amdgcn_s_setprio(1); _Pragma("unroll") for (int m = 0; m < 4; ++m) _Pragma("unroll") for (int n = 0; n < 2; ++n) _Pragma("unroll") for (int k = 0; k < 2; ++k) \
;         acc[ai][bj][m][n] = __builtin_amdgcn_mfma_f32_16x16x32_bf16(Bt[n][k], At[m][k], acc[ai][bj][m][n], 0, 0, 0); __builtin_amdgcn_s_setprio(0); } while (0)
; #define PG8_WAIT_V(n) asm volatile("s_waitcnt vmcnt(" #n ")" ::: "memory")
; #define PG8_WAIT_L(n) asm volatile("s_waitcnt lgkmcnt(" #n ")" ::: "memory")
; template <class Epi, class Sched, bool ALIGN_EPI = false, bool SP2 = false>
; __device__ __forceinline__ void gemm_phase(PG8_LAS unsigned char* lds, const Gemm g, const Sched& S, const Epi& E) {
;     ...
;             const bool last = (t == nt - 2);
;             const char* a1 = cA + (size_t)(t + 1) * kstep;
;             const char* a2 = last ? nA : cA + (size_t)(t + 2) * kstep; const char* b2 = last ? nB : cB + (size_t)(t + 2) * kstep;
;             const char* a3 = a2 + kstep; const char* b3 = b2 + kstep;
;             if (last && has_next) S.a_ready(nxt);
;             if constexpr (SP2) {
;             PG8_LDB(B0, 0, 0); PG8_LDB(B1, 0, 1); PG8_SCHED; PG8_LDA(At, 0, 0); PG8_STAGE(PG8_SA(1, 1), a1 + hstepA, voffA);
;             PG8_WAIT_V(8); PG8_WAIT_L(0); PG8_BAR; PG8_MMA(0, 0, At, B0); PG8_MMA(0, 1, At, B1); PG8_BAR; PG8_SCHED;
;             PG8_LDA(At, 0, 1); PG8_STAGE(PG8_SB(0, 0), b2, voffB); PG8_STAGE(PG8_SB(0, 1), b2 + hstepB, voffB); PG8_STAGE(PG8_SA(0, 0), a2, voffA);
;             PG8_WAIT_V(8); PG8_WAIT_L(0); PG8_BAR; PG8_MMA(1, 0, At, B0); PG8_MMA(1, 1, At, B1); PG8_BAR; PG8_SCHED;
.LBB0_1247:
	s_add_u32 s10, s23, s8
	s_addc_u32 s11, s30, s9
	s_add_u32 s10, s10, 0xb000100
	s_addc_u32 s11, s11, 0
	s_add_u32 s33, s28, s8
	s_addc_u32 s34, s29, s9
	s_add_i32 s35, 0, 0x10000
	s_cmpk_eq_i32 s8, 0x700
	s_cselect_b32 s13, s7, s11
	s_cselect_b32 s12, s6, s10
	v_add_u32_e32 v147, s35, v145
	s_cselect_b32 s11, s5, s34
	s_cselect_b32 s10, s4, s33
	s_add_i32 s33, 0, 0x14000
	ds_read_b128 v[148:151], v147
	ds_read_b128 v[152:155], v147 offset:1024
	ds_read_b128 v[156:159], v147 offset:2048
	ds_read_b128 v[160:163], v147 offset:3072
	v_add_u32_e32 v147, s33, v145
	ds_read_b128 v[164:167], v147
	ds_read_b128 v[168:171], v147 offset:1024
	ds_read_b128 v[172:175], v147 offset:2048
	ds_read_b128 v[176:179], v147 offset:3072
	v_lshl_add_u64 v[196:197], v[142:143], 0, s[8:9]
	s_add_i32 m0, s19, 0xc000
	ds_read_b128 v[180:183], v146
	ds_read_b128 v[184:187], v146 offset:1024
	ds_read_b128 v[188:191], v146 offset:2048
	ds_read_b128 v[192:195], v146 offset:3072
	ds_read_b128 v[210:213], v146 offset:4096
	ds_read_b128 v[226:229], v146 offset:5120
	ds_read_b128 v[230:233], v146 offset:6144
	ds_read_b128 v[234:237], v146 offset:7168
	global_load_lds_dwordx4 v[196:197], off
	v_lshl_add_u64 v[196:197], v[140:141], 0, s[8:9]
	s_add_i32 m0, s19, 0xe000
	s_nop 0
	global_load_lds_dwordx4 v[196:197], off
	s_waitcnt vmcnt(8)
	s_waitcnt lgkmcnt(0)
	s_barrier
	s_setprio 1
	s_waitcnt lgkmcnt(0)
	v_mfma_f32_16x16x32_bf16 v[128:131], v[148:151], v[180:183], v[128:131]
	v_mfma_f32_16x16x32_bf16 v[124:127], v[156:159], v[180:183], v[124:127]
	v_mfma_f32_16x16x32_bf16 v[116:119], v[148:151], v[188:191], v[116:119]
	v_mfma_f32_16x16x32_bf16 v[108:111], v[156:159], v[188:191], v[108:111]
	v_mfma_f32_16x16x32_bf16 v[104:107], v[148:151], v[210:213], v[104:107]
	v_mfma_f32_16x16x32_bf16 v[96:99], v[156:159], v[210:213], v[96:99]
	v_mfma_f32_16x16x32_bf16 v[88:91], v[148:151], v[230:233], v[88:91]
	v_mfma_f32_16x16x32_bf16 v[80:83], v[156:159], v[230:233], v[80:83]
	v_mfma_f32_16x16x32_bf16 v[128:131], v[152:155], v[184:187], v[128:131]
	v_mfma_f32_16x16x32_bf16 v[124:127], v[160:163], v[184:187], v[124:127]
	v_mfma_f32_16x16x32_bf16 v[116:119], v[152:155], v[192:195], v[116:119]
	v_mfma_f32_16x16x32_bf16 v[108:111], v[160:163], v[192:195], v[108:111]
	v_mfma_f32_16x16x32_bf16 v[104:107], v[152:155], v[226:229], v[104:107]
	v_mfma_f32_16x16x32_bf16 v[96:99], v[160:163], v[226:229], v[96:99]
	v_mfma_f32_16x16x32_bf16 v[88:91], v[152:155], v[234:237], v[88:91]
	v_mfma_f32_16x16x32_bf16 v[80:83], v[160:163], v[234:237], v[80:83]
	s_setprio 0
	s_setprio 1
	v_mfma_f32_16x16x32_bf16 v[120:123], v[164:167], v[180:183], v[120:123]
	v_mfma_f32_16x16x32_bf16 v[112:115], v[172:175], v[180:183], v[112:115]
	v_mfma_f32_16x16x32_bf16 v[100:103], v[164:167], v[188:191], v[100:103]
	v_mfma_f32_16x16x32_bf16 v[92:95], v[172:175], v[188:191], v[92:95]
	v_mfma_f32_16x16x32_bf16 v[84:87], v[164:167], v[210:213], v[84:87]
	v_mfma_f32_16x16x32_bf16 v[76:79], v[172:175], v[210:213], v[76:79]
	v_mfma_f32_16x16x32_bf16 v[72:75], v[164:167], v[230:233], v[72:75]
	v_mfma_f32_16x16x32_bf16 v[68:71], v[172:175], v[230:233], v[68:71]
	v_mfma_f32_16x16x32_bf16 v[120:123], v[168:171], v[184:187], v[120:123]
	v_mfma_f32_16x16x32_bf16 v[112:115], v[176:179], v[184:187], v[112:115]
	v_mfma_f32_16x16x32_bf16 v[100:103], v[168:171], v[192:195], v[100:103]
	v_mfma_f32_16x16x32_bf16 v[92:95], v[176:179], v[192:195], v[92:95]
	v_mfma_f32_16x16x32_bf16 v[84:87], v[168:171], v[226:229], v[84:87]
	v_mfma_f32_16x16x32_bf16 v[76:79], v[176:179], v[226:229], v[76:79]
	v_mfma_f32_16x16x32_bf16 v[72:75], v[168:171], v[234:237], v[72:75]
	s_barrier
	v_mfma_f32_16x16x32_bf16 v[68:71], v[176:179], v[234:237], v[68:71]
	s_setprio 0
	s_add_i32 s34, s35, s18
	v_lshl_add_u64 v[196:197], s[10:11], 0, v[134:135]
	s_mov_b32 m0, s34
	ds_read_b128 v[180:183], v146 offset:16384
	ds_read_b128 v[184:187], v146 offset:17408
	ds_read_b128 v[188:191], v146 offset:18432
	ds_read_b128 v[192:195], v146 offset:19456
	ds_read_b128 v[210:213], v146 offset:20480
	ds_read_b128 v[226:229], v146 offset:21504
	ds_read_b128 v[230:233], v146 offset:22528
	ds_read_b128 v[234:237], v146 offset:23552
	global_load_lds_dwordx4 v[196:197], off
	s_add_i32 m0, s34, 0x2000
	s_add_u32 s34, s10, 0x40000
	v_lshl_add_u64 v[238:239], s[10:11], 0, v[138:139]
	s_addc_u32 s35, s11, 0
	s_add_i32 s33, s33, s18
	global_load_lds_dwordx4 v[238:239], off
	v_lshl_add_u64 v[240:241], s[34:35], 0, v[134:135]
	s_mov_b32 m0, s33
	v_lshl_add_u64 v[242:243], s[12:13], 0, v[136:137]
	global_load_lds_dwordx4 v[240:241], off
	v_lshl_add_u64 v[240:241], s[34:35], 0, v[138:139]
	s_add_i32 m0, s33, 0x2000
	s_nop 0
	global_load_lds_dwordx4 v[240:241], off
	v_lshl_add_u64 v[240:241], s[12:13], 0, v[132:133]
	s_mov_b32 m0, s19
	s_nop 0
	global_load_lds_dwordx4 v[240:241], off
	s_mov_b32 m0, s20
	s_nop 0
	global_load_lds_dwordx4 v[242:243], off
	s_waitcnt vmcnt(8)
	s_waitcnt lgkmcnt(0)
	s_barrier
; #define PG8_STAGE(bufoff, gbase, voff) do { _Pragma("unroll") for (int _i = 0; _i < 2; ++_i) \
;         __builtin_amdgcn_global_load_lds((const unsigned*)((const char*)(gbase) + (voff)[_i]), (PG8_LAS unsigned*)(lds + (bufoff) + ldsw + _i * 8192), 16, 0, 0); } while (0)
; #define PG8_LDA(dst, b, h) do { _Pragma("unroll") for (int m = 0; m < 4; ++m) _Pragma("unroll") for (int k = 0; k < 2; ++k) dst[m][k] = *(const PG8_LAS bf16x8*)(lds + PG8_SA(b, h) + aoff + m * 2048 + k * 1024); } while (0)
; #define PG8_LDB(dst, b, h) do { _Pragma("unroll") for (int n = 0; n < 2; ++n) _Pragma("unroll") for (int k = 0; k < 2; ++k) dst[n][k] = *(const PG8_LAS bf16x8*)(lds + PG8_SB(b, h) + boff + n * 2048 + k * 1024); } while (0)
; #define PG8_MMA(ai, bj, At, Bt) do { __builtin_amdgcn_s_setprio(1); _Pragma("unroll") for (int m = 0; m < 4; ++m) _Pragma("unroll") for (int n = 0; n < 2; ++n) _Pragma("unroll") for (int k = 0; k < 2; ++k) \
;         acc[ai][bj][m][n] = __builtin_amdgcn_mfma_f32_16x16x32_bf16(Bt[n][k], At[m][k], acc[ai][bj][m][n], 0, 0, 0); __builtin_amdgcn_s_setprio(0); } while (0)
; #define PG8_WAIT_V(n) asm volatile("s_waitcnt vmcnt(" #n ")" ::: "memory")
; #define PG8_WAIT_L(n) asm volatile("s_waitcnt lgkmcnt(" #n ")" ::: "memory")
; #define PG8_BAR __builtin_amdgcn_s_barrier()
; #define PG8_SCHED __builtin_amdgcn_sched_barrier(0)
; template <class Epi, class Sched, bool ALIGN_EPI = false, bool SP2 = false>
; __device__ __forceinline__ void gemm_phase(PG8_LAS unsigned char* lds, const Gemm g, const Sched& S, const Epi& E) {
;     ...
;             PG8_WAIT_V(8); PG8_WAIT_L(0); PG8_BAR; PG8_MMA(1, 0, At, B0); PG8_MMA(1, 1, At, B1); PG8_BAR; PG8_SCHED;
;             PG8_LDB(B0, 1, 0); PG8_LDB(B1, 1, 1); PG8_SCHED; PG8_LDA(At, 1, 0); PG8_STAGE(PG8_SA(0, 1), a2 + hstepA, voffA);
;             PG8_WAIT_V(8); PG8_WAIT_L(0); PG8_BAR; PG8_MMA(0, 0, At, B0); PG8_MMA(0, 1, At, B1); PG8_BAR; PG8_SCHED;
;             PG8_LDA(At, 1, 1); PG8_STAGE(PG8_SB(1, 0), b3, voffB); PG8_STAGE(PG8_SB(1, 1), b3 + hstepB, voffB); PG8_STAGE(PG8_SA(1, 0), a3, voffA);
	s_setprio 1
	s_waitcnt lgkmcnt(0)
	v_mfma_f32_16x16x32_bf16 v[64:67], v[148:151], v[180:183], v[64:67]
	v_mfma_f32_16x16x32_bf16 v[60:63], v[156:159], v[180:183], v[60:63]
	v_mfma_f32_16x16x32_bf16 v[52:55], v[148:151], v[188:191], v[52:55]
	v_mfma_f32_16x16x32_bf16 v[44:47], v[156:159], v[188:191], v[44:47]
	v_mfma_f32_16x16x32_bf16 v[40:43], v[148:151], v[210:213], v[40:43]
	v_mfma_f32_16x16x32_bf16 v[32:35], v[156:159], v[210:213], v[32:35]
	v_mfma_f32_16x16x32_bf16 v[24:27], v[148:151], v[230:233], v[24:27]
	v_mfma_f32_16x16x32_bf16 v[16:19], v[156:159], v[230:233], v[16:19]
	v_mfma_f32_16x16x32_bf16 v[64:67], v[152:155], v[184:187], v[64:67]
	v_mfma_f32_16x16x32_bf16 v[60:63], v[160:163], v[184:187], v[60:63]
	v_mfma_f32_16x16x32_bf16 v[52:55], v[152:155], v[192:195], v[52:55]
	v_mfma_f32_16x16x32_bf16 v[44:47], v[160:163], v[192:195], v[44:47]
	v_mfma_f32_16x16x32_bf16 v[40:43], v[152:155], v[226:229], v[40:43]
	v_mfma_f32_16x16x32_bf16 v[32:35], v[160:163], v[226:229], v[32:35]
	v_mfma_f32_16x16x32_bf16 v[24:27], v[152:155], v[234:237], v[24:27]
	v_mfma_f32_16x16x32_bf16 v[16:19], v[160:163], v[234:237], v[16:19]
	s_setprio 0
	s_setprio 1
	v_mfma_f32_16x16x32_bf16 v[56:59], v[164:167], v[180:183], v[56:59]
	v_mfma_f32_16x16x32_bf16 v[48:51], v[172:175], v[180:183], v[48:51]
	v_mfma_f32_16x16x32_bf16 v[36:39], v[164:167], v[188:191], v[36:39]
	v_mfma_f32_16x16x32_bf16 v[28:31], v[172:175], v[188:191], v[28:31]
	v_mfma_f32_16x16x32_bf16 v[20:23], v[164:167], v[210:213], v[20:23]
	v_mfma_f32_16x16x32_bf16 v[12:15], v[172:175], v[210:213], v[12:15]
	v_mfma_f32_16x16x32_bf16 v[8:11], v[164:167], v[230:233], v[8:11]
	v_mfma_f32_16x16x32_bf16 v[4:7], v[172:175], v[230:233], v[4:7]
	v_mfma_f32_16x16x32_bf16 v[56:59], v[168:171], v[184:187], v[56:59]
	v_mfma_f32_16x16x32_bf16 v[48:51], v[176:179], v[184:187], v[48:51]
	v_mfma_f32_16x16x32_bf16 v[36:39], v[168:171], v[192:195], v[36:39]
	v_mfma_f32_16x16x32_bf16 v[28:31], v[176:179], v[192:195], v[28:31]
	v_mfma_f32_16x16x32_bf16 v[20:23], v[168:171], v[226:229], v[20:23]
	v_mfma_f32_16x16x32_bf16 v[12:15], v[176:179], v[226:229], v[12:15]
	v_mfma_f32_16x16x32_bf16 v[8:11], v[168:171], v[234:237], v[8:11]
	s_barrier
	v_mfma_f32_16x16x32_bf16 v[4:7], v[176:179], v[234:237], v[4:7]
	s_setprio 0
	s_add_i32 s33, 0, 0x18000
	v_add_u32_e32 v147, s33, v145
	s_add_i32 s34, 0, 0x1c000
	ds_read_b128 v[148:151], v147
	ds_read_b128 v[152:155], v147 offset:1024
	ds_read_b128 v[156:159], v147 offset:2048
	ds_read_b128 v[160:163], v147 offset:3072
	v_add_u32_e32 v147, s34, v145
	ds_read_b128 v[164:167], v147
	ds_read_b128 v[168:171], v147 offset:1024
	ds_read_b128 v[172:175], v147 offset:2048
	ds_read_b128 v[176:179], v147 offset:3072
	s_add_u32 s12, s12, 0x40000
	s_addc_u32 s13, s13, 0
	s_mov_b32 m0, s21
	v_lshl_add_u64 v[244:245], s[12:13], 0, v[132:133]
	ds_read_b128 v[180:183], v146 offset:32768
	ds_read_b128 v[184:187], v146 offset:33792
	ds_read_b128 v[188:191], v146 offset:34816
	ds_read_b128 v[192:195], v146 offset:35840
	ds_read_b128 v[210:213], v146 offset:36864
	ds_read_b128 v[226:229], v146 offset:37888
	ds_read_b128 v[230:233], v146 offset:38912
	ds_read_b128 v[234:237], v146 offset:39936
	global_load_lds_dwordx4 v[244:245], off
	v_lshl_add_u64 v[244:245], s[12:13], 0, v[136:137]
	s_mov_b32 m0, s24
	s_nop 0
	global_load_lds_dwordx4 v[244:245], off
	s_waitcnt vmcnt(8)
	s_waitcnt lgkmcnt(0)
	s_barrier
	s_setprio 1
	s_waitcnt lgkmcnt(0)
	v_mfma_f32_16x16x32_bf16 v[128:131], v[148:151], v[180:183], v[128:131]
	v_mfma_f32_16x16x32_bf16 v[124:127], v[156:159], v[180:183], v[124:127]
	v_mfma_f32_16x16x32_bf16 v[116:119], v[148:151], v[188:191], v[116:119]
	v_mfma_f32_16x16x32_bf16 v[108:111], v[156:159], v[188:191], v[108:111]
	v_mfma_f32_16x16x32_bf16 v[104:107], v[148:151], v[210:213], v[104:107]
	v_mfma_f32_16x16x32_bf16 v[96:99], v[156:159], v[210:213], v[96:99]
	v_mfma_f32_16x16x32_bf16 v[88:91], v[148:151], v[230:233], v[88:91]
	v_mfma_f32_16x16x32_bf16 v[80:83], v[156:159], v[230:233], v[80:83]
	v_mfma_f32_16x16x32_bf16 v[128:131], v[152:155], v[184:187], v[128:131]
	v_mfma_f32_16x16x32_bf16 v[124:127], v[160:163], v[184:187], v[124:127]
	v_mfma_f32_16x16x32_bf16 v[116:119], v[152:155], v[192:195], v[116:119]
	v_mfma_f32_16x16x32_bf16 v[108:111], v[160:163], v[192:195], v[108:111]
	v_mfma_f32_16x16x32_bf16 v[104:107], v[152:155], v[226:229], v[104:107]
	v_mfma_f32_16x16x32_bf16 v[96:99], v[160:163], v[226:229], v[96:99]
	v_mfma_f32_16x16x32_bf16 v[88:91], v[152:155], v[234:237], v[88:91]
	v_mfma_f32_16x16x32_bf16 v[80:83], v[160:163], v[234:237], v[80:83]
	s_setprio 0
	s_setprio 1
	v_mfma_f32_16x16x32_bf16 v[120:123], v[164:167], v[180:183], v[120:123]
	v_mfma_f32_16x16x32_bf16 v[112:115], v[172:175], v[180:183], v[112:115]
	v_mfma_f32_16x16x32_bf16 v[100:103], v[164:167], v[188:191], v[100:103]
	v_mfma_f32_16x16x32_bf16 v[92:95], v[172:175], v[188:191], v[92:95]
	v_mfma_f32_16x16x32_bf16 v[84:87], v[164:167], v[210:213], v[84:87]
	v_mfma_f32_16x16x32_bf16 v[76:79], v[172:175], v[210:213], v[76:79]
	v_mfma_f32_16x16x32_bf16 v[72:75], v[164:167], v[230:233], v[72:75]
	v_mfma_f32_16x16x32_bf16 v[68:71], v[172:175], v[230:233], v[68:71]
	v_mfma_f32_16x16x32_bf16 v[120:123], v[168:171], v[184:187], v[120:123]
	v_mfma_f32_16x16x32_bf16 v[112:115], v[176:179], v[184:187], v[112:115]
	v_mfma_f32_16x16x32_bf16 v[100:103], v[168:171], v[192:195], v[100:103]
	v_mfma_f32_16x16x32_bf16 v[92:95], v[176:179], v[192:195], v[92:95]
	v_mfma_f32_16x16x32_bf16 v[84:87], v[168:171], v[226:229], v[84:87]
	v_mfma_f32_16x16x32_bf16 v[76:79], v[176:179], v[226:229], v[76:79]
	v_mfma_f32_16x16x32_bf16 v[72:75], v[168:171], v[234:237], v[72:75]
	s_barrier
; #define PG8_STAGE(bufoff, gbase, voff) do { _Pragma("unroll") for (int _i = 0; _i < 2; ++_i) \
;         __builtin_amdgcn_global_load_lds((const unsigned*)((const char*)(gbase) + (voff)[_i]), (PG8_LAS unsigned*)(lds + (bufoff) + ldsw + _i * 8192), 16, 0, 0); } while (0)
; #define PG8_LDA(dst, b, h) do { _Pragma("unroll") for (int m = 0; m < 4; ++m) _Pragma("unroll") for (int k = 0; k < 2; ++k) dst[m][k] = *(const PG8_LAS bf16x8*)(lds + PG8_SA(b, h) + aoff + m * 2048 + k * 1024); } while (0)
; #define PG8_MMA(ai, bj, At, Bt) do { __builtin_amdgcn_s_setprio(1); _Pragma("unroll") for (int m = 0; m < 4; ++m) _Pragma("unroll") for (int n = 0; n < 2; ++n) _Pragma("unroll") for (int k = 0; k < 2; ++k) \
;         acc[ai][bj][m][n] = __builtin_amdgcn_mfma_f32_16x16x32_bf16(Bt[n][k], At[m][k], acc[ai][bj][m][n], 0, 0, 0); __builtin_amdgcn_s_setprio(0); } while (0)
; #define PG8_WAIT_V(n) asm volatile("s_waitcnt vmcnt(" #n ")" ::: "memory")
; #define PG8_WAIT_L(n) asm volatile("s_waitcnt lgkmcnt(" #n ")" ::: "memory")
; #define PG8_BAR __builtin_amdgcn_s_barrier()
; #define PG8_SCHED __builtin_amdgcn_sched_barrier(0)
; template <class Epi, class Sched, bool ALIGN_EPI = false, bool SP2 = false>
; __device__ __forceinline__ void gemm_phase(PG8_LAS unsigned char* lds, const Gemm g, const Sched& S, const Epi& E) {
;     ...
;             PG8_WAIT_V(8); PG8_WAIT_L(0); PG8_BAR; PG8_MMA(0, 0, At, B0); PG8_MMA(0, 1, At, B1); PG8_BAR; PG8_SCHED;
;             PG8_LDA(At, 1, 1); PG8_STAGE(PG8_SB(1, 0), b3, voffB); PG8_STAGE(PG8_SB(1, 1), b3 + hstepB, voffB); PG8_STAGE(PG8_SA(1, 0), a3, voffA);
;             PG8_WAIT_V(8); PG8_WAIT_L(0); PG8_BAR; PG8_MMA(1, 0, At, B0); PG8_MMA(1, 1, At, B1); PG8_BAR; PG8_SCHED;
	v_mfma_f32_16x16x32_bf16 v[68:71], v[176:179], v[234:237], v[68:71]
	s_setprio 0
	s_add_i32 s12, s33, s18
	v_lshl_add_u64 v[196:197], v[196:197], 0, s[64:65]
	s_mov_b32 m0, s12
	ds_read_b128 v[180:183], v146 offset:49152
	ds_read_b128 v[184:187], v146 offset:50176
	ds_read_b128 v[188:191], v146 offset:51200
	ds_read_b128 v[192:195], v146 offset:52224
	ds_read_b128 v[210:213], v146 offset:53248
	ds_read_b128 v[226:229], v146 offset:54272
	ds_read_b128 v[230:233], v146 offset:55296
	ds_read_b128 v[234:237], v146 offset:56320
	global_load_lds_dwordx4 v[196:197], off
	s_add_i32 m0, s12, 0x2000
	s_add_u32 s10, s10, 0x40080
	v_lshl_add_u64 v[196:197], v[238:239], 0, s[64:65]
	s_addc_u32 s11, s11, 0
	s_add_i32 s12, s34, s18
	global_load_lds_dwordx4 v[196:197], off
	v_lshl_add_u64 v[196:197], s[10:11], 0, v[134:135]
	s_mov_b32 m0, s12
	s_nop 0
	global_load_lds_dwordx4 v[196:197], off
	v_lshl_add_u64 v[196:197], s[10:11], 0, v[138:139]
	s_add_i32 m0, s12, 0x2000
	s_nop 0
	global_load_lds_dwordx4 v[196:197], off
	v_lshl_add_u64 v[196:197], v[240:241], 0, s[64:65]
	s_mov_b32 m0, s26
	s_nop 0
	global_load_lds_dwordx4 v[196:197], off
	v_lshl_add_u64 v[196:197], v[242:243], 0, s[64:65]
	s_mov_b32 m0, s27
	s_nop 0
	global_load_lds_dwordx4 v[196:197], off
	s_waitcnt vmcnt(8)
	s_waitcnt lgkmcnt(0)
	s_barrier
	s_setprio 1
	s_waitcnt lgkmcnt(0)
	v_mfma_f32_16x16x32_bf16 v[64:67], v[148:151], v[180:183], v[64:67]
	v_mfma_f32_16x16x32_bf16 v[60:63], v[156:159], v[180:183], v[60:63]
	v_mfma_f32_16x16x32_bf16 v[52:55], v[148:151], v[188:191], v[52:55]
	v_mfma_f32_16x16x32_bf16 v[44:47], v[156:159], v[188:191], v[44:47]
	v_mfma_f32_16x16x32_bf16 v[40:43], v[148:151], v[210:213], v[40:43]
	v_mfma_f32_16x16x32_bf16 v[32:35], v[156:159], v[210:213], v[32:35]
	v_mfma_f32_16x16x32_bf16 v[24:27], v[148:151], v[230:233], v[24:27]
	v_mfma_f32_16x16x32_bf16 v[16:19], v[156:159], v[230:233], v[16:19]
	v_mfma_f32_16x16x32_bf16 v[64:67], v[152:155], v[184:187], v[64:67]
	v_mfma_f32_16x16x32_bf16 v[60:63], v[160:163], v[184:187], v[60:63]
	v_mfma_f32_16x16x32_bf16 v[52:55], v[152:155], v[192:195], v[52:55]
	v_mfma_f32_16x16x32_bf16 v[44:47], v[160:163], v[192:195], v[44:47]
	v_mfma_f32_16x16x32_bf16 v[40:43], v[152:155], v[226:229], v[40:43]
	v_mfma_f32_16x16x32_bf16 v[32:35], v[160:163], v[226:229], v[32:35]
	v_mfma_f32_16x16x32_bf16 v[24:27], v[152:155], v[234:237], v[24:27]
	v_mfma_f32_16x16x32_bf16 v[16:19], v[160:163], v[234:237], v[16:19]
	s_setprio 0
	s_setprio 1
	v_mfma_f32_16x16x32_bf16 v[56:59], v[164:167], v[180:183], v[56:59]
	v_mfma_f32_16x16x32_bf16 v[48:51], v[172:175], v[180:183], v[48:51]
	v_mfma_f32_16x16x32_bf16 v[36:39], v[164:167], v[188:191], v[36:39]
	v_mfma_f32_16x16x32_bf16 v[28:31], v[172:175], v[188:191], v[28:31]
	v_mfma_f32_16x16x32_bf16 v[20:23], v[164:167], v[210:213], v[20:23]
	v_mfma_f32_16x16x32_bf16 v[12:15], v[172:175], v[210:213], v[12:15]
	v_mfma_f32_16x16x32_bf16 v[8:11], v[164:167], v[230:233], v[8:11]
	v_mfma_f32_16x16x32_bf16 v[4:7], v[172:175], v[230:233], v[4:7]
	v_mfma_f32_16x16x32_bf16 v[56:59], v[168:171], v[184:187], v[56:59]
	v_mfma_f32_16x16x32_bf16 v[48:51], v[176:179], v[184:187], v[48:51]
	v_mfma_f32_16x16x32_bf16 v[36:39], v[168:171], v[192:195], v[36:39]
	v_mfma_f32_16x16x32_bf16 v[28:31], v[176:179], v[192:195], v[28:31]
	v_mfma_f32_16x16x32_bf16 v[20:23], v[168:171], v[226:229], v[20:23]
	v_mfma_f32_16x16x32_bf16 v[12:15], v[176:179], v[226:229], v[12:15]
	v_mfma_f32_16x16x32_bf16 v[8:11], v[168:171], v[234:237], v[8:11]
	s_barrier
	v_mfma_f32_16x16x32_bf16 v[4:7], v[176:179], v[234:237], v[4:7]
	s_setprio 0
	s_add_i32 s31, s31, 2
	s_add_u32 s8, s8, 0x100
	s_addc_u32 s9, s9, 0
	s_cmp_gt_u32 s31, 13
	s_cbranch_scc0 .LBB0_1247
	s_cmpk_lt_u32 s16, 0x100
	s_cbranch_scc0 .LBB0_1250
	s_barrier

; #define PG8_STAGE(bufoff, gbase, voff) do { _Pragma("unroll") for (int _i = 0; _i < 2; ++_i) \
;         __builtin_amdgcn_global_load_lds((const unsigned*)((const char*)(gbase) + (voff)[_i]), (PG8_LAS unsigned*)(lds + (bufoff) + ldsw + _i * 8192), 16, 0, 0); } while (0)
; #define PG8_LDA(dst, b, h) do { _Pragma("unroll") for (int m = 0; m < 4; ++m) _Pragma("unroll") for (int k = 0; k < 2; ++k) dst[m][k] = *(const PG8_LAS bf16x8*)(lds + PG8_SA(b, h) + aoff + m * 2048 + k * 1024); } while (0)
; #define PG8_LDB(dst, b, h) do { _Pragma("unroll") for (int n = 0; n < 2; ++n) _Pragma("unroll") for (int k = 0; k < 2; ++k) dst[n][k] = *(const PG8_LAS bf16x8*)(lds + PG8_SB(b, h) + boff + n * 2048 + k * 1024); } while (0)
; #define PG8_MMA(ai, bj, At, Bt) do { __builtin_amdgcn_s_setprio(1); _Pragma("unroll") for (int m = 0; m < 4; ++m) _Pragma("unroll") for (int n = 0; n < 2; ++n) _Pragma("unroll") for (int k = 0; k < 2; ++k) \
;         acc[ai][bj][m][n] = __builtin_amdgcn_mfma_f32_16x16x32_bf16(Bt[n][k], At[m][k], acc[ai][bj][m][n], 0, 0, 0); __builtin_amdgcn_s_setprio(0); } while (0)
; #define PG8_WAIT_V(n) asm volatile("s_waitcnt vmcnt(" #n ")" ::: "memory")
; #define PG8_WAIT_L(n) asm volatile("s_waitcnt lgkmcnt(" #n ")" ::: "memory")
; template <class Epi, class Sched, bool ALIGN_EPI = false, bool SP2 = false>
; __device__ __forceinline__ void gemm_phase(PG8_LAS unsigned char* lds, const Gemm g, const Sched& S, const Epi& E) {
;     ...
;             const bool last = (t == nt - 2);
;             const char* a1 = cA + (size_t)(t + 1) * kstep;
;             const char* a2 = last ? nA : cA + (size_t)(t + 2) * kstep; const char* b2 = last ? nB : cB + (size_t)(t + 2) * kstep;
;             const char* a3 = a2 + kstep; const char* b3 = b2 + kstep;
;             if (last && has_next) S.a_ready(nxt);
;             if constexpr (SP2) {
;             PG8_LDB(B0, 0, 0); PG8_LDB(B1, 0, 1); PG8_SCHED; PG8_LDA(At, 0, 0); PG8_STAGE(PG8_SA(1, 1), a1 + hstepA, voffA);
;             PG8_WAIT_V(8); PG8_WAIT_L(0); PG8_BAR; PG8_MMA(0, 0, At, B0); PG8_MMA(0, 1, At, B1); PG8_BAR; PG8_SCHED;
;             PG8_LDA(At, 0, 1); PG8_STAGE(PG8_SB(0, 0), b2, voffB); PG8_STAGE(PG8_SB(0, 1), b2 + hstepB, voffB); PG8_STAGE(PG8_SA(0, 0), a2, voffA);
;             PG8_WAIT_V(8); PG8_WAIT_L(0); PG8_BAR; PG8_MMA(1, 0, At, B0); PG8_MMA(1, 1, At, B1); PG8_BAR; PG8_SCHED;
.LBB0_1693:
	s_add_u32 s22, s20, 0xfffc0080
	s_addc_u32 s23, s21, -1
	s_add_i32 s46, 0, 0x10000
	s_cmp_eq_u32 s45, 12
	s_cselect_b32 s25, s13, s23
	s_cselect_b32 s24, s41, s22
	v_add_u32_e32 v144, s46, v146
	s_cselect_b32 s23, s11, s44
	s_cselect_b32 s22, s42, s43
	s_add_i32 s48, 0, 0x14000
	ds_read_b128 v[150:153], v144
	ds_read_b128 v[154:157], v144 offset:1024
	ds_read_b128 v[158:161], v144 offset:2048
	ds_read_b128 v[162:165], v144 offset:3072
	v_add_u32_e32 v144, s48, v146
	ds_read_b128 v[166:169], v144
	ds_read_b128 v[170:173], v144 offset:1024
	ds_read_b128 v[174:177], v144 offset:2048
	ds_read_b128 v[178:181], v144 offset:3072
	v_lshl_add_u64 v[144:145], s[20:21], 0, v[142:143]
	s_add_i32 m0, s15, 0xc000
	ds_read_b128 v[182:185], v148
	ds_read_b128 v[186:189], v148 offset:1024
	ds_read_b128 v[190:193], v148 offset:2048
	ds_read_b128 v[194:197], v148 offset:3072
	ds_read_b128 v[210:213], v148 offset:4096
	ds_read_b128 v[226:229], v148 offset:5120
	ds_read_b128 v[230:233], v148 offset:6144
	ds_read_b128 v[234:237], v148 offset:7168
	v_lshl_add_u64 v[244:245], v[240:241], 0, s[64:65]
	s_mov_b32 m0, s36
	s_nop 0
	global_load_lds_dwordx4 v[244:245], off
	v_lshl_add_u64 v[244:245], v[242:243], 0, s[64:65]
	s_mov_b32 m0, s37
	s_nop 0
	global_load_lds_dwordx4 v[244:245], off
	s_add_i32 m0, s15, 0xc000
	s_nop 0
	global_load_lds_dwordx4 v[144:145], off
	v_lshl_add_u64 v[144:145], s[20:21], 0, v[140:141]
	s_add_i32 m0, s15, 0xe000
	s_nop 0
	global_load_lds_dwordx4 v[144:145], off
	s_waitcnt vmcnt(8)
	s_waitcnt lgkmcnt(0)
	s_barrier
	s_setprio 1
	s_waitcnt lgkmcnt(0)
	v_mfma_f32_16x16x32_bf16 v[128:131], v[150:153], v[182:185], v[128:131]
	v_mfma_f32_16x16x32_bf16 v[124:127], v[158:161], v[182:185], v[124:127]
	v_mfma_f32_16x16x32_bf16 v[120:123], v[150:153], v[190:193], v[120:123]
	v_mfma_f32_16x16x32_bf16 v[112:115], v[158:161], v[190:193], v[112:115]
	v_mfma_f32_16x16x32_bf16 v[104:107], v[150:153], v[210:213], v[104:107]
	v_mfma_f32_16x16x32_bf16 v[96:99], v[158:161], v[210:213], v[96:99]
	v_mfma_f32_16x16x32_bf16 v[88:91], v[150:153], v[230:233], v[88:91]
	v_mfma_f32_16x16x32_bf16 v[80:83], v[158:161], v[230:233], v[80:83]
	v_mfma_f32_16x16x32_bf16 v[128:131], v[154:157], v[186:189], v[128:131]
	v_mfma_f32_16x16x32_bf16 v[124:127], v[162:165], v[186:189], v[124:127]
	v_mfma_f32_16x16x32_bf16 v[120:123], v[154:157], v[194:197], v[120:123]
	v_mfma_f32_16x16x32_bf16 v[112:115], v[162:165], v[194:197], v[112:115]
	v_mfma_f32_16x16x32_bf16 v[104:107], v[154:157], v[226:229], v[104:107]
	v_mfma_f32_16x16x32_bf16 v[96:99], v[162:165], v[226:229], v[96:99]
	v_mfma_f32_16x16x32_bf16 v[88:91], v[154:157], v[234:237], v[88:91]
	v_mfma_f32_16x16x32_bf16 v[80:83], v[162:165], v[234:237], v[80:83]
	s_setprio 0
	s_setprio 1
	v_mfma_f32_16x16x32_bf16 v[116:119], v[166:169], v[182:185], v[116:119]
	v_mfma_f32_16x16x32_bf16 v[108:111], v[174:177], v[182:185], v[108:111]
	v_mfma_f32_16x16x32_bf16 v[100:103], v[166:169], v[190:193], v[100:103]
	v_mfma_f32_16x16x32_bf16 v[92:95], v[174:177], v[190:193], v[92:95]
	v_mfma_f32_16x16x32_bf16 v[84:87], v[166:169], v[210:213], v[84:87]
	v_mfma_f32_16x16x32_bf16 v[76:79], v[174:177], v[210:213], v[76:79]
	v_mfma_f32_16x16x32_bf16 v[72:75], v[166:169], v[230:233], v[72:75]
	v_mfma_f32_16x16x32_bf16 v[68:71], v[174:177], v[230:233], v[68:71]
	v_mfma_f32_16x16x32_bf16 v[116:119], v[170:173], v[186:189], v[116:119]
	v_mfma_f32_16x16x32_bf16 v[108:111], v[178:181], v[186:189], v[108:111]
	v_mfma_f32_16x16x32_bf16 v[100:103], v[170:173], v[194:197], v[100:103]
	v_mfma_f32_16x16x32_bf16 v[92:95], v[178:181], v[194:197], v[92:95]
	v_mfma_f32_16x16x32_bf16 v[84:87], v[170:173], v[226:229], v[84:87]
	v_mfma_f32_16x16x32_bf16 v[76:79], v[178:181], v[226:229], v[76:79]
	v_mfma_f32_16x16x32_bf16 v[72:75], v[170:173], v[234:237], v[72:75]
	s_barrier
	v_mfma_f32_16x16x32_bf16 v[68:71], v[178:181], v[234:237], v[68:71]
	s_setprio 0
	s_add_i32 s46, s46, s31
	v_lshl_add_u64 v[144:145], s[22:23], 0, v[134:135]
	s_mov_b32 m0, s46
	ds_read_b128 v[182:185], v148 offset:16384
	ds_read_b128 v[186:189], v148 offset:17408
	ds_read_b128 v[190:193], v148 offset:18432
	ds_read_b128 v[194:197], v148 offset:19456
	ds_read_b128 v[210:213], v148 offset:20480
	ds_read_b128 v[226:229], v148 offset:21504
	ds_read_b128 v[230:233], v148 offset:22528
	ds_read_b128 v[234:237], v148 offset:23552
	global_load_lds_dwordx4 v[144:145], off
	s_add_i32 m0, s46, 0x2000
	s_add_u32 s46, s22, 0x40000
	v_lshl_add_u64 v[238:239], s[22:23], 0, v[138:139]
	s_addc_u32 s47, s23, 0
	s_add_i32 s48, s48, s31
	global_load_lds_dwordx4 v[238:239], off
	v_lshl_add_u64 v[240:241], s[46:47], 0, v[134:135]
	s_mov_b32 m0, s48
	v_lshl_add_u64 v[242:243], s[24:25], 0, v[136:137]
	global_load_lds_dwordx4 v[240:241], off
	v_lshl_add_u64 v[240:241], s[46:47], 0, v[138:139]
	s_add_i32 m0, s48, 0x2000
	s_nop 0
	global_load_lds_dwordx4 v[240:241], off
	v_lshl_add_u64 v[240:241], s[24:25], 0, v[132:133]
	s_waitcnt vmcnt(6)
	s_waitcnt lgkmcnt(0)
	s_barrier
; #define PG8_STAGE(bufoff, gbase, voff) do { _Pragma("unroll") for (int _i = 0; _i < 2; ++_i) \
;         __builtin_amdgcn_global_load_lds((const unsigned*)((const char*)(gbase) + (voff)[_i]), (PG8_LAS unsigned*)(lds + (bufoff) + ldsw + _i * 8192), 16, 0, 0); } while (0)
; #define PG8_LDA(dst, b, h) do { _Pragma("unroll") for (int m = 0; m < 4; ++m) _Pragma("unroll") for (int k = 0; k < 2; ++k) dst[m][k] = *(const PG8_LAS bf16x8*)(lds + PG8_SA(b, h) + aoff + m * 2048 + k * 1024); } while (0)
; #define PG8_LDB(dst, b, h) do { _Pragma("unroll") for (int n = 0; n < 2; ++n) _Pragma("unroll") for (int k = 0; k < 2; ++k) dst[n][k] = *(const PG8_LAS bf16x8*)(lds + PG8_SB(b, h) + boff + n * 2048 + k * 1024); } while (0)
; #define PG8_MMA(ai, bj, At, Bt) do { __builtin_amdgcn_s_setprio(1); _Pragma("unroll") for (int m = 0; m < 4; ++m) _Pragma("unroll") for (int n = 0; n < 2; ++n) _Pragma("unroll") for (int k = 0; k < 2; ++k) \
;         acc[ai][bj][m][n] = __builtin_amdgcn_mfma_f32_16x16x32_bf16(Bt[n][k], At[m][k], acc[ai][bj][m][n], 0, 0, 0); __builtin_amdgcn_s_setprio(0); } while (0)
; #define PG8_WAIT_V(n) asm volatile("s_waitcnt vmcnt(" #n ")" ::: "memory")
; #define PG8_WAIT_L(n) asm volatile("s_waitcnt lgkmcnt(" #n ")" ::: "memory")
; #define PG8_BAR __builtin_amdgcn_s_barrier()
; #define PG8_SCHED __builtin_amdgcn_sched_barrier(0)
; template <class Epi, class Sched, bool ALIGN_EPI = false, bool SP2 = false>
; __device__ __forceinline__ void gemm_phase(PG8_LAS unsigned char* lds, const Gemm g, const Sched& S, const Epi& E) {
;     ...
;             PG8_WAIT_V(8); PG8_WAIT_L(0); PG8_BAR; PG8_MMA(1, 0, At, B0); PG8_MMA(1, 1, At, B1); PG8_BAR; PG8_SCHED;
;             PG8_LDB(B0, 1, 0); PG8_LDB(B1, 1, 1); PG8_SCHED; PG8_LDA(At, 1, 0); PG8_STAGE(PG8_SA(0, 1), a2 + hstepA, voffA);
;             PG8_WAIT_V(8); PG8_WAIT_L(0); PG8_BAR; PG8_MMA(0, 0, At, B0); PG8_MMA(0, 1, At, B1); PG8_BAR; PG8_SCHED;
;             PG8_LDA(At, 1, 1); PG8_STAGE(PG8_SB(1, 0), b3, voffB); PG8_STAGE(PG8_SB(1, 1), b3 + hstepB, voffB); PG8_STAGE(PG8_SA(1, 0), a3, voffA);
	s_setprio 1
	s_waitcnt lgkmcnt(0)
	v_mfma_f32_16x16x32_bf16 v[64:67], v[150:153], v[182:185], v[64:67]
	v_mfma_f32_16x16x32_bf16 v[60:63], v[158:161], v[182:185], v[60:63]
	v_mfma_f32_16x16x32_bf16 v[56:59], v[150:153], v[190:193], v[56:59]
	v_mfma_f32_16x16x32_bf16 v[48:51], v[158:161], v[190:193], v[48:51]
	v_mfma_f32_16x16x32_bf16 v[40:43], v[150:153], v[210:213], v[40:43]
	v_mfma_f32_16x16x32_bf16 v[32:35], v[158:161], v[210:213], v[32:35]
	v_mfma_f32_16x16x32_bf16 v[24:27], v[150:153], v[230:233], v[24:27]
	v_mfma_f32_16x16x32_bf16 v[16:19], v[158:161], v[230:233], v[16:19]
	v_mfma_f32_16x16x32_bf16 v[64:67], v[154:157], v[186:189], v[64:67]
	v_mfma_f32_16x16x32_bf16 v[60:63], v[162:165], v[186:189], v[60:63]
	v_mfma_f32_16x16x32_bf16 v[56:59], v[154:157], v[194:197], v[56:59]
	v_mfma_f32_16x16x32_bf16 v[48:51], v[162:165], v[194:197], v[48:51]
	v_mfma_f32_16x16x32_bf16 v[40:43], v[154:157], v[226:229], v[40:43]
	v_mfma_f32_16x16x32_bf16 v[32:35], v[162:165], v[226:229], v[32:35]
	v_mfma_f32_16x16x32_bf16 v[24:27], v[154:157], v[234:237], v[24:27]
	v_mfma_f32_16x16x32_bf16 v[16:19], v[162:165], v[234:237], v[16:19]
	s_setprio 0
	s_setprio 1
	v_mfma_f32_16x16x32_bf16 v[52:55], v[166:169], v[182:185], v[52:55]
	v_mfma_f32_16x16x32_bf16 v[44:47], v[174:177], v[182:185], v[44:47]
	v_mfma_f32_16x16x32_bf16 v[36:39], v[166:169], v[190:193], v[36:39]
	v_mfma_f32_16x16x32_bf16 v[28:31], v[174:177], v[190:193], v[28:31]
	v_mfma_f32_16x16x32_bf16 v[20:23], v[166:169], v[210:213], v[20:23]
	v_mfma_f32_16x16x32_bf16 v[12:15], v[174:177], v[210:213], v[12:15]
	v_mfma_f32_16x16x32_bf16 v[8:11], v[166:169], v[230:233], v[8:11]
	v_mfma_f32_16x16x32_bf16 v[4:7], v[174:177], v[230:233], v[4:7]
	v_mfma_f32_16x16x32_bf16 v[52:55], v[170:173], v[186:189], v[52:55]
	v_mfma_f32_16x16x32_bf16 v[44:47], v[178:181], v[186:189], v[44:47]
	v_mfma_f32_16x16x32_bf16 v[36:39], v[170:173], v[194:197], v[36:39]
	v_mfma_f32_16x16x32_bf16 v[28:31], v[178:181], v[194:197], v[28:31]
	v_mfma_f32_16x16x32_bf16 v[20:23], v[170:173], v[226:229], v[20:23]
	v_mfma_f32_16x16x32_bf16 v[12:15], v[178:181], v[226:229], v[12:15]
	v_mfma_f32_16x16x32_bf16 v[8:11], v[170:173], v[234:237], v[8:11]
	s_barrier
	v_mfma_f32_16x16x32_bf16 v[4:7], v[178:181], v[234:237], v[4:7]
	s_setprio 0
	s_add_i32 s46, 0, 0x18000
	v_add_u32_e32 v149, s46, v146
	s_add_i32 s47, 0, 0x1c000
	ds_read_b128 v[150:153], v149
	ds_read_b128 v[154:157], v149 offset:1024
	ds_read_b128 v[158:161], v149 offset:2048
	ds_read_b128 v[162:165], v149 offset:3072
	v_add_u32_e32 v149, s47, v146
	ds_read_b128 v[166:169], v149
	ds_read_b128 v[170:173], v149 offset:1024
	ds_read_b128 v[174:177], v149 offset:2048
	ds_read_b128 v[178:181], v149 offset:3072
	s_add_u32 s24, s24, 0x40000
	s_addc_u32 s25, s25, 0
	s_mov_b32 m0, s34
	v_lshl_add_u64 v[244:245], s[24:25], 0, v[132:133]
	ds_read_b128 v[182:185], v148 offset:32768
	ds_read_b128 v[186:189], v148 offset:33792
	ds_read_b128 v[190:193], v148 offset:34816
	ds_read_b128 v[194:197], v148 offset:35840
	ds_read_b128 v[210:213], v148 offset:36864
	ds_read_b128 v[226:229], v148 offset:37888
	ds_read_b128 v[230:233], v148 offset:38912
	ds_read_b128 v[234:237], v148 offset:39936
	s_mov_b32 m0, s15
	s_nop 0
	global_load_lds_dwordx4 v[240:241], off
	s_mov_b32 m0, s33
	s_nop 0
	global_load_lds_dwordx4 v[242:243], off
	s_mov_b32 m0, s34
	s_nop 0
	global_load_lds_dwordx4 v[244:245], off
	v_lshl_add_u64 v[244:245], s[24:25], 0, v[136:137]
	s_mov_b32 m0, s35
	s_nop 0
	global_load_lds_dwordx4 v[244:245], off
	s_waitcnt vmcnt(8)
	s_waitcnt lgkmcnt(0)
	s_barrier
	s_setprio 1
	s_waitcnt lgkmcnt(0)
	v_mfma_f32_16x16x32_bf16 v[128:131], v[150:153], v[182:185], v[128:131]
	v_mfma_f32_16x16x32_bf16 v[124:127], v[158:161], v[182:185], v[124:127]
	v_mfma_f32_16x16x32_bf16 v[120:123], v[150:153], v[190:193], v[120:123]
	v_mfma_f32_16x16x32_bf16 v[112:115], v[158:161], v[190:193], v[112:115]
	v_mfma_f32_16x16x32_bf16 v[104:107], v[150:153], v[210:213], v[104:107]
	v_mfma_f32_16x16x32_bf16 v[96:99], v[158:161], v[210:213], v[96:99]
	v_mfma_f32_16x16x32_bf16 v[88:91], v[150:153], v[230:233], v[88:91]
	v_mfma_f32_16x16x32_bf16 v[80:83], v[158:161], v[230:233], v[80:83]
	v_mfma_f32_16x16x32_bf16 v[128:131], v[154:157], v[186:189], v[128:131]
	v_mfma_f32_16x16x32_bf16 v[124:127], v[162:165], v[186:189], v[124:127]
	v_mfma_f32_16x16x32_bf16 v[120:123], v[154:157], v[194:197], v[120:123]
	v_mfma_f32_16x16x32_bf16 v[112:115], v[162:165], v[194:197], v[112:115]
	v_mfma_f32_16x16x32_bf16 v[104:107], v[154:157], v[226:229], v[104:107]
	v_mfma_f32_16x16x32_bf16 v[96:99], v[162:165], v[226:229], v[96:99]
	v_mfma_f32_16x16x32_bf16 v[88:91], v[154:157], v[234:237], v[88:91]
	v_mfma_f32_16x16x32_bf16 v[80:83], v[162:165], v[234:237], v[80:83]
	s_setprio 0
	s_setprio 1
	v_mfma_f32_16x16x32_bf16 v[116:119], v[166:169], v[182:185], v[116:119]
	v_mfma_f32_16x16x32_bf16 v[108:111], v[174:177], v[182:185], v[108:111]
	v_mfma_f32_16x16x32_bf16 v[100:103], v[166:169], v[190:193], v[100:103]
	v_mfma_f32_16x16x32_bf16 v[92:95], v[174:177], v[190:193], v[92:95]
	v_mfma_f32_16x16x32_bf16 v[84:87], v[166:169], v[210:213], v[84:87]
	v_mfma_f32_16x16x32_bf16 v[76:79], v[174:177], v[210:213], v[76:79]
	v_mfma_f32_16x16x32_bf16 v[72:75], v[166:169], v[230:233], v[72:75]
	v_mfma_f32_16x16x32_bf16 v[68:71], v[174:177], v[230:233], v[68:71]
	v_mfma_f32_16x16x32_bf16 v[116:119], v[170:173], v[186:189], v[116:119]
	v_mfma_f32_16x16x32_bf16 v[108:111], v[178:181], v[186:189], v[108:111]
	v_mfma_f32_16x16x32_bf16 v[100:103], v[170:173], v[194:197], v[100:103]
	v_mfma_f32_16x16x32_bf16 v[92:95], v[178:181], v[194:197], v[92:95]
	v_mfma_f32_16x16x32_bf16 v[84:87], v[170:173], v[226:229], v[84:87]
	v_mfma_f32_16x16x32_bf16 v[76:79], v[178:181], v[226:229], v[76:79]
	v_mfma_f32_16x16x32_bf16 v[72:75], v[170:173], v[234:237], v[72:75]
	s_barrier
; #define PG8_STAGE(bufoff, gbase, voff) do { _Pragma("unroll") for (int _i = 0; _i < 2; ++_i) \
;         __builtin_amdgcn_global_load_lds((const unsigned*)((const char*)(gbase) + (voff)[_i]), (PG8_LAS unsigned*)(lds + (bufoff) + ldsw + _i * 8192), 16, 0, 0); } while (0)
; #define PG8_LDA(dst, b, h) do { _Pragma("unroll") for (int m = 0; m < 4; ++m) _Pragma("unroll") for (int k = 0; k < 2; ++k) dst[m][k] = *(const PG8_LAS bf16x8*)(lds + PG8_SA(b, h) + aoff + m * 2048 + k * 1024); } while (0)
; #define PG8_MMA(ai, bj, At, Bt) do { __builtin_amdgcn_s_setprio(1); _Pragma("unroll") for (int m = 0; m < 4; ++m) _Pragma("unroll") for (int n = 0; n < 2; ++n) _Pragma("unroll") for (int k = 0; k < 2; ++k) \
;         acc[ai][bj][m][n] = __builtin_amdgcn_mfma_f32_16x16x32_bf16(Bt[n][k], At[m][k], acc[ai][bj][m][n], 0, 0, 0); __builtin_amdgcn_s_setprio(0); } while (0)
; #define PG8_WAIT_V(n) asm volatile("s_waitcnt vmcnt(" #n ")" ::: "memory")
; #define PG8_WAIT_L(n) asm volatile("s_waitcnt lgkmcnt(" #n ")" ::: "memory")
; #define PG8_BAR __builtin_amdgcn_s_barrier()
; #define PG8_SCHED __builtin_amdgcn_sched_barrier(0)
; template <class Epi, class Sched, bool ALIGN_EPI = false, bool SP2 = false>
; __device__ __forceinline__ void gemm_phase(PG8_LAS unsigned char* lds, const Gemm g, const Sched& S, const Epi& E) {
;     ...
;             PG8_WAIT_V(8); PG8_WAIT_L(0); PG8_BAR; PG8_MMA(0, 0, At, B0); PG8_MMA(0, 1, At, B1); PG8_BAR; PG8_SCHED;
;             PG8_LDA(At, 1, 1); PG8_STAGE(PG8_SB(1, 0), b3, voffB); PG8_STAGE(PG8_SB(1, 1), b3 + hstepB, voffB); PG8_STAGE(PG8_SA(1, 0), a3, voffA);
;             PG8_WAIT_V(8); PG8_WAIT_L(0); PG8_BAR; PG8_MMA(1, 0, At, B0); PG8_MMA(1, 1, At, B1); PG8_BAR; PG8_SCHED;
;     ...
;         if constexpr (ALIGN_EPI) { if (wr == 0) PG8_BAR; }
	v_mfma_f32_16x16x32_bf16 v[68:71], v[178:181], v[234:237], v[68:71]
	s_setprio 0
	s_add_i32 s24, s46, s31
	v_lshl_add_u64 v[144:145], v[144:145], 0, s[64:65]
	s_mov_b32 m0, s24
	ds_read_b128 v[182:185], v148 offset:49152
	ds_read_b128 v[186:189], v148 offset:50176
	ds_read_b128 v[190:193], v148 offset:51200
	ds_read_b128 v[194:197], v148 offset:52224
	ds_read_b128 v[210:213], v148 offset:53248
	ds_read_b128 v[226:229], v148 offset:54272
	ds_read_b128 v[230:233], v148 offset:55296
	ds_read_b128 v[234:237], v148 offset:56320
	global_load_lds_dwordx4 v[144:145], off
	s_add_i32 m0, s24, 0x2000
	s_add_u32 s22, s22, 0x40080
	v_lshl_add_u64 v[144:145], v[238:239], 0, s[64:65]
	s_addc_u32 s23, s23, 0
	s_add_i32 s24, s47, s31
	global_load_lds_dwordx4 v[144:145], off
	v_lshl_add_u64 v[144:145], s[22:23], 0, v[134:135]
	s_mov_b32 m0, s24
	s_nop 0
	global_load_lds_dwordx4 v[144:145], off
	v_lshl_add_u64 v[144:145], s[22:23], 0, v[138:139]
	s_add_i32 m0, s24, 0x2000
	s_nop 0
	global_load_lds_dwordx4 v[144:145], off
	s_waitcnt vmcnt(6)
	s_waitcnt lgkmcnt(0)
	s_barrier
	s_setprio 1
	s_waitcnt lgkmcnt(0)
	v_mfma_f32_16x16x32_bf16 v[64:67], v[150:153], v[182:185], v[64:67]
	v_mfma_f32_16x16x32_bf16 v[60:63], v[158:161], v[182:185], v[60:63]
	v_mfma_f32_16x16x32_bf16 v[56:59], v[150:153], v[190:193], v[56:59]
	v_mfma_f32_16x16x32_bf16 v[48:51], v[158:161], v[190:193], v[48:51]
	v_mfma_f32_16x16x32_bf16 v[40:43], v[150:153], v[210:213], v[40:43]
	v_mfma_f32_16x16x32_bf16 v[32:35], v[158:161], v[210:213], v[32:35]
	v_mfma_f32_16x16x32_bf16 v[24:27], v[150:153], v[230:233], v[24:27]
	v_mfma_f32_16x16x32_bf16 v[16:19], v[158:161], v[230:233], v[16:19]
	v_mfma_f32_16x16x32_bf16 v[64:67], v[154:157], v[186:189], v[64:67]
	v_mfma_f32_16x16x32_bf16 v[60:63], v[162:165], v[186:189], v[60:63]
	v_mfma_f32_16x16x32_bf16 v[56:59], v[154:157], v[194:197], v[56:59]
	v_mfma_f32_16x16x32_bf16 v[48:51], v[162:165], v[194:197], v[48:51]
	v_mfma_f32_16x16x32_bf16 v[40:43], v[154:157], v[226:229], v[40:43]
	v_mfma_f32_16x16x32_bf16 v[32:35], v[162:165], v[226:229], v[32:35]
	v_mfma_f32_16x16x32_bf16 v[24:27], v[154:157], v[234:237], v[24:27]
	v_mfma_f32_16x16x32_bf16 v[16:19], v[162:165], v[234:237], v[16:19]
	s_setprio 0
	s_setprio 1
	v_mfma_f32_16x16x32_bf16 v[52:55], v[166:169], v[182:185], v[52:55]
	v_mfma_f32_16x16x32_bf16 v[44:47], v[174:177], v[182:185], v[44:47]
	v_mfma_f32_16x16x32_bf16 v[36:39], v[166:169], v[190:193], v[36:39]
	v_mfma_f32_16x16x32_bf16 v[28:31], v[174:177], v[190:193], v[28:31]
	v_mfma_f32_16x16x32_bf16 v[20:23], v[166:169], v[210:213], v[20:23]
	v_mfma_f32_16x16x32_bf16 v[12:15], v[174:177], v[210:213], v[12:15]
	v_mfma_f32_16x16x32_bf16 v[8:11], v[166:169], v[230:233], v[8:11]
	v_mfma_f32_16x16x32_bf16 v[4:7], v[174:177], v[230:233], v[4:7]
	v_mfma_f32_16x16x32_bf16 v[52:55], v[170:173], v[186:189], v[52:55]
	v_mfma_f32_16x16x32_bf16 v[44:47], v[178:181], v[186:189], v[44:47]
	v_mfma_f32_16x16x32_bf16 v[36:39], v[170:173], v[194:197], v[36:39]
	v_mfma_f32_16x16x32_bf16 v[28:31], v[178:181], v[194:197], v[28:31]
	v_mfma_f32_16x16x32_bf16 v[20:23], v[170:173], v[226:229], v[20:23]
	v_mfma_f32_16x16x32_bf16 v[12:15], v[178:181], v[226:229], v[12:15]
	v_mfma_f32_16x16x32_bf16 v[8:11], v[170:173], v[234:237], v[8:11]
	s_barrier
	v_mfma_f32_16x16x32_bf16 v[4:7], v[178:181], v[234:237], v[4:7]
	s_setprio 0
	s_add_i32 s45, s45, 2
	s_add_u32 s43, s43, 0x100
	s_addc_u32 s44, s44, 0
	s_add_u32 s20, s20, 0x100
	s_addc_u32 s21, s21, 0
	s_cmp_gt_u32 s45, 13
	s_cbranch_scc0 .LBB0_1693
	s_and_b64 vcc, exec, s[8:9]
	s_cbranch_vccz .LBB0_1696
	s_barrier
